# IEEE f32 division chains (silu, 1/n pool mean) replaced by v_rcp_f32+v_mul in P2a epilogue, pool mixer, shared expert; dead refinement chains removed
# speedup vs baseline: 1.0163x; 1.0163x over previous
.LBB0_98:
	s_ashr_i32 s81, s80, 31
	v_lshl_add_u64 v[4:5], v[2:3], 2, s[70:71]
	s_lshl_b64 s[10:11], s[80:81], 12
	v_lshl_add_u64 v[14:15], v[4:5], 0, s[10:11]
	global_load_dwordx2 v[14:15], v[14:15], off
	s_or_b32 s10, s80, 1
	s_ashr_i32 s11, s10, 31
	s_lshl_b64 s[10:11], s[10:11], 12
	v_lshl_add_u64 v[16:17], v[4:5], 0, s[10:11]
	global_load_dwordx2 v[16:17], v[16:17], off
	s_or_b32 s10, s80, 2
	s_ashr_i32 s11, s10, 31
	s_lshl_b64 s[10:11], s[10:11], 12
	v_lshl_add_u64 v[18:19], v[4:5], 0, s[10:11]
	s_or_b32 s10, s80, 3
	s_ashr_i32 s11, s10, 31
	s_lshl_b64 s[10:11], s[10:11], 12
	v_lshl_add_u64 v[24:25], v[4:5], 0, s[10:11]
	s_or_b32 s10, s80, 4
	s_ashr_i32 s11, s10, 31
	s_lshl_b64 s[10:11], s[10:11], 12
	v_lshl_add_u64 v[52:53], v[4:5], 0, s[10:11]
	s_or_b32 s10, s80, 5
	s_ashr_i32 s11, s10, 31
	s_lshl_b64 s[10:11], s[10:11], 12
	v_lshl_add_u64 v[56:57], v[4:5], 0, s[10:11]
	s_or_b32 s10, s80, 6
	s_ashr_i32 s11, s10, 31
	s_lshl_b64 s[10:11], s[10:11], 12
	v_lshl_add_u64 v[48:49], v[4:5], 0, s[10:11]
	s_or_b32 s10, s80, 7
	s_ashr_i32 s11, s10, 31
	s_lshl_b64 s[10:11], s[10:11], 12
	v_lshl_add_u64 v[46:47], v[4:5], 0, s[10:11]
	s_or_b32 s10, s80, 8
	s_ashr_i32 s11, s10, 31
	s_lshl_b64 s[10:11], s[10:11], 12
	v_lshl_add_u64 v[44:45], v[4:5], 0, s[10:11]
	s_or_b32 s10, s80, 9
	s_ashr_i32 s11, s10, 31
	s_lshl_b64 s[10:11], s[10:11], 12
	v_lshl_add_u64 v[42:43], v[4:5], 0, s[10:11]
	s_or_b32 s10, s80, 10
	s_ashr_i32 s11, s10, 31
	s_lshl_b64 s[10:11], s[10:11], 12
	s_min_i32 s35, s31, 7
	v_lshl_add_u64 v[40:41], v[4:5], 0, s[10:11]
	s_or_b32 s10, s80, 11
	s_add_i32 s35, s35, 1
	s_ashr_i32 s11, s10, 31
	v_cvt_f32_i32_e32 v3, s35
	s_lshl_b64 s[10:11], s[10:11], 12
	v_lshl_add_u64 v[38:39], v[4:5], 0, s[10:11]
	s_or_b32 s10, s80, 12
	global_load_dwordx2 v[22:23], v[18:19], off
	s_ashr_i32 s11, s10, 31
	s_lshl_b64 s[10:11], s[10:11], 12
	v_lshl_add_u64 v[32:33], v[4:5], 0, s[10:11]
	s_or_b32 s10, s80, 13
	s_ashr_i32 s11, s10, 31
	s_lshl_b64 s[10:11], s[10:11], 12
	v_lshl_add_u64 v[28:29], v[4:5], 0, s[10:11]
	s_or_b32 s10, s80, 14
	s_ashr_i32 s11, s10, 31
	s_lshl_b64 s[10:11], s[10:11], 12
	global_load_dwordx2 v[24:25], v[24:25], off
	v_lshl_add_u64 v[18:19], v[4:5], 0, s[10:11]
	s_or_b32 s10, s80, 15
	s_ashr_i32 s11, s10, 31
	s_lshl_b64 s[10:11], s[10:11], 12
	v_lshl_add_u64 v[20:21], v[4:5], 0, s[10:11]
	s_min_i32 s10, s31, 6
	s_add_i32 s10, s10, 2
	v_rcp_f32_e32 v54, v3
	s_nop 0
	v_cvt_f32_i32_e32 v51, s10
	s_waitcnt vmcnt(3)
	v_pk_add_f32 v[58:59], v[26:27], v[14:15]
	v_lshlrev_b32_e32 v50, 2, v221
	v_pk_fma_f32 v[26:27], v[54:55], v[58:59], v[14:15] op_sel_hi:[0,1,1] neg_lo:[0,0,1] neg_hi:[0,0,1]
	v_and_b32_e32 v68, 12, v50
	v_and_b32_e32 v3, -16, v50
	v_cvt_pk_bf16_f32 v26, v26, v27
	v_add3_u32 v70, 0, v3, v68
	ds_write_b32 v70, v26
	global_load_dwordx2 v[26:27], v[52:53], off
	s_min_i32 s10, s31, 5
	s_add_i32 s10, s10, 3
	v_rcp_f32_e32 v52, v51
	s_nop 0
	v_cvt_f32_i32_e32 v51, s10
	s_waitcnt vmcnt(3)
	v_pk_add_f32 v[34:35], v[16:17], v[34:35] neg_lo:[0,1] neg_hi:[0,1]
	v_bitop3_b32 v54, v50, 16, -16 bitop3:0x6c
	v_pk_add_f32 v[58:59], v[58:59], v[34:35]
	v_add3_u32 v71, 0, v54, v68
	v_pk_fma_f32 v[34:35], v[52:53], v[58:59], v[16:17] op_sel_hi:[0,1,1] neg_lo:[0,0,1] neg_hi:[0,0,1]
	v_cvt_pk_bf16_f32 v34, v34, v35
	ds_write_b32 v71, v34 offset:2048
	global_load_dwordx2 v[34:35], v[56:57], off
	s_min_i32 s10, s31, 4
	s_add_i32 s10, s10, 4
	v_rcp_f32_e32 v52, v51
	s_nop 0
	v_cvt_f32_i32_e32 v51, s10
	s_waitcnt vmcnt(3)
	v_pk_add_f32 v[36:37], v[22:23], v[36:37] neg_lo:[0,1] neg_hi:[0,1]
	v_bitop3_b32 v55, v50, 32, -16 bitop3:0x6c
	v_pk_add_f32 v[56:57], v[58:59], v[36:37]
	v_add3_u32 v72, 0, v55, v68
	v_pk_fma_f32 v[36:37], v[52:53], v[56:57], v[22:23] op_sel_hi:[0,1,1] neg_lo:[0,0,1] neg_hi:[0,0,1]
	v_cvt_pk_bf16_f32 v36, v36, v37
	ds_write_b32 v72, v36 offset:4096
	s_min_i32 s10, s31, 3
	global_load_dwordx2 v[36:37], v[48:49], off
	s_add_i32 s10, s10, 5
	v_cvt_f32_i32_e32 v49, s10
	s_waitcnt vmcnt(3)
	v_pk_add_f32 v[30:31], v[24:25], v[30:31] neg_lo:[0,1] neg_hi:[0,1]
	v_rcp_f32_e32 v48, v51
	s_nop 0
	v_pk_add_f32 v[52:53], v[56:57], v[30:31]
	v_bitop3_b32 v56, v50, 48, -16 bitop3:0x6c
	v_pk_fma_f32 v[30:31], v[48:49], v[52:53], v[24:25] op_sel_hi:[0,1,1] neg_lo:[0,0,1] neg_hi:[0,0,1]
	v_cvt_pk_bf16_f32 v30, v30, v31
	v_add3_u32 v73, 0, v56, v68
	ds_write_b32 v73, v30 offset:6144
	s_min_i32 s10, s31, 2
	s_add_i32 s10, s10, 6
	global_load_dwordx2 v[30:31], v[46:47], off
	v_cvt_f32_i32_e32 v47, s10
	v_rcp_f32_e32 v46, v49
	s_nop 0
	v_bitop3_b32 v57, v50, 64, -16 bitop3:0x6c
	s_waitcnt vmcnt(3)
	v_pk_add_f32 v[8:9], v[26:27], v[8:9] neg_lo:[0,1] neg_hi:[0,1]
	v_add3_u32 v74, 0, v57, v68
	v_pk_add_f32 v[48:49], v[52:53], v[8:9]
	v_pk_fma_f32 v[8:9], v[46:47], v[48:49], v[26:27] op_sel_hi:[0,1,1] neg_lo:[0,0,1] neg_hi:[0,0,1]
	v_cvt_pk_bf16_f32 v8, v8, v9
	ds_write_b32 v74, v8 offset:8192
	s_min_i32 s10, s31, 1
	global_load_dwordx2 v[8:9], v[44:45], off
	s_add_i32 s10, s10, 7
	v_cvt_f32_i32_e32 v45, s10
	v_rcp_f32_e32 v44, v47
	s_nop 0
	global_load_dwordx2 v[18:19], v[18:19], off
	s_waitcnt vmcnt(4)
	v_pk_add_f32 v[10:11], v[34:35], v[10:11] neg_lo:[0,1] neg_hi:[0,1]
	s_min_i32 s35, s31, -9
	v_pk_add_f32 v[46:47], v[48:49], v[10:11]
	v_pk_fma_f32 v[10:11], v[44:45], v[46:47], v[34:35] op_sel_hi:[0,1,1] neg_lo:[0,0,1] neg_hi:[0,0,1]
	s_movk_i32 s10, 0x50
	v_bitop3_b32 v58, v50, s10, -16 bitop3:0x6c
	v_cvt_pk_bf16_f32 v10, v10, v11
	v_add3_u32 v75, 0, v58, v68
	ds_write_b32 v75, v10 offset:10240
	global_load_dwordx2 v[10:11], v[42:43], off
	s_min_i32 s10, s31, 0
	s_or_b32 s10, s10, 8
	v_cvt_f32_i32_e32 v43, s10
	s_waitcnt vmcnt(4)
	v_pk_add_f32 v[12:13], v[36:37], v[12:13] neg_lo:[0,1] neg_hi:[0,1]
	v_rcp_f32_e32 v42, v45
	s_nop 0
	v_pk_add_f32 v[44:45], v[46:47], v[12:13]
	v_pk_fma_f32 v[12:13], v[42:43], v[44:45], v[36:37] op_sel_hi:[0,1,1] neg_lo:[0,0,1] neg_hi:[0,0,1]
	s_movk_i32 s10, 0x60
	v_bitop3_b32 v59, v50, s10, -16 bitop3:0x6c
	v_cvt_pk_bf16_f32 v12, v12, v13
	v_add3_u32 v76, 0, v59, v68
	ds_write_b32 v76, v12 offset:12288
	s_min_i32 s10, s31, -1
	global_load_dwordx2 v[12:13], v[40:41], off
	s_add_i32 s10, s10, 9
	v_cvt_f32_i32_e32 v41, s10
	s_waitcnt vmcnt(4)
	v_pk_add_f32 v[6:7], v[30:31], v[6:7] neg_lo:[0,1] neg_hi:[0,1]
	v_rcp_f32_e32 v40, v43
	s_nop 0
	v_pk_add_f32 v[42:43], v[44:45], v[6:7]
	v_pk_fma_f32 v[6:7], v[40:41], v[42:43], v[30:31] op_sel_hi:[0,1,1] neg_lo:[0,0,1] neg_hi:[0,0,1]
	s_movk_i32 s10, 0x70
	v_bitop3_b32 v60, v50, s10, -16 bitop3:0x6c
	v_cvt_pk_bf16_f32 v6, v6, v7
	v_add3_u32 v78, 0, v60, v68
	ds_write_b32 v78, v6 offset:14336
	s_min_i32 s10, s31, -2
	s_add_i32 s10, s10, 10
	global_load_dwordx2 v[6:7], v[38:39], off
	v_cvt_f32_i32_e32 v39, s10
	s_waitcnt vmcnt(4)
	v_pk_add_f32 v[14:15], v[8:9], v[14:15] neg_lo:[0,1] neg_hi:[0,1]
	v_rcp_f32_e32 v38, v41
	s_nop 0
	v_pk_add_f32 v[40:41], v[42:43], v[14:15]
	v_pk_fma_f32 v[14:15], v[38:39], v[40:41], v[8:9] op_sel_hi:[0,1,1] neg_lo:[0,0,1] neg_hi:[0,0,1]
	s_movk_i32 s10, 0x80
	v_bitop3_b32 v61, v50, s10, -16 bitop3:0x6c
	v_cvt_pk_bf16_f32 v14, v14, v15
	v_add3_u32 v79, 0, v61, v68
	ds_write_b32 v79, v14 offset:16384
	global_load_dwordx2 v[14:15], v[32:33], off
	s_min_i32 s10, s31, -3
	s_add_i32 s10, s10, 11
	v_cvt_f32_i32_e32 v33, s10
	s_waitcnt vmcnt(3)
	v_pk_add_f32 v[16:17], v[10:11], v[16:17] neg_lo:[0,1] neg_hi:[0,1]
	v_rcp_f32_e32 v32, v39
	s_nop 0
	v_pk_add_f32 v[38:39], v[40:41], v[16:17]
	v_pk_fma_f32 v[16:17], v[32:33], v[38:39], v[10:11] op_sel_hi:[0,1,1] neg_lo:[0,0,1] neg_hi:[0,0,1]
	s_movk_i32 s10, 0x90
	v_bitop3_b32 v62, v50, s10, -16 bitop3:0x6c
	v_cvt_pk_bf16_f32 v16, v16, v17
	v_add3_u32 v80, 0, v62, v68
	ds_write_b32 v80, v16 offset:18432
	global_load_dwordx2 v[16:17], v[28:29], off
	s_min_i32 s10, s31, -4
	s_add_i32 s10, s10, 12
	global_load_dwordx2 v[20:21], v[20:21], off
	v_cvt_f32_i32_e32 v32, s10
	s_waitcnt vmcnt(4)
	v_pk_add_f32 v[22:23], v[12:13], v[22:23] neg_lo:[0,1] neg_hi:[0,1]
	v_rcp_f32_e32 v28, v33
	s_nop 0
	v_pk_add_f32 v[22:23], v[38:39], v[22:23]
	s_add_i32 s35, s35, 17
	v_pk_fma_f32 v[28:29], v[28:29], v[22:23], v[12:13] op_sel_hi:[0,1,1] neg_lo:[0,0,1] neg_hi:[0,0,1]
	v_cvt_pk_bf16_f32 v28, v28, v29
	s_movk_i32 s10, 0xa0
	v_bitop3_b32 v63, v50, s10, -16 bitop3:0x6c
	v_add3_u32 v81, 0, v63, v68
	ds_write_b32 v81, v28 offset:20480
	s_min_i32 s10, s31, -5
	s_add_i32 s10, s10, 13
	v_cvt_f32_i32_e32 v29, s10
	s_waitcnt vmcnt(3)
	v_pk_add_f32 v[24:25], v[6:7], v[24:25] neg_lo:[0,1] neg_hi:[0,1]
	v_rcp_f32_e32 v28, v32
	s_nop 0
	v_pk_add_f32 v[22:23], v[22:23], v[24:25]
	v_cvt_f32_i32_e32 v88, s35
	v_pk_fma_f32 v[24:25], v[28:29], v[22:23], v[6:7] op_sel_hi:[0,1,1] neg_lo:[0,0,1] neg_hi:[0,0,1]
	v_cvt_pk_bf16_f32 v24, v24, v25
	s_movk_i32 s10, 0xb0
	v_bitop3_b32 v64, v50, s10, -16 bitop3:0x6c
	v_add3_u32 v77, 0, v64, v68
	ds_write_b32 v77, v24 offset:22528
	s_min_i32 s10, s31, -6
	s_add_i32 s10, s10, 14
	s_waitcnt vmcnt(2)
	v_pk_add_f32 v[26:27], v[14:15], v[26:27] neg_lo:[0,1] neg_hi:[0,1]
	v_pk_add_f32 v[22:23], v[22:23], v[26:27]
	v_cvt_f32_i32_e32 v26, s10
	v_rcp_f32_e32 v24, v29
	s_nop 0
	v_pk_fma_f32 v[24:25], v[24:25], v[22:23], v[14:15] op_sel_hi:[0,1,1] neg_lo:[0,0,1] neg_hi:[0,0,1]
	v_cvt_pk_bf16_f32 v24, v24, v25
	s_movk_i32 s10, 0xc0
	v_bitop3_b32 v65, v50, s10, -16 bitop3:0x6c
	v_add3_u32 v82, 0, v65, v68
	ds_write_b32 v82, v24 offset:24576
	s_min_i32 s10, s31, -7
	v_rcp_f32_e32 v24, v26
	s_nop 0
	s_waitcnt vmcnt(1)
	v_pk_add_f32 v[26:27], v[16:17], v[34:35] neg_lo:[0,1] neg_hi:[0,1]
	s_add_i32 s10, s10, 15
	v_pk_add_f32 v[22:23], v[22:23], v[26:27]
	v_cvt_f32_i32_e32 v26, s10
	v_pk_fma_f32 v[24:25], v[24:25], v[22:23], v[16:17] op_sel_hi:[0,1,1] neg_lo:[0,0,1] neg_hi:[0,0,1]
	v_cvt_pk_bf16_f32 v24, v24, v25
	s_min_i32 s35, s31, 0xffffffe7
	s_movk_i32 s10, 0xd0
	v_bitop3_b32 v66, v50, s10, -16 bitop3:0x6c
	v_add3_u32 v83, 0, v66, v68
	ds_write_b32 v83, v24 offset:26624
	s_min_i32 s10, s31, -8
	v_rcp_f32_e32 v24, v26
	s_nop 0
	v_pk_add_f32 v[26:27], v[18:19], v[36:37] neg_lo:[0,1] neg_hi:[0,1]
	s_add_i32 s10, s10, 16
	v_pk_add_f32 v[22:23], v[22:23], v[26:27]
	v_cvt_f32_i32_e32 v26, s10
	v_pk_fma_f32 v[24:25], v[24:25], v[22:23], v[18:19] op_sel_hi:[0,1,1] neg_lo:[0,0,1] neg_hi:[0,0,1]
	v_cvt_pk_bf16_f32 v24, v24, v25
	s_add_i32 s35, s35, 33
	s_movk_i32 s10, 0xe0
	v_bitop3_b32 v67, v50, s10, -16 bitop3:0x6c
	v_add3_u32 v84, 0, v67, v68
	ds_write_b32 v84, v24 offset:28672
	v_rcp_f32_e32 v24, v26
	s_nop 0
	s_waitcnt vmcnt(0)
	v_pk_add_f32 v[26:27], v[20:21], v[30:31] neg_lo:[0,1] neg_hi:[0,1]
	s_movk_i32 s10, 0xf0
	v_pk_add_f32 v[36:37], v[22:23], v[26:27]
	v_bitop3_b32 v69, v50, s10, -16 bitop3:0x6c
	s_or_b32 s10, s80, 16
	v_pk_fma_f32 v[22:23], v[24:25], v[36:37], v[20:21] op_sel_hi:[0,1,1] neg_lo:[0,0,1] neg_hi:[0,0,1]
	s_ashr_i32 s11, s10, 31
	v_cvt_pk_bf16_f32 v22, v22, v23
	v_add3_u32 v85, 0, v69, v68
	s_lshl_b64 s[10:11], s[10:11], 12
	ds_write_b32 v85, v22 offset:30720
	v_lshl_add_u64 v[22:23], v[4:5], 0, s[10:11]
	global_load_dwordx2 v[30:31], v[22:23], off
	s_or_b32 s10, s80, 17
	s_ashr_i32 s11, s10, 31
	s_lshl_b64 s[10:11], s[10:11], 12
	v_lshl_add_u64 v[24:25], v[4:5], 0, s[10:11]
	global_load_dwordx2 v[32:33], v[24:25], off
	s_or_b32 s10, s80, 18
	s_ashr_i32 s11, s10, 31
	s_lshl_b64 s[10:11], s[10:11], 12
	v_lshl_add_u64 v[26:27], v[4:5], 0, s[10:11]
	s_or_b32 s10, s80, 19
	s_ashr_i32 s11, s10, 31
	s_lshl_b64 s[10:11], s[10:11], 12
	v_lshl_add_u64 v[38:39], v[4:5], 0, s[10:11]
	s_or_b32 s10, s80, 20
	s_ashr_i32 s11, s10, 31
	s_lshl_b64 s[10:11], s[10:11], 12
	v_lshl_add_u64 v[42:43], v[4:5], 0, s[10:11]
	s_or_b32 s10, s80, 21
	s_ashr_i32 s11, s10, 31
	s_lshl_b64 s[10:11], s[10:11], 12
	v_lshl_add_u64 v[46:47], v[4:5], 0, s[10:11]
	s_or_b32 s10, s80, 22
	s_ashr_i32 s11, s10, 31
	s_lshl_b64 s[10:11], s[10:11], 12
	v_lshl_add_u64 v[86:87], v[4:5], 0, s[10:11]
	s_or_b32 s10, s80, 23
	s_ashr_i32 s11, s10, 31
	s_lshl_b64 s[10:11], s[10:11], 12
	v_lshl_add_u64 v[50:51], v[4:5], 0, s[10:11]
	s_or_b32 s10, s80, 24
	s_ashr_i32 s11, s10, 31
	s_lshl_b64 s[10:11], s[10:11], 12
	global_load_dwordx2 v[34:35], v[26:27], off
	v_readlane_b32 s12, v254, 53
	global_load_dwordx2 v[50:51], v[50:51], off
	v_lshl_add_u64 v[24:25], v[4:5], 0, s[10:11]
	s_or_b32 s10, s80, 25
	s_ashr_i32 s11, s10, 31
	s_lshl_b64 s[10:11], s[10:11], 12
	v_lshl_add_u64 v[22:23], v[4:5], 0, s[10:11]
	s_or_b32 s10, s80, 26
	s_ashr_i32 s11, s10, 31
	s_lshl_b64 s[10:11], s[10:11], 12
	v_lshl_add_u64 v[52:53], v[4:5], 0, s[10:11]
	s_or_b32 s10, s80, 27
	s_ashr_i32 s11, s10, 31
	s_lshl_b64 s[10:11], s[10:11], 12
	v_lshl_add_u64 v[48:49], v[4:5], 0, s[10:11]
	s_or_b32 s10, s80, 28
	s_ashr_i32 s11, s10, 31
	s_lshl_b64 s[10:11], s[10:11], 12
	v_lshl_add_u64 v[44:45], v[4:5], 0, s[10:11]
	s_or_b32 s10, s80, 29
	s_ashr_i32 s11, s10, 31
	s_lshl_b64 s[10:11], s[10:11], 12
	v_lshl_add_u64 v[40:41], v[4:5], 0, s[10:11]
	s_or_b32 s10, s80, 30
	s_ashr_i32 s11, s10, 31
	s_lshl_b64 s[10:11], s[10:11], 12
	v_lshl_add_u64 v[28:29], v[4:5], 0, s[10:11]
	s_or_b32 s10, s80, 31
	s_ashr_i32 s11, s10, 31
	s_lshl_b64 s[10:11], s[10:11], 12
	global_load_dwordx2 v[38:39], v[38:39], off
	v_lshl_add_u64 v[26:27], v[4:5], 0, s[10:11]
	s_min_i32 s10, s31, -10
	s_add_i32 s10, s10, 18
	v_rcp_f32_e32 v88, v88
	s_nop 0
	v_cvt_f32_i32_e32 v89, s10
	s_waitcnt vmcnt(4)
	v_pk_add_f32 v[8:9], v[30:31], v[8:9] neg_lo:[0,1] neg_hi:[0,1]
	global_load_dwordx2 v[22:23], v[22:23], off
	v_pk_add_f32 v[8:9], v[36:37], v[8:9]
	v_pk_fma_f32 v[36:37], v[88:89], v[8:9], v[30:31] op_sel_hi:[0,1,1] neg_lo:[0,0,1] neg_hi:[0,0,1]
	v_cvt_pk_bf16_f32 v36, v36, v37
	ds_write_b32 v70, v36 offset:32768
	global_load_dwordx2 v[36:37], v[42:43], off
	s_waitcnt vmcnt(5)
	v_pk_add_f32 v[10:11], v[32:33], v[10:11] neg_lo:[0,1] neg_hi:[0,1]
	v_rcp_f32_e32 v42, v89
	s_nop 0
	v_pk_add_f32 v[8:9], v[8:9], v[10:11]
	s_min_i32 s10, s31, -11
	v_pk_fma_f32 v[10:11], v[42:43], v[8:9], v[32:33] op_sel_hi:[0,1,1] neg_lo:[0,0,1] neg_hi:[0,0,1]
	global_load_dwordx2 v[42:43], v[46:47], off
	s_add_i32 s10, s10, 19
	v_cvt_f32_i32_e32 v70, s10
	v_cvt_pk_bf16_f32 v10, v10, v11
	ds_write_b32 v71, v10 offset:34816
	global_load_dwordx2 v[24:25], v[24:25], off
	s_min_i32 s10, s31, -12
	s_add_i32 s10, s10, 20
	s_waitcnt vmcnt(6)
	v_pk_add_f32 v[12:13], v[34:35], v[12:13] neg_lo:[0,1] neg_hi:[0,1]
	global_load_dwordx2 v[46:47], v[86:87], off
	v_rcp_f32_e32 v10, v70
	s_nop 0
	v_cvt_f32_i32_e32 v70, s10
	v_pk_add_f32 v[8:9], v[8:9], v[12:13]
	v_add3_u32 v92, s24, v54, v68
	v_pk_fma_f32 v[10:11], v[10:11], v[8:9], v[34:35] op_sel_hi:[0,1,1] neg_lo:[0,0,1] neg_hi:[0,0,1]
	v_cvt_pk_bf16_f32 v10, v10, v11
	ds_write_b32 v72, v10 offset:36864
	s_min_i32 s10, s31, -13
	s_add_i32 s10, s10, 21
	v_cvt_f32_i32_e32 v11, s10
	v_rcp_f32_e32 v10, v70
	s_nop 0
	s_waitcnt vmcnt(5)
	v_pk_add_f32 v[6:7], v[38:39], v[6:7] neg_lo:[0,1] neg_hi:[0,1]
	v_pk_add_f32 v[6:7], v[8:9], v[6:7]
	s_min_i32 s10, s31, -14
	v_pk_fma_f32 v[8:9], v[10:11], v[6:7], v[38:39] op_sel_hi:[0,1,1] neg_lo:[0,0,1] neg_hi:[0,0,1]
	v_cvt_pk_bf16_f32 v8, v8, v9
	ds_write_b32 v73, v8 offset:38912
	s_add_i32 s10, s10, 22
	v_cvt_f32_i32_e32 v12, s10
	v_rcp_f32_e32 v8, v11
	s_nop 0
	s_waitcnt vmcnt(3)
	v_pk_add_f32 v[10:11], v[36:37], v[14:15] neg_lo:[0,1] neg_hi:[0,1]
	s_nop 0
	v_pk_add_f32 v[6:7], v[6:7], v[10:11]
	v_pk_fma_f32 v[8:9], v[8:9], v[6:7], v[36:37] op_sel_hi:[0,1,1] neg_lo:[0,0,1] neg_hi:[0,0,1]
	v_cvt_pk_bf16_f32 v8, v8, v9
	ds_write_b32 v74, v8 offset:40960
	s_min_i32 s10, s31, -15
	s_add_i32 s10, s10, 23
	v_rcp_f32_e32 v8, v12
	s_nop 0
	v_cvt_f32_i32_e32 v12, s10
	s_waitcnt vmcnt(2)
	v_pk_add_f32 v[10:11], v[42:43], v[16:17] neg_lo:[0,1] neg_hi:[0,1]
	v_cvt_f32_i32_e32 v74, s35
	v_pk_add_f32 v[6:7], v[6:7], v[10:11]
	v_pk_fma_f32 v[8:9], v[8:9], v[6:7], v[42:43] op_sel_hi:[0,1,1] neg_lo:[0,0,1] neg_hi:[0,0,1]
	v_cvt_pk_bf16_f32 v8, v8, v9
	ds_write_b32 v75, v8 offset:43008
	s_min_i32 s10, s31, -16
	s_add_i32 s10, s10, 24
	v_cvt_f32_i32_e32 v9, s10
	v_rcp_f32_e32 v8, v12
	s_nop 0
	s_waitcnt vmcnt(0)
	v_pk_add_f32 v[10:11], v[46:47], v[18:19] neg_lo:[0,1] neg_hi:[0,1]
	v_pk_add_f32 v[10:11], v[6:7], v[10:11]
	s_min_i32 s10, s31, 0xffffffef
	v_pk_fma_f32 v[6:7], v[8:9], v[10:11], v[46:47] op_sel_hi:[0,1,1] neg_lo:[0,0,1] neg_hi:[0,0,1]
	v_cvt_pk_bf16_f32 v6, v6, v7
	ds_write_b32 v76, v6 offset:45056
	global_load_dwordx2 v[6:7], v[52:53], off
	v_pk_add_f32 v[12:13], v[50:51], v[20:21] neg_lo:[0,1] neg_hi:[0,1]
	v_rcp_f32_e32 v8, v9
	s_nop 0
	v_pk_add_f32 v[10:11], v[10:11], v[12:13]
	s_add_i32 s10, s10, 25
	v_pk_fma_f32 v[8:9], v[8:9], v[10:11], v[50:51] op_sel_hi:[0,1,1] neg_lo:[0,0,1] neg_hi:[0,0,1]
	v_cvt_pk_bf16_f32 v8, v8, v9
	ds_write_b32 v78, v8 offset:47104
	global_load_dwordx2 v[8:9], v[48:49], off
	v_cvt_f32_i32_e32 v14, s10
	s_min_i32 s35, s31, 0xffffffd7
	s_add_i32 s35, s35, 49
	s_min_i32 s10, s31, 0xffffffee
	s_add_i32 s10, s10, 26
	v_cvt_f32_i32_e32 v13, s10
	v_rcp_f32_e32 v12, v14
	s_nop 0
	v_pk_add_f32 v[14:15], v[24:25], v[30:31] neg_lo:[0,1] neg_hi:[0,1]
	v_pk_add_f32 v[14:15], v[10:11], v[14:15]
	s_min_i32 s10, s31, 0xffffffed
	v_pk_fma_f32 v[10:11], v[12:13], v[14:15], v[24:25] op_sel_hi:[0,1,1] neg_lo:[0,0,1] neg_hi:[0,0,1]
	v_cvt_pk_bf16_f32 v10, v10, v11
	ds_write_b32 v79, v10 offset:49152
	global_load_dwordx2 v[10:11], v[44:45], off
	s_add_i32 s10, s10, 27
	v_cvt_f32_i32_e32 v18, s10
	v_pk_add_f32 v[16:17], v[22:23], v[32:33] neg_lo:[0,1] neg_hi:[0,1]
	v_rcp_f32_e32 v12, v13
	s_nop 0
	v_pk_add_f32 v[16:17], v[14:15], v[16:17]
	v_pk_fma_f32 v[12:13], v[12:13], v[16:17], v[22:23] op_sel_hi:[0,1,1] neg_lo:[0,0,1] neg_hi:[0,0,1]
	v_cvt_pk_bf16_f32 v12, v12, v13
	ds_write_b32 v80, v12 offset:51200
	global_load_dwordx2 v[14:15], v[40:41], off
	s_min_i32 s10, s31, 0xffffffec
	s_add_i32 s10, s10, 28
	v_cvt_f32_i32_e32 v20, s10
	v_rcp_f32_e32 v12, v18
	s_nop 0
	s_waitcnt vmcnt(3)
	v_pk_add_f32 v[18:19], v[6:7], v[34:35] neg_lo:[0,1] neg_hi:[0,1]
	v_pk_add_f32 v[16:17], v[16:17], v[18:19]
	v_pk_fma_f32 v[12:13], v[12:13], v[16:17], v[6:7] op_sel_hi:[0,1,1] neg_lo:[0,0,1] neg_hi:[0,0,1]
	v_cvt_pk_bf16_f32 v12, v12, v13
	ds_write_b32 v81, v12 offset:53248
	global_load_dwordx2 v[12:13], v[28:29], off
	v_rcp_f32_e32 v18, v20
	s_nop 0
	s_waitcnt vmcnt(3)
	v_pk_add_f32 v[20:21], v[8:9], v[38:39] neg_lo:[0,1] neg_hi:[0,1]
	s_min_i32 s10, s31, 0xffffffeb
	v_pk_add_f32 v[20:21], v[16:17], v[20:21]
	global_load_dwordx2 v[16:17], v[26:27], off
	s_add_i32 s10, s10, 29
	v_cvt_f32_i32_e32 v28, s10
	v_pk_fma_f32 v[18:19], v[18:19], v[20:21], v[8:9] op_sel_hi:[0,1,1] neg_lo:[0,0,1] neg_hi:[0,0,1]
	v_cvt_pk_bf16_f32 v18, v18, v19
	ds_write_b32 v77, v18 offset:55296
	s_min_i32 s10, s31, 0xffffffea
	s_add_i32 s10, s10, 30
	v_rcp_f32_e32 v18, v28
	s_nop 0
	v_cvt_f32_i32_e32 v28, s10
	s_waitcnt vmcnt(3)
	v_pk_add_f32 v[26:27], v[10:11], v[36:37] neg_lo:[0,1] neg_hi:[0,1]
	s_nop 0
	v_pk_add_f32 v[20:21], v[20:21], v[26:27]
	v_pk_fma_f32 v[18:19], v[18:19], v[20:21], v[10:11] op_sel_hi:[0,1,1] neg_lo:[0,0,1] neg_hi:[0,0,1]
	v_cvt_pk_bf16_f32 v18, v18, v19
	ds_write_b32 v82, v18 offset:57344
	s_min_i32 s10, s31, 0xffffffe9
	s_add_i32 s10, s10, 31
	v_rcp_f32_e32 v18, v28
	s_nop 0
	v_cvt_f32_i32_e32 v28, s10
	s_waitcnt vmcnt(2)
	v_pk_add_f32 v[26:27], v[14:15], v[42:43] neg_lo:[0,1] neg_hi:[0,1]
	s_nop 0
	v_pk_add_f32 v[20:21], v[20:21], v[26:27]
	v_pk_fma_f32 v[18:19], v[18:19], v[20:21], v[14:15] op_sel_hi:[0,1,1] neg_lo:[0,0,1] neg_hi:[0,0,1]
	v_cvt_pk_bf16_f32 v18, v18, v19
	ds_write_b32 v83, v18 offset:59392
	s_min_i32 s10, s31, 0xffffffe8
	s_add_i32 s10, s10, 32
	v_rcp_f32_e32 v18, v28
	s_nop 0
	v_cvt_f32_i32_e32 v28, s10
	s_waitcnt vmcnt(1)
	v_pk_add_f32 v[26:27], v[12:13], v[46:47] neg_lo:[0,1] neg_hi:[0,1]
	s_nop 0
	v_pk_add_f32 v[20:21], v[20:21], v[26:27]
	v_pk_fma_f32 v[18:19], v[18:19], v[20:21], v[12:13] op_sel_hi:[0,1,1] neg_lo:[0,0,1] neg_hi:[0,0,1]
	v_cvt_pk_bf16_f32 v18, v18, v19
	ds_write_b32 v84, v18 offset:61440
	s_waitcnt vmcnt(0)
	v_pk_add_f32 v[26:27], v[16:17], v[50:51] neg_lo:[0,1] neg_hi:[0,1]
	v_rcp_f32_e32 v18, v28
	s_nop 0
	v_pk_add_f32 v[26:27], v[20:21], v[26:27]
	s_or_b32 s10, s80, 32
	v_pk_fma_f32 v[18:19], v[18:19], v[26:27], v[16:17] op_sel_hi:[0,1,1] neg_lo:[0,0,1] neg_hi:[0,0,1]
	s_ashr_i32 s11, s10, 31
	v_cvt_pk_bf16_f32 v18, v18, v19
	s_lshl_b64 s[10:11], s[10:11], 12
	ds_write_b32 v85, v18 offset:63488
	v_lshl_add_u64 v[18:19], v[4:5], 0, s[10:11]
	global_load_dwordx2 v[30:31], v[18:19], off
	s_or_b32 s10, s80, 33
	s_ashr_i32 s11, s10, 31
	s_lshl_b64 s[10:11], s[10:11], 12
	v_lshl_add_u64 v[18:19], v[4:5], 0, s[10:11]
	global_load_dwordx2 v[32:33], v[18:19], off
	s_or_b32 s10, s80, 34
	s_ashr_i32 s11, s10, 31
	s_lshl_b64 s[10:11], s[10:11], 12
	v_lshl_add_u64 v[20:21], v[4:5], 0, s[10:11]
	s_or_b32 s10, s80, 35
	s_ashr_i32 s11, s10, 31
	s_lshl_b64 s[10:11], s[10:11], 12
	v_lshl_add_u64 v[28:29], v[4:5], 0, s[10:11]
	s_or_b32 s10, s80, 36
	s_ashr_i32 s11, s10, 31
	s_lshl_b64 s[10:11], s[10:11], 12
	v_lshl_add_u64 v[70:71], v[4:5], 0, s[10:11]
	s_or_b32 s10, s80, 37
	s_ashr_i32 s11, s10, 31
	s_lshl_b64 s[10:11], s[10:11], 12
	v_lshl_add_u64 v[72:73], v[4:5], 0, s[10:11]
	s_or_b32 s10, s80, 38
	s_ashr_i32 s11, s10, 31
	s_lshl_b64 s[10:11], s[10:11], 12
	v_lshl_add_u64 v[52:53], v[4:5], 0, s[10:11]
	s_or_b32 s10, s80, 39
	s_ashr_i32 s11, s10, 31
	s_lshl_b64 s[10:11], s[10:11], 12
	v_lshl_add_u64 v[50:51], v[4:5], 0, s[10:11]
	s_or_b32 s10, s80, 40
	s_ashr_i32 s11, s10, 31
	s_lshl_b64 s[10:11], s[10:11], 12
	v_lshl_add_u64 v[48:49], v[4:5], 0, s[10:11]
	s_or_b32 s10, s80, 41
	s_ashr_i32 s11, s10, 31
	global_load_dwordx2 v[34:35], v[20:21], off
	global_load_dwordx2 v[38:39], v[28:29], off
	s_lshl_b64 s[10:11], s[10:11], 12
	v_lshl_add_u64 v[46:47], v[4:5], 0, s[10:11]
	s_or_b32 s10, s80, 42
	s_ashr_i32 s11, s10, 31
	s_lshl_b64 s[10:11], s[10:11], 12
	v_lshl_add_u64 v[44:45], v[4:5], 0, s[10:11]
	s_or_b32 s10, s80, 43
	s_ashr_i32 s11, s10, 31
	s_lshl_b64 s[10:11], s[10:11], 12
	v_lshl_add_u64 v[42:43], v[4:5], 0, s[10:11]
	s_or_b32 s10, s80, 44
	s_ashr_i32 s11, s10, 31
	s_lshl_b64 s[10:11], s[10:11], 12
	v_lshl_add_u64 v[40:41], v[4:5], 0, s[10:11]
	s_or_b32 s10, s80, 45
	s_ashr_i32 s11, s10, 31
	s_lshl_b64 s[10:11], s[10:11], 12
	v_lshl_add_u64 v[36:37], v[4:5], 0, s[10:11]
	s_or_b32 s10, s80, 46
	s_ashr_i32 s11, s10, 31
	s_lshl_b64 s[10:11], s[10:11], 12
	v_lshl_add_u64 v[18:19], v[4:5], 0, s[10:11]
	s_or_b32 s10, s80, 47
	s_ashr_i32 s11, s10, 31
	s_lshl_b64 s[10:11], s[10:11], 12
	v_lshl_add_u64 v[20:21], v[4:5], 0, s[10:11]
	s_min_i32 s10, s31, 0xffffffe6
	s_add_i32 s10, s10, 34
	v_cvt_f32_i32_e32 v29, s10
	v_rcp_f32_e32 v28, v74
	s_nop 0
	s_waitcnt vmcnt(3)
	v_pk_add_f32 v[24:25], v[30:31], v[24:25] neg_lo:[0,1] neg_hi:[0,1]
	s_nop 0
	v_pk_add_f32 v[24:25], v[26:27], v[24:25]
	s_waitcnt vmcnt(2)
	v_pk_add_f32 v[22:23], v[32:33], v[22:23] neg_lo:[0,1] neg_hi:[0,1]
	v_pk_fma_f32 v[26:27], v[28:29], v[24:25], v[30:31] op_sel_hi:[0,1,1] neg_lo:[0,0,1] neg_hi:[0,0,1]
	v_readlane_b32 s10, v254, 19
	v_cvt_pk_bf16_f32 v26, v26, v27
	v_pk_add_f32 v[22:23], v[24:25], v[22:23]
	v_add3_u32 v27, s10, v3, v68
	ds_write_b32 v27, v26
	global_load_dwordx2 v[26:27], v[70:71], off
	v_rcp_f32_e32 v28, v29
	s_nop 0
	v_pk_fma_f32 v[24:25], v[28:29], v[22:23], v[32:33] op_sel_hi:[0,1,1] neg_lo:[0,0,1] neg_hi:[0,0,1]
	global_load_dwordx2 v[28:29], v[72:73], off
	s_min_i32 s10, s31, 0xffffffe5
	s_add_i32 s10, s10, 35
	v_cvt_f32_i32_e32 v70, s10
	v_cvt_pk_bf16_f32 v24, v24, v25
	v_add3_u32 v3, s12, v3, v68
	v_readlane_b32 s10, v254, 21
	s_waitcnt vmcnt(3)
	v_pk_add_f32 v[6:7], v[34:35], v[6:7] neg_lo:[0,1] neg_hi:[0,1]
	s_waitcnt vmcnt(2)
	v_pk_add_f32 v[8:9], v[38:39], v[8:9] neg_lo:[0,1] neg_hi:[0,1]
	v_add3_u32 v25, s10, v54, v68
	ds_write_b32 v25, v24
	s_min_i32 s10, s31, 0xffffffe4
	s_add_i32 s10, s10, 36
	v_cvt_f32_i32_e32 v25, s10
	v_rcp_f32_e32 v24, v70
	s_nop 0
	v_pk_add_f32 v[22:23], v[22:23], v[6:7]
	v_pk_fma_f32 v[6:7], v[24:25], v[22:23], v[34:35] op_sel_hi:[0,1,1] neg_lo:[0,0,1] neg_hi:[0,0,1]
	v_readlane_b32 s10, v254, 23
	v_cvt_pk_bf16_f32 v6, v6, v7
	v_pk_add_f32 v[22:23], v[22:23], v[8:9]
	v_add3_u32 v7, s10, v55, v68
	ds_write_b32 v7, v6
	global_load_dwordx2 v[6:7], v[52:53], off
	s_min_i32 s10, s31, 0xffffffe3
	s_add_i32 s10, s10, 37
	v_rcp_f32_e32 v24, v25
	s_nop 0
	v_cvt_f32_i32_e32 v25, s10
	v_add3_u32 v55, s25, v55, v68
	v_pk_fma_f32 v[8:9], v[24:25], v[22:23], v[38:39] op_sel_hi:[0,1,1] neg_lo:[0,0,1] neg_hi:[0,0,1]
	v_readlane_b32 s10, v254, 25
	v_cvt_pk_bf16_f32 v8, v8, v9
	s_nop 1
	v_add3_u32 v9, s10, v56, v68
	ds_write_b32 v9, v8
	global_load_dwordx2 v[8:9], v[50:51], off
	s_min_i32 s10, s31, 0xffffffe2
	s_add_i32 s10, s10, 38
	v_rcp_f32_e32 v24, v25
	s_nop 0
	v_cvt_f32_i32_e32 v25, s10
	s_waitcnt vmcnt(3)
	v_pk_add_f32 v[10:11], v[26:27], v[10:11] neg_lo:[0,1] neg_hi:[0,1]
	s_waitcnt vmcnt(2)
	v_pk_add_f32 v[14:15], v[28:29], v[14:15] neg_lo:[0,1] neg_hi:[0,1]
	v_pk_add_f32 v[22:23], v[22:23], v[10:11]
	v_pk_fma_f32 v[10:11], v[24:25], v[22:23], v[26:27] op_sel_hi:[0,1,1] neg_lo:[0,0,1] neg_hi:[0,0,1]
	v_readlane_b32 s10, v254, 29
	v_cvt_pk_bf16_f32 v10, v10, v11
	v_pk_add_f32 v[22:23], v[22:23], v[14:15]
	v_add3_u32 v11, s10, v57, v68
	ds_write_b32 v11, v10
	global_load_dwordx2 v[10:11], v[48:49], off
	s_min_i32 s10, s31, 0xffffffe1
	s_add_i32 s10, s10, 39
	v_rcp_f32_e32 v24, v25
	s_nop 0
	v_cvt_f32_i32_e32 v25, s10
	v_pk_fma_f32 v[14:15], v[24:25], v[22:23], v[28:29] op_sel_hi:[0,1,1] neg_lo:[0,0,1] neg_hi:[0,0,1]
	v_readlane_b32 s10, v254, 31
	v_cvt_pk_bf16_f32 v14, v14, v15
	s_nop 1
	v_add3_u32 v15, s10, v58, v68
	ds_write_b32 v15, v14
	global_load_dwordx2 v[14:15], v[46:47], off
	s_min_i32 s10, s31, 0xffffffe0
	s_add_i32 s10, s10, 40
	v_rcp_f32_e32 v24, v25
	s_nop 0
	v_cvt_f32_i32_e32 v25, s10
	s_waitcnt vmcnt(3)
	v_pk_add_f32 v[12:13], v[6:7], v[12:13] neg_lo:[0,1] neg_hi:[0,1]
	v_pk_add_f32 v[22:23], v[22:23], v[12:13]
	s_waitcnt vmcnt(2)
	v_pk_add_f32 v[16:17], v[8:9], v[16:17] neg_lo:[0,1] neg_hi:[0,1]
	v_pk_fma_f32 v[12:13], v[24:25], v[22:23], v[6:7] op_sel_hi:[0,1,1] neg_lo:[0,0,1] neg_hi:[0,0,1]
	v_readlane_b32 s10, v254, 33
	v_cvt_pk_bf16_f32 v12, v12, v13
	v_pk_add_f32 v[22:23], v[22:23], v[16:17]
	v_add3_u32 v13, s10, v59, v68
	ds_write_b32 v13, v12
	global_load_dwordx2 v[12:13], v[44:45], off
	s_min_i32 s10, s31, 0xffffffdf
	s_add_i32 s10, s10, 41
	v_rcp_f32_e32 v24, v25
	s_nop 0
	v_cvt_f32_i32_e32 v25, s10
	v_cvt_f32_i32_e32 v46, s35
	s_min_i32 s35, s31, 0xffffffd6
	s_add_i32 s35, s35, 50
	v_pk_fma_f32 v[16:17], v[24:25], v[22:23], v[8:9] op_sel_hi:[0,1,1] neg_lo:[0,0,1] neg_hi:[0,0,1]
	v_readlane_b32 s10, v254, 35
	v_cvt_pk_bf16_f32 v16, v16, v17
	s_waitcnt vmcnt(2)
	v_pk_add_f32 v[30:31], v[10:11], v[30:31] neg_lo:[0,1] neg_hi:[0,1]
	v_add3_u32 v17, s10, v60, v68
	ds_write_b32 v17, v16
	global_load_dwordx2 v[16:17], v[42:43], off
	s_min_i32 s10, s31, 0xffffffde
	s_add_i32 s10, s10, 42
	v_rcp_f32_e32 v24, v25
	s_nop 0
	v_cvt_f32_i32_e32 v25, s10
	v_pk_add_f32 v[30:31], v[22:23], v[30:31]
	v_cvt_f32_i32_e32 v48, s35
	s_min_i32 s35, s31, 0xffffffd5
	v_pk_fma_f32 v[22:23], v[24:25], v[30:31], v[10:11] op_sel_hi:[0,1,1] neg_lo:[0,0,1] neg_hi:[0,0,1]
	v_readlane_b32 s10, v254, 37
	v_cvt_pk_bf16_f32 v22, v22, v23
	s_nop 1
	v_add3_u32 v23, s10, v61, v68
	ds_write_b32 v23, v22
	global_load_dwordx2 v[22:23], v[40:41], off
	s_min_i32 s10, s31, 0xffffffdd
	s_add_i32 s10, s10, 43
	v_cvt_f32_i32_e32 v40, s10
	s_waitcnt vmcnt(3)
	v_pk_add_f32 v[32:33], v[14:15], v[32:33] neg_lo:[0,1] neg_hi:[0,1]
	v_rcp_f32_e32 v24, v25
	s_nop 0
	v_pk_add_f32 v[30:31], v[30:31], v[32:33]
	v_pk_fma_f32 v[24:25], v[24:25], v[30:31], v[14:15] op_sel_hi:[0,1,1] neg_lo:[0,0,1] neg_hi:[0,0,1]
	v_readlane_b32 s10, v254, 39
	v_cvt_pk_bf16_f32 v24, v24, v25
	s_add_i32 s35, s35, 51
	v_add3_u32 v25, s10, v62, v68
	ds_write_b32 v25, v24
	global_load_dwordx2 v[24:25], v[36:37], off
	s_min_i32 s10, s31, 0xffffffdc
	s_add_i32 s10, s10, 44
	v_cvt_f32_i32_e32 v36, s10
	s_waitcnt vmcnt(3)
	v_pk_add_f32 v[34:35], v[12:13], v[34:35] neg_lo:[0,1] neg_hi:[0,1]
	v_pk_add_f32 v[30:31], v[30:31], v[34:35]
	v_rcp_f32_e32 v32, v40
	s_nop 0
	v_pk_fma_f32 v[32:33], v[32:33], v[30:31], v[12:13] op_sel_hi:[0,1,1] neg_lo:[0,0,1] neg_hi:[0,0,1]
	v_readlane_b32 s10, v254, 41
	v_cvt_pk_bf16_f32 v32, v32, v33
	v_cvt_f32_i32_e32 v50, s35
	v_add3_u32 v33, s10, v63, v68
	ds_write_b32 v33, v32
	s_min_i32 s10, s31, 0xffffffdb
	s_add_i32 s10, s10, 45
	v_cvt_f32_i32_e32 v35, s10
	v_rcp_f32_e32 v34, v36
	s_nop 0
	s_waitcnt vmcnt(2)
	v_pk_add_f32 v[32:33], v[16:17], v[38:39] neg_lo:[0,1] neg_hi:[0,1]
	s_min_i32 s35, s31, 0xffffffd4
	v_pk_add_f32 v[32:33], v[30:31], v[32:33]
	s_add_i32 s35, s35, 52
	v_pk_fma_f32 v[30:31], v[34:35], v[32:33], v[16:17] op_sel_hi:[0,1,1] neg_lo:[0,0,1] neg_hi:[0,0,1]
	v_readlane_b32 s10, v254, 43
	v_cvt_pk_bf16_f32 v30, v30, v31
	v_cvt_f32_i32_e32 v51, s35
	v_add3_u32 v31, s10, v64, v68
	ds_write_b32 v31, v30
	s_min_i32 s10, s31, 0xffffffda
	s_add_i32 s10, s10, 46
	v_rcp_f32_e32 v34, v35
	s_nop 0
	v_cvt_f32_i32_e32 v35, s10
	global_load_dwordx2 v[30:31], v[18:19], off
	s_nop 0
	global_load_dwordx2 v[18:19], v[20:21], off
	s_waitcnt vmcnt(3)
	v_pk_add_f32 v[20:21], v[22:23], v[26:27] neg_lo:[0,1] neg_hi:[0,1]
	s_min_i32 s35, s31, 0xffffffd3
	v_pk_add_f32 v[20:21], v[32:33], v[20:21]
	v_pk_fma_f32 v[26:27], v[34:35], v[20:21], v[22:23] op_sel_hi:[0,1,1] neg_lo:[0,0,1] neg_hi:[0,0,1]
	v_readlane_b32 s10, v254, 45
	v_cvt_pk_bf16_f32 v26, v26, v27
	s_add_i32 s35, s35, 53
	v_add3_u32 v27, s10, v65, v68
	ds_write_b32 v27, v26
	s_min_i32 s10, s31, 0xffffffd9
	s_add_i32 s10, s10, 47
	v_cvt_f32_i32_e32 v32, s10
	s_waitcnt vmcnt(2)
	v_pk_add_f32 v[28:29], v[24:25], v[28:29] neg_lo:[0,1] neg_hi:[0,1]
	v_pk_add_f32 v[20:21], v[20:21], v[28:29]
	v_rcp_f32_e32 v26, v35
	s_nop 0
	v_pk_fma_f32 v[26:27], v[26:27], v[20:21], v[24:25] op_sel_hi:[0,1,1] neg_lo:[0,0,1] neg_hi:[0,0,1]
	v_readlane_b32 s10, v254, 47
	v_cvt_pk_bf16_f32 v26, v26, v27
	v_cvt_f32_i32_e32 v53, s35
	v_add3_u32 v27, s10, v66, v68
	s_min_i32 s10, s31, 0xffffffd8
	s_add_i32 s10, s10, 48
	ds_write_b32 v27, v26
	v_cvt_f32_i32_e32 v34, s10
	v_readlane_b32 s10, v254, 49
	s_nop 1
	v_add3_u32 v27, s10, v67, v68
	v_readlane_b32 s10, v254, 51
	v_rcp_f32_e32 v28, v32
	s_nop 0
	v_add3_u32 v44, s10, v69, v68
	s_or_b32 s10, s80, 48
	s_ashr_i32 s11, s10, 31
	s_lshl_b64 s[10:11], s[10:11], 12
	v_lshl_add_u64 v[36:37], v[4:5], 0, s[10:11]
	s_or_b32 s10, s80, 49
	s_ashr_i32 s11, s10, 31
	s_lshl_b64 s[10:11], s[10:11], 12
	v_lshl_add_u64 v[38:39], v[4:5], 0, s[10:11]
	s_or_b32 s10, s80, 50
	s_ashr_i32 s11, s10, 31
	s_lshl_b64 s[10:11], s[10:11], 12
	v_lshl_add_u64 v[32:33], v[4:5], 0, s[10:11]
	s_or_b32 s10, s80, 51
	s_ashr_i32 s11, s10, 31
	s_lshl_b64 s[10:11], s[10:11], 12
	v_rcp_f32_e32 v26, v34
	s_nop 0
	v_lshl_add_u64 v[34:35], v[4:5], 0, s[10:11]
	s_min_i32 s35, s31, 0xffffffd2
	s_add_i32 s35, s35, 54
	v_cvt_f32_i32_e32 v71, s35
	s_min_i32 s35, s31, 0xffffffd1
	s_add_i32 s35, s35, 55
	v_cvt_f32_i32_e32 v73, s35
	s_min_i32 s35, s31, 0xffffffd0
	s_add_i32 s35, s35, 56
	v_cvt_f32_i32_e32 v75, s35
	s_min_i32 s35, s31, 0xffffffcf
	s_add_i32 s35, s35, 57
	v_cvt_f32_i32_e32 v77, s35
	s_min_i32 s35, s31, 0xffffffce
	s_add_i32 s35, s35, 58
	v_cvt_f32_i32_e32 v79, s35
	s_min_i32 s35, s31, 0xffffffcd
	s_add_i32 s35, s35, 59
	global_load_dwordx2 v[36:37], v[36:37], off
	v_cvt_f32_i32_e32 v81, s35
	global_load_dwordx2 v[38:39], v[38:39], off
	s_min_i32 s35, s31, 0xffffffcc
	s_add_i32 s35, s35, 60
	v_cvt_f32_i32_e32 v83, s35
	s_min_i32 s35, s31, 0xffffffcb
	s_add_i32 s35, s35, 61
	v_cvt_f32_i32_e32 v85, s35
	s_min_i32 s35, s31, 0xffffffca
	s_add_i32 s35, s35, 62
	v_cvt_f32_i32_e32 v87, s35
	s_min_i32 s35, s31, 0xffffffc9
	s_add_i32 s35, s35, 63
	v_cvt_f32_i32_e32 v89, s35
	s_waitcnt vmcnt(3)
	v_pk_add_f32 v[6:7], v[30:31], v[6:7] neg_lo:[0,1] neg_hi:[0,1]
	v_pk_add_f32 v[6:7], v[20:21], v[6:7]
	v_pk_fma_f32 v[28:29], v[28:29], v[6:7], v[30:31] op_sel_hi:[0,1,1] neg_lo:[0,0,1] neg_hi:[0,0,1]
	s_waitcnt vmcnt(2)
	v_pk_add_f32 v[8:9], v[18:19], v[8:9] neg_lo:[0,1] neg_hi:[0,1]
	v_cvt_pk_bf16_f32 v28, v28, v29
	v_pk_add_f32 v[6:7], v[6:7], v[8:9]
	ds_write_b32 v27, v28
	v_pk_fma_f32 v[26:27], v[26:27], v[6:7], v[18:19] op_sel_hi:[0,1,1] neg_lo:[0,0,1] neg_hi:[0,0,1]
	v_cvt_pk_bf16_f32 v45, v26, v27
	global_load_dwordx2 v[26:27], v[32:33], off
	s_or_b32 s10, s80, 52
	s_ashr_i32 s11, s10, 31
	global_load_dwordx2 v[34:35], v[34:35], off
	s_lshl_b64 s[10:11], s[10:11], 12
	v_lshl_add_u64 v[40:41], v[4:5], 0, s[10:11]
	s_or_b32 s10, s80, 53
	s_ashr_i32 s11, s10, 31
	global_load_dwordx2 v[40:41], v[40:41], off
	s_lshl_b64 s[10:11], s[10:11], 12
	v_lshl_add_u64 v[42:43], v[4:5], 0, s[10:11]
	s_or_b32 s10, s80, 54
	s_ashr_i32 s11, s10, 31
	global_load_dwordx2 v[42:43], v[42:43], off
	s_lshl_b64 s[10:11], s[10:11], 12
	v_lshl_add_u64 v[20:21], v[4:5], 0, s[10:11]
	s_or_b32 s10, s80, 55
	s_ashr_i32 s11, s10, 31
	global_load_dwordx2 v[20:21], v[20:21], off
	s_lshl_b64 s[10:11], s[10:11], 12
	v_lshl_add_u64 v[28:29], v[4:5], 0, s[10:11]
	s_or_b32 s10, s80, 56
	s_ashr_i32 s11, s10, 31
	global_load_dwordx2 v[28:29], v[28:29], off
	s_lshl_b64 s[10:11], s[10:11], 12
	v_lshl_add_u64 v[8:9], v[4:5], 0, s[10:11]
	s_or_b32 s10, s80, 57
	s_ashr_i32 s11, s10, 31
	global_load_dwordx2 v[8:9], v[8:9], off
	s_lshl_b64 s[10:11], s[10:11], 12
	v_lshl_add_u64 v[32:33], v[4:5], 0, s[10:11]
	s_or_b32 s10, s80, 58
	s_ashr_i32 s11, s10, 31
	global_load_dwordx2 v[32:33], v[32:33], off
	s_lshl_b64 s[10:11], s[10:11], 12
	ds_write_b32 v44, v45
	v_lshl_add_u64 v[44:45], v[4:5], 0, s[10:11]
	s_or_b32 s10, s80, 59
	s_ashr_i32 s11, s10, 31
	global_load_dwordx2 v[44:45], v[44:45], off
	s_lshl_b64 s[10:11], s[10:11], 12
	s_waitcnt vmcnt(10)
	v_pk_add_f32 v[10:11], v[36:37], v[10:11] neg_lo:[0,1] neg_hi:[0,1]
	v_rcp_f32_e32 v46, v46
	s_nop 0
	v_pk_add_f32 v[6:7], v[6:7], v[10:11]
	v_lshl_add_u64 v[10:11], v[4:5], 0, s[10:11]
	s_or_b32 s10, s80, 60
	s_ashr_i32 s11, s10, 31
	v_pk_fma_f32 v[46:47], v[46:47], v[6:7], v[36:37] op_sel_hi:[0,1,1] neg_lo:[0,0,1] neg_hi:[0,0,1]
	global_load_dwordx2 v[10:11], v[10:11], off
	s_lshl_b64 s[10:11], s[10:11], 12
	v_cvt_pk_bf16_f32 v46, v46, v47
	ds_write_b32 v3, v46
	v_lshl_add_u64 v[46:47], v[4:5], 0, s[10:11]
	s_or_b32 s10, s80, 61
	s_ashr_i32 s11, s10, 31
	global_load_dwordx2 v[46:47], v[46:47], off
	s_lshl_b64 s[10:11], s[10:11], 12
	s_waitcnt vmcnt(11)
	v_pk_add_f32 v[14:15], v[38:39], v[14:15] neg_lo:[0,1] neg_hi:[0,1]
	v_rcp_f32_e32 v48, v48
	s_nop 0
	v_pk_add_f32 v[6:7], v[6:7], v[14:15]
	v_lshl_add_u64 v[14:15], v[4:5], 0, s[10:11]
	s_or_b32 s10, s80, 62
	s_ashr_i32 s11, s10, 31
	global_load_dwordx2 v[14:15], v[14:15], off
	s_lshl_b64 s[10:11], s[10:11], 12
	v_pk_fma_f32 v[48:49], v[48:49], v[6:7], v[38:39] op_sel_hi:[0,1,1] neg_lo:[0,0,1] neg_hi:[0,0,1]
	v_cvt_pk_bf16_f32 v3, v48, v49
	v_lshl_add_u64 v[48:49], v[4:5], 0, s[10:11]
	s_or_b32 s10, s80, 63
	s_ashr_i32 s11, s10, 31
	global_load_dwordx2 v[48:49], v[48:49], off
	s_lshl_b64 s[10:11], s[10:11], 12
	v_lshl_add_u64 v[4:5], v[4:5], 0, s[10:11]
	global_load_dwordx2 v[4:5], v[4:5], off
	v_rcp_f32_e32 v50, v50
	s_nop 0
	v_rcp_f32_e32 v52, v51
	s_nop 0
	v_add3_u32 v51, s26, v56, v68
	ds_write_b32 v92, v3
	v_rcp_f32_e32 v54, v53
	s_nop 0
	v_add3_u32 v53, s27, v57, v68
	s_waitcnt vmcnt(13)
	v_pk_add_f32 v[12:13], v[26:27], v[12:13] neg_lo:[0,1] neg_hi:[0,1]
	v_rcp_f32_e32 v56, v71
	s_nop 0
	v_pk_add_f32 v[6:7], v[6:7], v[12:13]
	v_add3_u32 v57, s77, v58, v68
	v_pk_fma_f32 v[12:13], v[50:51], v[6:7], v[26:27] op_sel_hi:[0,1,1] neg_lo:[0,0,1] neg_hi:[0,0,1]
	v_cvt_pk_bf16_f32 v3, v12, v13
	s_waitcnt vmcnt(12)
	v_pk_add_f32 v[12:13], v[34:35], v[16:17] neg_lo:[0,1] neg_hi:[0,1]
	ds_write_b32 v55, v3
	v_pk_add_f32 v[6:7], v[6:7], v[12:13]
	v_rcp_f32_e32 v58, v73
	s_nop 0
	v_pk_fma_f32 v[12:13], v[52:53], v[6:7], v[34:35] op_sel_hi:[0,1,1] neg_lo:[0,0,1] neg_hi:[0,0,1]
	v_cvt_pk_bf16_f32 v3, v12, v13
	s_waitcnt vmcnt(11)
	v_pk_add_f32 v[12:13], v[40:41], v[22:23] neg_lo:[0,1] neg_hi:[0,1]
	ds_write_b32 v51, v3
	v_pk_add_f32 v[6:7], v[6:7], v[12:13]
	v_add3_u32 v59, s91, v59, v68
	v_pk_fma_f32 v[12:13], v[54:55], v[6:7], v[40:41] op_sel_hi:[0,1,1] neg_lo:[0,0,1] neg_hi:[0,0,1]
	v_cvt_pk_bf16_f32 v3, v12, v13
	s_waitcnt vmcnt(10)
	v_pk_add_f32 v[12:13], v[42:43], v[24:25] neg_lo:[0,1] neg_hi:[0,1]
	ds_write_b32 v53, v3
	v_pk_add_f32 v[6:7], v[6:7], v[12:13]
	v_rcp_f32_e32 v70, v75
	s_nop 0
	v_pk_fma_f32 v[12:13], v[56:57], v[6:7], v[42:43] op_sel_hi:[0,1,1] neg_lo:[0,0,1] neg_hi:[0,0,1]
	v_cvt_pk_bf16_f32 v3, v12, v13
	s_waitcnt vmcnt(9)
	v_pk_add_f32 v[12:13], v[20:21], v[30:31] neg_lo:[0,1] neg_hi:[0,1]
	ds_write_b32 v57, v3
	v_pk_add_f32 v[6:7], v[6:7], v[12:13]
	v_add3_u32 v71, s94, v60, v68
	v_pk_fma_f32 v[12:13], v[58:59], v[6:7], v[20:21] op_sel_hi:[0,1,1] neg_lo:[0,0,1] neg_hi:[0,0,1]
	v_cvt_pk_bf16_f32 v3, v12, v13
	s_waitcnt vmcnt(8)
	v_pk_add_f32 v[12:13], v[28:29], v[18:19] neg_lo:[0,1] neg_hi:[0,1]
	ds_write_b32 v59, v3
	v_pk_add_f32 v[6:7], v[6:7], v[12:13]
	v_rcp_f32_e32 v60, v77
	s_nop 0
	v_pk_fma_f32 v[12:13], v[70:71], v[6:7], v[28:29] op_sel_hi:[0,1,1] neg_lo:[0,0,1] neg_hi:[0,0,1]
	v_cvt_pk_bf16_f32 v3, v12, v13
	s_waitcnt vmcnt(7)
	v_pk_add_f32 v[12:13], v[8:9], v[36:37] neg_lo:[0,1] neg_hi:[0,1]
	v_add3_u32 v61, s33, v61, v68
	v_pk_add_f32 v[6:7], v[6:7], v[12:13]
	ds_write_b32 v71, v3
	v_pk_fma_f32 v[8:9], v[60:61], v[6:7], v[8:9] op_sel_hi:[0,1,1] neg_lo:[0,0,1] neg_hi:[0,0,1]
	v_cvt_pk_bf16_f32 v3, v8, v9
	s_waitcnt vmcnt(6)
	v_pk_add_f32 v[8:9], v[32:33], v[38:39] neg_lo:[0,1] neg_hi:[0,1]
	v_rcp_f32_e32 v72, v79
	s_nop 0
	v_add3_u32 v73, s75, v62, v68
	v_pk_add_f32 v[6:7], v[6:7], v[8:9]
	ds_write_b32 v61, v3
	v_pk_fma_f32 v[8:9], v[72:73], v[6:7], v[32:33] op_sel_hi:[0,1,1] neg_lo:[0,0,1] neg_hi:[0,0,1]
	v_cvt_pk_bf16_f32 v3, v8, v9
	s_waitcnt vmcnt(5)
	v_pk_add_f32 v[8:9], v[44:45], v[26:27] neg_lo:[0,1] neg_hi:[0,1]
	v_rcp_f32_e32 v62, v81
	s_nop 0
	v_add3_u32 v63, s95, v63, v68
	v_pk_add_f32 v[6:7], v[6:7], v[8:9]
	ds_write_b32 v73, v3
	v_pk_fma_f32 v[8:9], v[62:63], v[6:7], v[44:45] op_sel_hi:[0,1,1] neg_lo:[0,0,1] neg_hi:[0,0,1]
	v_cvt_pk_bf16_f32 v3, v8, v9
	s_waitcnt vmcnt(4)
	v_pk_add_f32 v[8:9], v[10:11], v[34:35] neg_lo:[0,1] neg_hi:[0,1]
	v_rcp_f32_e32 v74, v83
	s_nop 0
	v_add3_u32 v75, s96, v64, v68
	v_pk_add_f32 v[6:7], v[6:7], v[8:9]
	ds_write_b32 v63, v3
	v_pk_fma_f32 v[8:9], v[74:75], v[6:7], v[10:11] op_sel_hi:[0,1,1] neg_lo:[0,0,1] neg_hi:[0,0,1]
	v_cvt_pk_bf16_f32 v3, v8, v9
	s_waitcnt vmcnt(3)
	v_pk_add_f32 v[8:9], v[46:47], v[40:41] neg_lo:[0,1] neg_hi:[0,1]
	v_rcp_f32_e32 v64, v85
	s_nop 0
	v_add3_u32 v65, s97, v65, v68
	v_pk_add_f32 v[6:7], v[6:7], v[8:9]
	ds_write_b32 v75, v3
	v_pk_fma_f32 v[8:9], v[64:65], v[6:7], v[46:47] op_sel_hi:[0,1,1] neg_lo:[0,0,1] neg_hi:[0,0,1]
	v_cvt_pk_bf16_f32 v3, v8, v9
	s_waitcnt vmcnt(2)
	v_pk_add_f32 v[8:9], v[14:15], v[42:43] neg_lo:[0,1] neg_hi:[0,1]
	v_rcp_f32_e32 v76, v87
	s_nop 0
	v_add3_u32 v77, s36, v66, v68
	v_pk_add_f32 v[6:7], v[6:7], v[8:9]
	ds_write_b32 v65, v3
	v_pk_fma_f32 v[8:9], v[76:77], v[6:7], v[14:15] op_sel_hi:[0,1,1] neg_lo:[0,0,1] neg_hi:[0,0,1]
	v_cvt_pk_bf16_f32 v3, v8, v9
	s_waitcnt vmcnt(1)
	v_pk_add_f32 v[8:9], v[48:49], v[20:21] neg_lo:[0,1] neg_hi:[0,1]
	v_rcp_f32_e32 v66, v89
	s_nop 0
	v_add3_u32 v67, s37, v67, v68
	v_pk_add_f32 v[6:7], v[6:7], v[8:9]
	ds_write_b32 v77, v3
	v_pk_fma_f32 v[8:9], v[66:67], v[6:7], v[48:49] op_sel_hi:[0,1,1] neg_lo:[0,0,1] neg_hi:[0,0,1]
	v_cvt_pk_bf16_f32 v3, v8, v9
	s_waitcnt vmcnt(0)
	v_pk_add_f32 v[8:9], v[4:5], v[28:29] neg_lo:[0,1] neg_hi:[0,1]
	s_min_i32 s35, s31, 0xffffffc8
	ds_write_b32 v67, v3
	v_pk_add_f32 v[6:7], v[6:7], v[8:9]
	s_mov_b64 s[10:11], 0
	v_mov_b32_e32 v3, s35

.LBB0_105:
	s_ashr_i32 s81, s80, 31
	v_lshl_add_u64 v[4:5], v[2:3], 2, s[70:71]
	s_lshl_b64 s[82:83], s[80:81], 12
	v_lshl_add_u64 v[6:7], v[4:5], 0, s[82:83]
	global_load_dwordx2 v[26:27], v[6:7], off
	s_or_b32 s82, s80, 1
	s_ashr_i32 s83, s82, 31
	s_lshl_b64 s[82:83], s[82:83], 12
	v_lshl_add_u64 v[6:7], v[4:5], 0, s[82:83]
	global_load_dwordx2 v[28:29], v[6:7], off
	s_or_b32 s82, s80, 2
	s_ashr_i32 s83, s82, 31
	s_lshl_b64 s[82:83], s[82:83], 12
	v_lshl_add_u64 v[8:9], v[4:5], 0, s[82:83]
	global_load_dwordx2 v[30:31], v[8:9], off
	s_or_b32 s82, s80, 3
	s_ashr_i32 s83, s82, 31
	s_lshl_b64 s[82:83], s[82:83], 12
	v_lshl_add_u64 v[32:33], v[4:5], 0, s[82:83]
	s_or_b32 s82, s80, 4
	s_ashr_i32 s83, s82, 31
	s_lshl_b64 s[82:83], s[82:83], 12
	v_lshl_add_u64 v[36:37], v[4:5], 0, s[82:83]
	s_or_b32 s82, s80, 5
	global_load_dwordx2 v[32:33], v[32:33], off
	s_ashr_i32 s83, s82, 31
	s_lshl_b64 s[82:83], s[82:83], 12
	v_lshl_add_u64 v[44:45], v[4:5], 0, s[82:83]
	s_or_b32 s82, s80, 6
	s_ashr_i32 s83, s82, 31
	s_lshl_b64 s[82:83], s[82:83], 12
	v_lshl_add_u64 v[42:43], v[4:5], 0, s[82:83]
	s_or_b32 s82, s80, 7
	s_ashr_i32 s83, s82, 31
	s_lshl_b64 s[82:83], s[82:83], 12
	v_lshl_add_u64 v[40:41], v[4:5], 0, s[82:83]
	s_or_b32 s82, s80, 8
	s_ashr_i32 s83, s82, 31
	s_lshl_b64 s[82:83], s[82:83], 12
	s_min_i32 s35, s31, 3
	v_lshl_add_u64 v[38:39], v[4:5], 0, s[82:83]
	s_or_b32 s82, s80, 9
	s_add_i32 s35, s35, 1
	s_ashr_i32 s83, s82, 31
	v_cvt_f32_i32_e32 v3, s35
	s_lshl_b64 s[82:83], s[82:83], 12
	v_lshl_add_u64 v[22:23], v[4:5], 0, s[82:83]
	s_or_b32 s82, s80, 10
	s_ashr_i32 s83, s82, 31
	s_lshl_b64 s[82:83], s[82:83], 12
	global_load_dwordx2 v[36:37], v[36:37], off
	v_lshl_add_u64 v[18:19], v[4:5], 0, s[82:83]
	s_or_b32 s82, s80, 11
	s_ashr_i32 s83, s82, 31
	s_lshl_b64 s[82:83], s[82:83], 12
	v_lshl_add_u64 v[14:15], v[4:5], 0, s[82:83]
	s_or_b32 s82, s80, 12
	s_ashr_i32 s83, s82, 31
	s_lshl_b64 s[82:83], s[82:83], 12
	v_lshl_add_u64 v[12:13], v[4:5], 0, s[82:83]
	s_or_b32 s82, s80, 13
	s_ashr_i32 s83, s82, 31
	s_lshl_b64 s[82:83], s[82:83], 12
	v_lshl_add_u64 v[10:11], v[4:5], 0, s[82:83]
	s_or_b32 s82, s80, 14
	s_min_i32 s35, s31, 2
	s_ashr_i32 s83, s82, 31
	s_add_i32 s35, s35, 2
	s_lshl_b64 s[82:83], s[82:83], 12
	v_rcp_f32_e32 v46, v3
	s_nop 0
	v_cvt_f32_i32_e32 v3, s35
	global_load_dwordx2 v[14:15], v[14:15], off
	s_waitcnt vmcnt(5)
	v_pk_add_f32 v[34:35], v[34:35], v[26:27]
	global_load_dwordx2 v[10:11], v[10:11], off
	v_lshl_add_u64 v[8:9], v[4:5], 0, s[82:83]
	s_or_b32 s82, s80, 15
	s_ashr_i32 s83, s82, 31
	s_lshl_b64 s[82:83], s[82:83], 12
	v_lshl_add_u64 v[6:7], v[4:5], 0, s[82:83]
	v_lshlrev_b32_e32 v58, 2, v221
	v_pk_fma_f32 v[46:47], v[46:47], v[34:35], v[26:27] op_sel_hi:[0,1,1] neg_lo:[0,0,1] neg_hi:[0,0,1]
	v_and_b32_e32 v68, 12, v58
	v_cvt_pk_bf16_f32 v46, v46, v47
	v_and_b32_e32 v47, -16, v58
	v_add3_u32 v61, 0, v47, v68
	ds_write_b32 v61, v46
	s_min_i32 s35, s31, 1
	s_add_i32 s35, s35, 3
	v_rcp_f32_e32 v46, v3
	s_nop 0
	v_cvt_f32_i32_e32 v3, s35
	s_waitcnt vmcnt(5)
	v_pk_add_f32 v[24:25], v[28:29], v[24:25] neg_lo:[0,1] neg_hi:[0,1]
	v_bitop3_b32 v48, v58, 16, -16 bitop3:0x6c
	v_pk_add_f32 v[24:25], v[34:35], v[24:25]
	v_add3_u32 v59, 0, v48, v68
	v_pk_fma_f32 v[34:35], v[46:47], v[24:25], v[28:29] op_sel_hi:[0,1,1] neg_lo:[0,0,1] neg_hi:[0,0,1]
	v_cvt_pk_bf16_f32 v34, v34, v35
	ds_write_b32 v59, v34 offset:2048
	s_min_i32 s35, s31, 0
	s_or_b32 s35, s35, 4
	global_load_dwordx2 v[34:35], v[44:45], off
	v_cvt_f32_i32_e32 v45, s35
	s_waitcnt vmcnt(5)
	v_pk_add_f32 v[20:21], v[30:31], v[20:21] neg_lo:[0,1] neg_hi:[0,1]
	v_rcp_f32_e32 v44, v3
	s_nop 0
	v_pk_add_f32 v[20:21], v[24:25], v[20:21]
	v_bitop3_b32 v3, v58, 32, -16 bitop3:0x6c
	v_pk_fma_f32 v[24:25], v[44:45], v[20:21], v[30:31] op_sel_hi:[0,1,1] neg_lo:[0,0,1] neg_hi:[0,0,1]
	v_cvt_pk_bf16_f32 v24, v24, v25
	v_add3_u32 v60, 0, v3, v68
	ds_write_b32 v60, v24 offset:4096
	global_load_dwordx2 v[24:25], v[42:43], off
	s_min_i32 s35, s31, -1
	s_add_i32 s35, s35, 5
	v_cvt_f32_i32_e32 v43, s35
	v_rcp_f32_e32 v42, v45
	s_nop 0
	global_load_dwordx2 v[22:23], v[22:23], off
	s_waitcnt vmcnt(6)
	v_pk_add_f32 v[16:17], v[32:33], v[16:17] neg_lo:[0,1] neg_hi:[0,1]
	v_bitop3_b32 v44, v58, 48, -16 bitop3:0x6c
	v_pk_add_f32 v[16:17], v[20:21], v[16:17]
	v_pk_fma_f32 v[20:21], v[42:43], v[16:17], v[32:33] op_sel_hi:[0,1,1] neg_lo:[0,0,1] neg_hi:[0,0,1]
	v_cvt_pk_bf16_f32 v20, v20, v21
	v_add3_u32 v42, 0, v44, v68
	ds_write_b32 v42, v20 offset:6144
	global_load_dwordx2 v[20:21], v[40:41], off
	s_min_i32 s35, s31, -2
	s_add_i32 s35, s35, 6
	v_cvt_f32_i32_e32 v41, s35
	v_rcp_f32_e32 v40, v43
	s_nop 0
	s_waitcnt vmcnt(6)
	v_pk_add_f32 v[26:27], v[36:37], v[26:27] neg_lo:[0,1] neg_hi:[0,1]
	v_pk_add_f32 v[26:27], v[16:17], v[26:27]
	v_bitop3_b32 v45, v58, 64, -16 bitop3:0x6c
	v_pk_fma_f32 v[16:17], v[40:41], v[26:27], v[36:37] op_sel_hi:[0,1,1] neg_lo:[0,0,1] neg_hi:[0,0,1]
	v_cvt_pk_bf16_f32 v16, v16, v17
	v_add3_u32 v40, 0, v45, v68
	ds_write_b32 v40, v16 offset:8192
	global_load_dwordx2 v[16:17], v[38:39], off
	s_min_i32 s35, s31, -3
	s_add_i32 s35, s35, 7
	v_cvt_f32_i32_e32 v39, s35
	global_load_dwordx2 v[18:19], v[18:19], off
	v_rcp_f32_e32 v38, v41
	s_nop 0
	s_movk_i32 s35, 0x50
	s_waitcnt vmcnt(5)
	v_pk_add_f32 v[28:29], v[34:35], v[28:29] neg_lo:[0,1] neg_hi:[0,1]
	v_bitop3_b32 v46, v58, s35, -16 bitop3:0x6c
	v_pk_add_f32 v[26:27], v[26:27], v[28:29]
	v_add3_u32 v41, 0, v46, v68
	v_pk_fma_f32 v[28:29], v[38:39], v[26:27], v[34:35] op_sel_hi:[0,1,1] neg_lo:[0,0,1] neg_hi:[0,0,1]
	v_cvt_pk_bf16_f32 v28, v28, v29
	ds_write_b32 v41, v28 offset:10240
	s_min_i32 s35, s31, -4
	s_add_i32 s35, s35, 8
	v_rcp_f32_e32 v28, v39
	s_nop 0
	s_waitcnt vmcnt(4)
	v_pk_add_f32 v[30:31], v[24:25], v[30:31] neg_lo:[0,1] neg_hi:[0,1]
	global_load_dwordx2 v[12:13], v[12:13], off
	v_pk_add_f32 v[26:27], v[26:27], v[30:31]
	v_cvt_f32_i32_e32 v30, s35
	v_pk_fma_f32 v[28:29], v[28:29], v[26:27], v[24:25] op_sel_hi:[0,1,1] neg_lo:[0,0,1] neg_hi:[0,0,1]
	v_cvt_pk_bf16_f32 v28, v28, v29
	s_movk_i32 s35, 0x60
	v_bitop3_b32 v49, v58, s35, -16 bitop3:0x6c
	v_add3_u32 v43, 0, v49, v68
	ds_write_b32 v43, v28 offset:12288
	s_min_i32 s35, s31, -5
	v_rcp_f32_e32 v28, v30
	s_nop 0
	s_add_i32 s35, s35, 9
	s_waitcnt vmcnt(3)
	v_pk_add_f32 v[30:31], v[20:21], v[32:33] neg_lo:[0,1] neg_hi:[0,1]
	global_load_dwordx2 v[8:9], v[8:9], off
	v_pk_add_f32 v[26:27], v[26:27], v[30:31]
	v_cvt_f32_i32_e32 v30, s35
	v_pk_fma_f32 v[28:29], v[28:29], v[26:27], v[20:21] op_sel_hi:[0,1,1] neg_lo:[0,0,1] neg_hi:[0,0,1]
	v_cvt_pk_bf16_f32 v28, v28, v29
	s_movk_i32 s35, 0x70
	v_bitop3_b32 v50, v58, s35, -16 bitop3:0x6c
	v_add3_u32 v63, 0, v50, v68
	ds_write_b32 v63, v28 offset:14336
	s_min_i32 s35, s31, -6
	v_rcp_f32_e32 v28, v30
	s_nop 0
	s_waitcnt vmcnt(3)
	v_pk_add_f32 v[30:31], v[16:17], v[36:37] neg_lo:[0,1] neg_hi:[0,1]
	s_add_i32 s35, s35, 10
	v_pk_add_f32 v[26:27], v[26:27], v[30:31]
	v_cvt_f32_i32_e32 v30, s35
	v_pk_fma_f32 v[28:29], v[28:29], v[26:27], v[16:17] op_sel_hi:[0,1,1] neg_lo:[0,0,1] neg_hi:[0,0,1]
	v_cvt_pk_bf16_f32 v28, v28, v29
	s_movk_i32 s35, 0x80
	v_bitop3_b32 v51, v58, s35, -16 bitop3:0x6c
	v_add3_u32 v64, 0, v51, v68
	ds_write_b32 v64, v28 offset:16384
	s_min_i32 s35, s31, -7
	v_rcp_f32_e32 v28, v30
	s_nop 0
	v_pk_add_f32 v[30:31], v[22:23], v[34:35] neg_lo:[0,1] neg_hi:[0,1]
	s_add_i32 s35, s35, 11
	v_pk_add_f32 v[26:27], v[26:27], v[30:31]
	v_cvt_f32_i32_e32 v30, s35
	v_pk_fma_f32 v[28:29], v[28:29], v[26:27], v[22:23] op_sel_hi:[0,1,1] neg_lo:[0,0,1] neg_hi:[0,0,1]
	v_cvt_pk_bf16_f32 v28, v28, v29
	s_movk_i32 s35, 0x90
	v_bitop3_b32 v52, v58, s35, -16 bitop3:0x6c
	v_add3_u32 v65, 0, v52, v68
	ds_write_b32 v65, v28 offset:18432
	s_min_i32 s35, s31, -8
	s_add_i32 s35, s35, 12
	v_cvt_f32_i32_e32 v29, s35
	s_waitcnt vmcnt(2)
	v_pk_add_f32 v[24:25], v[18:19], v[24:25] neg_lo:[0,1] neg_hi:[0,1]
	v_rcp_f32_e32 v28, v30
	s_nop 0
	v_pk_add_f32 v[24:25], v[26:27], v[24:25]
	global_load_dwordx2 v[6:7], v[6:7], off
	v_pk_fma_f32 v[26:27], v[28:29], v[24:25], v[18:19] op_sel_hi:[0,1,1] neg_lo:[0,0,1] neg_hi:[0,0,1]
	v_cvt_pk_bf16_f32 v26, v26, v27
	s_movk_i32 s35, 0xa0
	v_bitop3_b32 v53, v58, s35, -16 bitop3:0x6c
	v_add3_u32 v66, 0, v53, v68
	ds_write_b32 v66, v26 offset:20480
	s_min_i32 s35, s31, -9
	s_add_i32 s35, s35, 13
	v_cvt_f32_i32_e32 v27, s35
	v_pk_add_f32 v[20:21], v[14:15], v[20:21] neg_lo:[0,1] neg_hi:[0,1]
	v_rcp_f32_e32 v26, v29
	s_nop 0
	v_pk_add_f32 v[20:21], v[24:25], v[20:21]
	s_movk_i32 s35, 0xb0
	v_pk_fma_f32 v[24:25], v[26:27], v[20:21], v[14:15] op_sel_hi:[0,1,1] neg_lo:[0,0,1] neg_hi:[0,0,1]
	v_cvt_pk_bf16_f32 v24, v24, v25
	v_bitop3_b32 v54, v58, s35, -16 bitop3:0x6c
	v_add3_u32 v62, 0, v54, v68
	ds_write_b32 v62, v24 offset:22528
	s_min_i32 s35, s31, -10
	s_add_i32 s35, s35, 14
	v_cvt_f32_i32_e32 v25, s35
	s_waitcnt vmcnt(2)
	v_pk_add_f32 v[16:17], v[12:13], v[16:17] neg_lo:[0,1] neg_hi:[0,1]
	v_rcp_f32_e32 v24, v27
	s_nop 0
	v_pk_add_f32 v[16:17], v[20:21], v[16:17]
	s_movk_i32 s35, 0xc0
	v_pk_fma_f32 v[20:21], v[24:25], v[16:17], v[12:13] op_sel_hi:[0,1,1] neg_lo:[0,0,1] neg_hi:[0,0,1]
	v_cvt_pk_bf16_f32 v20, v20, v21
	v_bitop3_b32 v55, v58, s35, -16 bitop3:0x6c
	v_add3_u32 v67, 0, v55, v68
	ds_write_b32 v67, v20 offset:24576
	s_min_i32 s35, s31, -11
	v_pk_add_f32 v[22:23], v[10:11], v[22:23] neg_lo:[0,1] neg_hi:[0,1]
	s_add_i32 s35, s35, 15
	v_pk_add_f32 v[16:17], v[16:17], v[22:23]
	v_cvt_f32_i32_e32 v22, s35
	v_rcp_f32_e32 v20, v25
	s_nop 0
	v_pk_fma_f32 v[20:21], v[20:21], v[16:17], v[10:11] op_sel_hi:[0,1,1] neg_lo:[0,0,1] neg_hi:[0,0,1]
	v_cvt_pk_bf16_f32 v20, v20, v21
	s_movk_i32 s35, 0xd0
	v_bitop3_b32 v56, v58, s35, -16 bitop3:0x6c
	v_add3_u32 v70, 0, v56, v68
	ds_write_b32 v70, v20 offset:26624
	s_min_i32 s35, s31, -12
	s_add_i32 s35, s35, 16
	v_cvt_f32_i32_e32 v21, s35
	s_waitcnt vmcnt(1)
	v_pk_add_f32 v[18:19], v[8:9], v[18:19] neg_lo:[0,1] neg_hi:[0,1]
	v_rcp_f32_e32 v20, v22
	s_nop 0
	v_pk_add_f32 v[16:17], v[16:17], v[18:19]
	s_movk_i32 s35, 0xe0
	v_pk_fma_f32 v[18:19], v[20:21], v[16:17], v[8:9] op_sel_hi:[0,1,1] neg_lo:[0,0,1] neg_hi:[0,0,1]
	v_cvt_pk_bf16_f32 v18, v18, v19
	v_bitop3_b32 v57, v58, s35, -16 bitop3:0x6c
	v_add3_u32 v71, 0, v57, v68
	ds_write_b32 v71, v18 offset:28672
	s_or_b32 s82, s80, 16
	s_ashr_i32 s83, s82, 31
	s_lshl_b64 s[82:83], s[82:83], 12
	v_lshl_add_u64 v[18:19], v[4:5], 0, s[82:83]
	global_load_dwordx2 v[22:23], v[18:19], off
	s_waitcnt vmcnt(1)
	v_pk_add_f32 v[14:15], v[6:7], v[14:15] neg_lo:[0,1] neg_hi:[0,1]
	v_rcp_f32_e32 v18, v21
	s_nop 0
	v_pk_add_f32 v[16:17], v[16:17], v[14:15]
	s_movk_i32 s35, 0xf0
	s_or_b32 s82, s80, 17
	v_pk_fma_f32 v[14:15], v[18:19], v[16:17], v[6:7] op_sel_hi:[0,1,1] neg_lo:[0,0,1] neg_hi:[0,0,1]
	v_bitop3_b32 v69, v58, s35, -16 bitop3:0x6c
	s_ashr_i32 s83, s82, 31
	v_cvt_pk_bf16_f32 v14, v14, v15
	v_add3_u32 v58, 0, v69, v68
	s_lshl_b64 s[82:83], s[82:83], 12
	ds_write_b32 v58, v14 offset:30720
	v_lshl_add_u64 v[14:15], v[4:5], 0, s[82:83]
	global_load_dwordx2 v[24:25], v[14:15], off
	s_or_b32 s82, s80, 18
	s_ashr_i32 s83, s82, 31
	s_lshl_b64 s[82:83], s[82:83], 12
	v_lshl_add_u64 v[26:27], v[4:5], 0, s[82:83]
	global_load_dwordx2 v[28:29], v[26:27], off
	s_or_b32 s82, s80, 19
	s_ashr_i32 s83, s82, 31
	s_lshl_b64 s[82:83], s[82:83], 12
	v_lshl_add_u64 v[30:31], v[4:5], 0, s[82:83]
	s_or_b32 s82, s80, 20
	s_ashr_i32 s83, s82, 31
	s_lshl_b64 s[82:83], s[82:83], 12
	v_lshl_add_u64 v[32:33], v[4:5], 0, s[82:83]
	s_or_b32 s82, s80, 21
	s_ashr_i32 s83, s82, 31
	s_lshl_b64 s[82:83], s[82:83], 12
	v_lshl_add_u64 v[34:35], v[4:5], 0, s[82:83]
	s_or_b32 s82, s80, 22
	s_ashr_i32 s83, s82, 31
	s_lshl_b64 s[82:83], s[82:83], 12
	v_lshl_add_u64 v[72:73], v[4:5], 0, s[82:83]
	s_or_b32 s82, s80, 23
	s_ashr_i32 s83, s82, 31
	s_lshl_b64 s[82:83], s[82:83], 12
	v_lshl_add_u64 v[36:37], v[4:5], 0, s[82:83]
	s_or_b32 s82, s80, 24
	s_ashr_i32 s83, s82, 31
	s_min_i32 s35, s31, -13
	s_lshl_b64 s[82:83], s[82:83], 12
	s_add_i32 s35, s35, 17
	v_lshl_add_u64 v[38:39], v[4:5], 0, s[82:83]
	s_or_b32 s82, s80, 25
	v_cvt_f32_i32_e32 v74, s35
	s_ashr_i32 s83, s82, 31
	s_lshl_b64 s[82:83], s[82:83], 12
	v_lshl_add_u64 v[20:21], v[4:5], 0, s[82:83]
	global_load_dwordx2 v[20:21], v[20:21], off
	s_min_i32 s35, s31, -14
	s_add_i32 s35, s35, 18
	s_or_b32 s82, s80, 26
	v_rcp_f32_e32 v74, v74
	s_nop 0
	global_load_dwordx2 v[26:27], v[30:31], off
	v_cvt_f32_i32_e32 v75, s35
	s_min_i32 s35, s31, -15
	s_add_i32 s35, s35, 19
	s_ashr_i32 s83, s82, 31
	s_lshl_b64 s[82:83], s[82:83], 12
	global_load_dwordx2 v[36:37], v[36:37], off
	v_lshl_add_u64 v[18:19], v[4:5], 0, s[82:83]
	s_waitcnt vmcnt(5)
	v_pk_add_f32 v[12:13], v[22:23], v[12:13] neg_lo:[0,1] neg_hi:[0,1]
	s_or_b32 s82, s80, 27
	v_pk_add_f32 v[76:77], v[16:17], v[12:13]
	s_ashr_i32 s83, s82, 31
	v_pk_fma_f32 v[12:13], v[74:75], v[76:77], v[22:23] op_sel_hi:[0,1,1] neg_lo:[0,0,1] neg_hi:[0,0,1]
	v_cvt_pk_bf16_f32 v12, v12, v13
	ds_write_b32 v61, v12 offset:32768
	global_load_dwordx2 v[30:31], v[32:33], off
	v_rcp_f32_e32 v32, v75
	s_nop 0
	v_cvt_f32_i32_e32 v61, s35
	s_waitcnt vmcnt(5)
	v_pk_add_f32 v[10:11], v[24:25], v[10:11] neg_lo:[0,1] neg_hi:[0,1]
	s_waitcnt vmcnt(4)
	v_pk_add_f32 v[8:9], v[28:29], v[8:9] neg_lo:[0,1] neg_hi:[0,1]
	v_pk_add_f32 v[74:75], v[76:77], v[10:11]
	v_pk_fma_f32 v[10:11], v[32:33], v[74:75], v[24:25] op_sel_hi:[0,1,1] neg_lo:[0,0,1] neg_hi:[0,0,1]
	v_cvt_pk_bf16_f32 v10, v10, v11
	ds_write_b32 v59, v10 offset:34816
	global_load_dwordx2 v[32:33], v[34:35], off
	v_rcp_f32_e32 v34, v61
	s_nop 0
	v_pk_add_f32 v[74:75], v[74:75], v[8:9]
	s_min_i32 s35, s31, -16
	v_pk_fma_f32 v[8:9], v[34:35], v[74:75], v[28:29] op_sel_hi:[0,1,1] neg_lo:[0,0,1] neg_hi:[0,0,1]
	global_load_dwordx2 v[34:35], v[72:73], off
	s_add_i32 s35, s35, 20
	v_cvt_f32_i32_e32 v59, s35
	s_lshl_b64 s[82:83], s[82:83], 12
	v_lshl_add_u64 v[14:15], v[4:5], 0, s[82:83]
	s_or_b32 s82, s80, 28
	v_cvt_pk_bf16_f32 v8, v8, v9
	s_ashr_i32 s83, s82, 31
	ds_write_b32 v60, v8 offset:36864
	s_lshl_b64 s[82:83], s[82:83], 12
	v_lshl_add_u64 v[16:17], v[4:5], 0, s[82:83]
	s_or_b32 s82, s80, 29
	s_ashr_i32 s83, s82, 31
	s_lshl_b64 s[82:83], s[82:83], 12
	v_lshl_add_u64 v[12:13], v[4:5], 0, s[82:83]
	s_or_b32 s82, s80, 30
	s_min_i32 s35, s31, 0xffffffef
	s_ashr_i32 s83, s82, 31
	s_add_i32 s35, s35, 21
	s_lshl_b64 s[82:83], s[82:83], 12
	v_rcp_f32_e32 v60, v59
	s_nop 0
	v_cvt_f32_i32_e32 v59, s35
	v_lshl_add_u64 v[10:11], v[4:5], 0, s[82:83]
	s_or_b32 s82, s80, 31
	s_ashr_i32 s83, s82, 31
	s_lshl_b64 s[82:83], s[82:83], 12
	v_lshl_add_u64 v[8:9], v[4:5], 0, s[82:83]
	s_waitcnt vmcnt(4)
	v_pk_add_f32 v[6:7], v[26:27], v[6:7] neg_lo:[0,1] neg_hi:[0,1]
	v_pk_add_f32 v[6:7], v[74:75], v[6:7]
	s_min_i32 s35, s31, 0xffffffee
	v_pk_fma_f32 v[60:61], v[60:61], v[6:7], v[26:27] op_sel_hi:[0,1,1] neg_lo:[0,0,1] neg_hi:[0,0,1]
	v_cvt_pk_bf16_f32 v60, v60, v61
	ds_write_b32 v42, v60 offset:38912
	s_add_i32 s35, s35, 22
	v_rcp_f32_e32 v42, v59
	s_nop 0
	v_cvt_f32_i32_e32 v59, s35
	s_waitcnt vmcnt(2)
	v_pk_add_f32 v[22:23], v[30:31], v[22:23] neg_lo:[0,1] neg_hi:[0,1]
	s_min_i32 s35, s31, 0xffffffed
	v_pk_add_f32 v[22:23], v[6:7], v[22:23]
	v_pk_fma_f32 v[6:7], v[42:43], v[22:23], v[30:31] op_sel_hi:[0,1,1] neg_lo:[0,0,1] neg_hi:[0,0,1]
	v_cvt_pk_bf16_f32 v6, v6, v7
	ds_write_b32 v40, v6 offset:40960
	global_load_dwordx2 v[6:7], v[38:39], off
	s_add_i32 s35, s35, 23
	v_cvt_f32_i32_e32 v39, s35
	s_waitcnt vmcnt(2)
	v_pk_add_f32 v[24:25], v[32:33], v[24:25] neg_lo:[0,1] neg_hi:[0,1]
	v_rcp_f32_e32 v38, v59
	s_nop 0
	v_pk_add_f32 v[22:23], v[22:23], v[24:25]
	v_pk_fma_f32 v[24:25], v[38:39], v[22:23], v[32:33] op_sel_hi:[0,1,1] neg_lo:[0,0,1] neg_hi:[0,0,1]
	v_cvt_pk_bf16_f32 v24, v24, v25
	ds_write_b32 v41, v24 offset:43008
	s_min_i32 s35, s31, 0xffffffec
	s_add_i32 s35, s35, 24
	v_cvt_f32_i32_e32 v25, s35
	v_rcp_f32_e32 v24, v39
	s_nop 0
	s_waitcnt vmcnt(1)
	v_pk_add_f32 v[28:29], v[34:35], v[28:29] neg_lo:[0,1] neg_hi:[0,1]
	s_min_i32 s35, s31, 0xffffffeb
	v_pk_add_f32 v[28:29], v[22:23], v[28:29]
	s_add_i32 s35, s35, 25
	v_pk_fma_f32 v[22:23], v[24:25], v[28:29], v[34:35] op_sel_hi:[0,1,1] neg_lo:[0,0,1] neg_hi:[0,0,1]
	v_cvt_pk_bf16_f32 v22, v22, v23
	ds_write_b32 v43, v22 offset:45056
	global_load_dwordx2 v[22:23], v[18:19], off
	v_rcp_f32_e32 v18, v25
	s_nop 0
	v_pk_add_f32 v[24:25], v[36:37], v[26:27] neg_lo:[0,1] neg_hi:[0,1]
	global_load_dwordx2 v[26:27], v[14:15], off
	v_cvt_f32_i32_e32 v38, s35
	v_pk_add_f32 v[24:25], v[28:29], v[24:25]
	s_min_i32 s35, s31, 0xffffffea
	v_pk_fma_f32 v[18:19], v[18:19], v[24:25], v[36:37] op_sel_hi:[0,1,1] neg_lo:[0,0,1] neg_hi:[0,0,1]
	v_cvt_pk_bf16_f32 v18, v18, v19
	ds_write_b32 v63, v18 offset:47104
	s_add_i32 s35, s35, 26
	v_cvt_f32_i32_e32 v28, s35
	v_rcp_f32_e32 v14, v38
	s_nop 0
	s_min_i32 s35, s31, 0xffffffe9
	s_add_i32 s35, s35, 27
	s_waitcnt vmcnt(2)
	v_pk_add_f32 v[18:19], v[6:7], v[30:31] neg_lo:[0,1] neg_hi:[0,1]
	v_pk_add_f32 v[24:25], v[24:25], v[18:19]
	global_load_dwordx2 v[18:19], v[16:17], off
	v_pk_fma_f32 v[14:15], v[14:15], v[24:25], v[6:7] op_sel_hi:[0,1,1] neg_lo:[0,0,1] neg_hi:[0,0,1]
	v_cvt_pk_bf16_f32 v14, v14, v15
	ds_write_b32 v64, v14 offset:49152
	v_rcp_f32_e32 v14, v28
	s_nop 0
	v_cvt_f32_i32_e32 v28, s35
	v_pk_add_f32 v[16:17], v[20:21], v[32:33] neg_lo:[0,1] neg_hi:[0,1]
	s_min_i32 s35, s31, 0xffffffe8
	v_pk_add_f32 v[24:25], v[24:25], v[16:17]
	v_pk_fma_f32 v[14:15], v[14:15], v[24:25], v[20:21] op_sel_hi:[0,1,1] neg_lo:[0,0,1] neg_hi:[0,0,1]
	v_cvt_pk_bf16_f32 v14, v14, v15
	global_load_dwordx2 v[16:17], v[12:13], off
	ds_write_b32 v65, v14 offset:51200
	s_add_i32 s35, s35, 28
	v_rcp_f32_e32 v12, v28
	s_nop 0
	v_cvt_f32_i32_e32 v28, s35
	s_min_i32 s35, s31, 0xffffffe7
	s_add_i32 s35, s35, 29
	v_readlane_b32 s12, v254, 47
	s_waitcnt vmcnt(3)
	v_pk_add_f32 v[14:15], v[22:23], v[34:35] neg_lo:[0,1] neg_hi:[0,1]
	v_pk_add_f32 v[24:25], v[24:25], v[14:15]
	global_load_dwordx2 v[14:15], v[10:11], off
	v_pk_fma_f32 v[12:13], v[12:13], v[24:25], v[22:23] op_sel_hi:[0,1,1] neg_lo:[0,0,1] neg_hi:[0,0,1]
	v_cvt_pk_bf16_f32 v12, v12, v13
	ds_write_b32 v66, v12 offset:53248
	s_waitcnt vmcnt(3)
	v_pk_add_f32 v[12:13], v[26:27], v[36:37] neg_lo:[0,1] neg_hi:[0,1]
	v_rcp_f32_e32 v10, v28
	s_nop 0
	v_pk_add_f32 v[12:13], v[24:25], v[12:13]
	v_cvt_f32_i32_e32 v28, s35
	v_pk_fma_f32 v[24:25], v[10:11], v[12:13], v[26:27] op_sel_hi:[0,1,1] neg_lo:[0,0,1] neg_hi:[0,0,1]
	global_load_dwordx2 v[10:11], v[8:9], off
	v_cvt_pk_bf16_f32 v8, v24, v25
	ds_write_b32 v62, v8 offset:55296
	s_min_i32 s35, s31, 0xffffffe6
	s_add_i32 s35, s35, 30
	v_cvt_f32_i32_e32 v24, s35
	s_waitcnt vmcnt(3)
	v_pk_add_f32 v[6:7], v[18:19], v[6:7] neg_lo:[0,1] neg_hi:[0,1]
	v_pk_add_f32 v[6:7], v[12:13], v[6:7]
	v_rcp_f32_e32 v8, v28
	s_nop 0
	v_pk_fma_f32 v[8:9], v[8:9], v[6:7], v[18:19] op_sel_hi:[0,1,1] neg_lo:[0,0,1] neg_hi:[0,0,1]
	v_cvt_pk_bf16_f32 v8, v8, v9
	ds_write_b32 v67, v8 offset:57344
	s_min_i32 s35, s31, 0xffffffe5
	s_add_i32 s35, s35, 31
	v_rcp_f32_e32 v8, v24
	s_nop 0
	v_cvt_f32_i32_e32 v24, s35
	s_waitcnt vmcnt(2)
	v_pk_add_f32 v[12:13], v[16:17], v[20:21] neg_lo:[0,1] neg_hi:[0,1]
	s_min_i32 s35, s31, 0xffffffe4
	v_pk_add_f32 v[6:7], v[6:7], v[12:13]
	v_pk_fma_f32 v[8:9], v[8:9], v[6:7], v[16:17] op_sel_hi:[0,1,1] neg_lo:[0,0,1] neg_hi:[0,0,1]
	v_cvt_pk_bf16_f32 v8, v8, v9
	ds_write_b32 v70, v8 offset:59392
	s_add_i32 s35, s35, 32
	v_cvt_f32_i32_e32 v20, s35
	v_rcp_f32_e32 v8, v24
	s_nop 0
	s_min_i32 s35, s31, 0xffffffe3
	s_waitcnt vmcnt(1)
	v_pk_add_f32 v[12:13], v[14:15], v[22:23] neg_lo:[0,1] neg_hi:[0,1]
	s_add_i32 s35, s35, 33
	v_pk_add_f32 v[6:7], v[6:7], v[12:13]
	v_pk_fma_f32 v[8:9], v[8:9], v[6:7], v[14:15] op_sel_hi:[0,1,1] neg_lo:[0,0,1] neg_hi:[0,0,1]
	v_cvt_pk_bf16_f32 v8, v8, v9
	ds_write_b32 v71, v8 offset:61440
	s_waitcnt vmcnt(0)
	v_pk_add_f32 v[12:13], v[10:11], v[26:27] neg_lo:[0,1] neg_hi:[0,1]
	v_rcp_f32_e32 v8, v20
	s_nop 0
	v_pk_add_f32 v[34:35], v[6:7], v[12:13]
	s_or_b32 s82, s80, 32
	v_pk_fma_f32 v[6:7], v[8:9], v[34:35], v[10:11] op_sel_hi:[0,1,1] neg_lo:[0,0,1] neg_hi:[0,0,1]
	s_ashr_i32 s83, s82, 31
	v_cvt_pk_bf16_f32 v6, v6, v7
	s_lshl_b64 s[82:83], s[82:83], 12
	ds_write_b32 v58, v6 offset:63488
	v_lshl_add_u64 v[6:7], v[4:5], 0, s[82:83]
	global_load_dwordx2 v[28:29], v[6:7], off
	s_or_b32 s82, s80, 33
	s_ashr_i32 s83, s82, 31
	s_lshl_b64 s[82:83], s[82:83], 12
	v_lshl_add_u64 v[6:7], v[4:5], 0, s[82:83]
	global_load_dwordx2 v[30:31], v[6:7], off
	s_or_b32 s82, s80, 34
	s_ashr_i32 s83, s82, 31
	s_lshl_b64 s[82:83], s[82:83], 12
	v_lshl_add_u64 v[8:9], v[4:5], 0, s[82:83]
	s_or_b32 s82, s80, 35
	s_ashr_i32 s83, s82, 31
	s_lshl_b64 s[82:83], s[82:83], 12
	v_lshl_add_u64 v[32:33], v[4:5], 0, s[82:83]
	s_or_b32 s82, s80, 36
	s_ashr_i32 s83, s82, 31
	s_lshl_b64 s[82:83], s[82:83], 12
	global_load_dwordx2 v[38:39], v[8:9], off
	v_lshl_add_u64 v[58:59], v[4:5], 0, s[82:83]
	s_or_b32 s82, s80, 37
	s_ashr_i32 s83, s82, 31
	s_lshl_b64 s[82:83], s[82:83], 12
	v_lshl_add_u64 v[60:61], v[4:5], 0, s[82:83]
	s_or_b32 s82, s80, 38
	s_ashr_i32 s83, s82, 31
	s_lshl_b64 s[82:83], s[82:83], 12
	v_lshl_add_u64 v[42:43], v[4:5], 0, s[82:83]
	s_or_b32 s82, s80, 39
	s_ashr_i32 s83, s82, 31
	s_lshl_b64 s[82:83], s[82:83], 12
	v_lshl_add_u64 v[36:37], v[4:5], 0, s[82:83]
	s_or_b32 s82, s80, 40
	s_ashr_i32 s83, s82, 31
	s_lshl_b64 s[82:83], s[82:83], 12
	v_lshl_add_u64 v[40:41], v[4:5], 0, s[82:83]
	s_or_b32 s82, s80, 41
	s_ashr_i32 s83, s82, 31
	v_cvt_f32_i32_e32 v62, s35
	s_lshl_b64 s[82:83], s[82:83], 12
	v_lshl_add_u64 v[26:27], v[4:5], 0, s[82:83]
	s_or_b32 s82, s80, 42
	s_ashr_i32 s83, s82, 31
	s_lshl_b64 s[82:83], s[82:83], 12
	v_lshl_add_u64 v[24:25], v[4:5], 0, s[82:83]
	s_or_b32 s82, s80, 43
	s_ashr_i32 s83, s82, 31
	s_lshl_b64 s[82:83], s[82:83], 12
	v_lshl_add_u64 v[22:23], v[4:5], 0, s[82:83]
	s_or_b32 s82, s80, 44
	s_ashr_i32 s83, s82, 31
	s_lshl_b64 s[82:83], s[82:83], 12
	v_lshl_add_u64 v[20:21], v[4:5], 0, s[82:83]
	s_or_b32 s82, s80, 45
	s_ashr_i32 s83, s82, 31
	s_lshl_b64 s[82:83], s[82:83], 12
	v_lshl_add_u64 v[12:13], v[4:5], 0, s[82:83]
	s_or_b32 s82, s80, 46
	s_min_i32 s35, s31, 0xffffffe2
	s_ashr_i32 s83, s82, 31
	s_add_i32 s35, s35, 34
	s_lshl_b64 s[82:83], s[82:83], 12
	v_rcp_f32_e32 v62, v62
	s_nop 0
	v_cvt_f32_i32_e32 v63, s35
	global_load_dwordx2 v[24:25], v[24:25], off
	v_readlane_b32 s35, v254, 19
	global_load_dwordx2 v[12:13], v[12:13], off
	v_lshl_add_u64 v[6:7], v[4:5], 0, s[82:83]
	s_or_b32 s82, s80, 47
	s_ashr_i32 s83, s82, 31
	s_waitcnt vmcnt(4)
	v_pk_add_f32 v[18:19], v[28:29], v[18:19] neg_lo:[0,1] neg_hi:[0,1]
	s_lshl_b64 s[82:83], s[82:83], 12
	v_pk_add_f32 v[34:35], v[34:35], v[18:19]
	v_lshl_add_u64 v[8:9], v[4:5], 0, s[82:83]
	v_pk_fma_f32 v[18:19], v[62:63], v[34:35], v[28:29] op_sel_hi:[0,1,1] neg_lo:[0,0,1] neg_hi:[0,0,1]
	v_cvt_pk_bf16_f32 v18, v18, v19
	v_add3_u32 v19, s35, v47, v68
	global_load_dwordx2 v[32:33], v[32:33], off
	ds_write_b32 v19, v18
	global_load_dwordx2 v[18:19], v[58:59], off
	s_min_i32 s35, s31, 0xffffffe1
	s_add_i32 s35, s35, 35
	v_cvt_f32_i32_e32 v59, s35
	s_waitcnt vmcnt(5)
	v_pk_add_f32 v[16:17], v[30:31], v[16:17] neg_lo:[0,1] neg_hi:[0,1]
	v_rcp_f32_e32 v58, v63
	s_nop 0
	v_pk_add_f32 v[16:17], v[34:35], v[16:17]
	v_readlane_b32 s35, v254, 21
	v_pk_fma_f32 v[34:35], v[58:59], v[16:17], v[30:31] op_sel_hi:[0,1,1] neg_lo:[0,0,1] neg_hi:[0,0,1]
	v_cvt_pk_bf16_f32 v34, v34, v35
	v_add3_u32 v35, s35, v48, v68
	ds_write_b32 v35, v34
	global_load_dwordx2 v[34:35], v[60:61], off
	s_min_i32 s35, s31, 0xffffffe0
	s_add_i32 s35, s35, 36
	v_rcp_f32_e32 v58, v59
	s_nop 0
	v_cvt_f32_i32_e32 v59, s35
	s_waitcnt vmcnt(5)
	v_pk_add_f32 v[14:15], v[38:39], v[14:15] neg_lo:[0,1] neg_hi:[0,1]
	v_readlane_b32 s35, v254, 23
	v_pk_add_f32 v[16:17], v[16:17], v[14:15]
	global_load_dwordx2 v[36:37], v[36:37], off
	v_pk_fma_f32 v[14:15], v[58:59], v[16:17], v[38:39] op_sel_hi:[0,1,1] neg_lo:[0,0,1] neg_hi:[0,0,1]
	v_cvt_pk_bf16_f32 v14, v14, v15
	v_add3_u32 v15, s35, v3, v68
	ds_write_b32 v15, v14
	global_load_dwordx2 v[14:15], v[42:43], off
	s_min_i32 s35, s31, 0xffffffdf
	s_add_i32 s35, s35, 37
	v_cvt_f32_i32_e32 v43, s35
	v_rcp_f32_e32 v42, v59
	s_nop 0
	v_readlane_b32 s35, v254, 25
	global_load_dwordx2 v[26:27], v[26:27], off
	v_add3_u32 v3, s25, v3, v68
	global_load_dwordx2 v[6:7], v[6:7], off
	s_waitcnt vmcnt(6)
	v_pk_add_f32 v[10:11], v[32:33], v[10:11] neg_lo:[0,1] neg_hi:[0,1]
	s_nop 0
	v_pk_add_f32 v[10:11], v[16:17], v[10:11]
	global_load_dwordx2 v[8:9], v[8:9], off
	v_pk_fma_f32 v[16:17], v[42:43], v[10:11], v[32:33] op_sel_hi:[0,1,1] neg_lo:[0,0,1] neg_hi:[0,0,1]
	s_waitcnt vmcnt(6)
	v_pk_add_f32 v[28:29], v[18:19], v[28:29] neg_lo:[0,1] neg_hi:[0,1]
	v_pk_add_f32 v[10:11], v[10:11], v[28:29]
	global_load_dwordx2 v[28:29], v[40:41], off
	v_cvt_pk_bf16_f32 v16, v16, v17
	v_add3_u32 v17, s35, v44, v68
	ds_write_b32 v17, v16
	s_min_i32 s35, s31, 0xffffffde
	s_add_i32 s35, s35, 38
	v_cvt_f32_i32_e32 v42, s35
	v_rcp_f32_e32 v16, v43
	s_nop 0
	v_pk_fma_f32 v[16:17], v[16:17], v[10:11], v[18:19] op_sel_hi:[0,1,1] neg_lo:[0,0,1] neg_hi:[0,0,1]
	v_readlane_b32 s35, v254, 29
	v_cvt_pk_bf16_f32 v16, v16, v17
	s_waitcnt vmcnt(6)
	v_pk_add_f32 v[30:31], v[34:35], v[30:31] neg_lo:[0,1] neg_hi:[0,1]
	v_add3_u32 v17, s35, v45, v68
	ds_write_b32 v17, v16
	s_min_i32 s35, s31, 0xffffffdd
	s_add_i32 s35, s35, 39
	v_cvt_f32_i32_e32 v40, s35
	v_pk_add_f32 v[10:11], v[10:11], v[30:31]
	v_rcp_f32_e32 v16, v42
	s_nop 0
	v_pk_fma_f32 v[16:17], v[16:17], v[10:11], v[34:35] op_sel_hi:[0,1,1] neg_lo:[0,0,1] neg_hi:[0,0,1]
	v_readlane_b32 s35, v254, 31
	v_cvt_pk_bf16_f32 v16, v16, v17
	s_waitcnt vmcnt(0)
	v_pk_add_f32 v[18:19], v[28:29], v[18:19] neg_lo:[0,1] neg_hi:[0,1]
	v_add3_u32 v17, s35, v46, v68
	ds_write_b32 v17, v16
	s_min_i32 s35, s31, 0xffffffdc
	s_add_i32 s35, s35, 40
	v_pk_add_f32 v[30:31], v[14:15], v[38:39] neg_lo:[0,1] neg_hi:[0,1]
	v_cvt_f32_i32_e32 v38, s35
	v_pk_add_f32 v[10:11], v[10:11], v[30:31]
	v_rcp_f32_e32 v16, v40
	s_nop 0
	v_pk_fma_f32 v[16:17], v[16:17], v[10:11], v[14:15] op_sel_hi:[0,1,1] neg_lo:[0,0,1] neg_hi:[0,0,1]
	v_readlane_b32 s35, v254, 33
	v_cvt_pk_bf16_f32 v16, v16, v17
	v_pk_add_f32 v[14:15], v[24:25], v[14:15] neg_lo:[0,1] neg_hi:[0,1]
	v_add3_u32 v17, s35, v49, v68
	ds_write_b32 v17, v16
	s_min_i32 s35, s31, 0xffffffdb
	s_add_i32 s35, s35, 41
	v_pk_add_f32 v[30:31], v[36:37], v[32:33] neg_lo:[0,1] neg_hi:[0,1]
	v_cvt_f32_i32_e32 v32, s35
	v_pk_add_f32 v[10:11], v[10:11], v[30:31]
	v_rcp_f32_e32 v16, v38
	s_nop 0
	v_pk_fma_f32 v[16:17], v[16:17], v[10:11], v[36:37] op_sel_hi:[0,1,1] neg_lo:[0,0,1] neg_hi:[0,0,1]
	v_readlane_b32 s35, v254, 35
	v_cvt_pk_bf16_f32 v16, v16, v17
	s_nop 1
	v_add3_u32 v17, s35, v50, v68
	ds_write_b32 v17, v16
	global_load_dwordx2 v[16:17], v[22:23], off
	s_min_i32 s35, s31, 0xffffffda
	s_add_i32 s35, s35, 42
	v_cvt_f32_i32_e32 v23, s35
	v_rcp_f32_e32 v22, v32
	s_nop 0
	v_pk_add_f32 v[18:19], v[10:11], v[18:19]
	v_readlane_b32 s35, v254, 37
	v_pk_fma_f32 v[10:11], v[22:23], v[18:19], v[28:29] op_sel_hi:[0,1,1] neg_lo:[0,0,1] neg_hi:[0,0,1]
	v_cvt_pk_bf16_f32 v10, v10, v11
	v_add3_u32 v11, s35, v51, v68
	ds_write_b32 v11, v10
	global_load_dwordx2 v[10:11], v[20:21], off
	s_min_i32 s35, s31, 0xffffffd9
	s_add_i32 s35, s35, 43
	v_cvt_f32_i32_e32 v30, s35
	v_rcp_f32_e32 v20, v23
	s_nop 0
	v_pk_add_f32 v[22:23], v[26:27], v[34:35] neg_lo:[0,1] neg_hi:[0,1]
	v_readlane_b32 s35, v254, 39
	v_pk_add_f32 v[18:19], v[18:19], v[22:23]
	v_pk_fma_f32 v[20:21], v[20:21], v[18:19], v[26:27] op_sel_hi:[0,1,1] neg_lo:[0,0,1] neg_hi:[0,0,1]
	v_cvt_pk_bf16_f32 v20, v20, v21
	v_add3_u32 v21, s35, v52, v68
	ds_write_b32 v21, v20
	s_min_i32 s35, s31, 0xffffffd8
	s_add_i32 s35, s35, 44
	v_cvt_f32_i32_e32 v21, s35
	v_rcp_f32_e32 v20, v30
	s_nop 0
	v_pk_add_f32 v[14:15], v[18:19], v[14:15]
	v_readlane_b32 s35, v254, 41
	v_pk_fma_f32 v[18:19], v[20:21], v[14:15], v[24:25] op_sel_hi:[0,1,1] neg_lo:[0,0,1] neg_hi:[0,0,1]
	v_cvt_pk_bf16_f32 v18, v18, v19
	v_add3_u32 v19, s35, v53, v68
	ds_write_b32 v19, v18
	s_min_i32 s35, s31, 0xffffffd7
	s_add_i32 s35, s35, 45
	v_cvt_f32_i32_e32 v22, s35
	v_rcp_f32_e32 v18, v21
	s_nop 0
	v_readlane_b32 s35, v254, 43
	v_add3_u32 v53, s95, v53, v68
	s_waitcnt vmcnt(1)
	v_pk_add_f32 v[20:21], v[16:17], v[36:37] neg_lo:[0,1] neg_hi:[0,1]
	s_nop 0
	v_pk_add_f32 v[14:15], v[14:15], v[20:21]
	v_pk_fma_f32 v[18:19], v[18:19], v[14:15], v[16:17] op_sel_hi:[0,1,1] neg_lo:[0,0,1] neg_hi:[0,0,1]
	v_cvt_pk_bf16_f32 v18, v18, v19
	v_add3_u32 v19, s35, v54, v68
	ds_write_b32 v19, v18
	s_min_i32 s35, s31, 0xffffffd6
	s_add_i32 s35, s35, 46
	v_rcp_f32_e32 v18, v22
	s_nop 0
	v_cvt_f32_i32_e32 v22, s35
	s_waitcnt vmcnt(0)
	v_pk_add_f32 v[20:21], v[10:11], v[28:29] neg_lo:[0,1] neg_hi:[0,1]
	v_readlane_b32 s35, v254, 45
	v_pk_add_f32 v[14:15], v[14:15], v[20:21]
	v_pk_fma_f32 v[18:19], v[18:19], v[14:15], v[10:11] op_sel_hi:[0,1,1] neg_lo:[0,0,1] neg_hi:[0,0,1]
	v_cvt_pk_bf16_f32 v18, v18, v19
	v_add3_u32 v19, s35, v55, v68
	ds_write_b32 v19, v18
	s_min_i32 s35, s31, 0xffffffd5
	s_add_i32 s35, s35, 47
	v_rcp_f32_e32 v18, v22
	s_nop 0
	v_cvt_f32_i32_e32 v22, s35
	v_pk_add_f32 v[20:21], v[12:13], v[26:27] neg_lo:[0,1] neg_hi:[0,1]
	s_min_i32 s35, s31, 0xffffffd4
	v_pk_add_f32 v[14:15], v[14:15], v[20:21]
	v_pk_fma_f32 v[18:19], v[18:19], v[14:15], v[12:13] op_sel_hi:[0,1,1] neg_lo:[0,0,1] neg_hi:[0,0,1]
	v_cvt_pk_bf16_f32 v18, v18, v19
	v_add3_u32 v19, s12, v56, v68
	ds_write_b32 v19, v18
	s_add_i32 s35, s35, 48
	v_rcp_f32_e32 v18, v22
	s_nop 0
	v_cvt_f32_i32_e32 v22, s35
	v_pk_add_f32 v[20:21], v[6:7], v[24:25] neg_lo:[0,1] neg_hi:[0,1]
	v_readlane_b32 s12, v254, 49
	v_pk_add_f32 v[20:21], v[14:15], v[20:21]
	s_or_b32 s82, s80, 48
	s_ashr_i32 s83, s82, 31
	s_lshl_b64 s[82:83], s[82:83], 12
	v_lshl_add_u64 v[14:15], v[4:5], 0, s[82:83]
	global_load_dwordx2 v[14:15], v[14:15], off
	v_pk_fma_f32 v[18:19], v[18:19], v[20:21], v[6:7] op_sel_hi:[0,1,1] neg_lo:[0,0,1] neg_hi:[0,0,1]
	v_cvt_pk_bf16_f32 v18, v18, v19
	v_add3_u32 v19, s12, v57, v68
	ds_write_b32 v19, v18
	v_pk_add_f32 v[16:17], v[8:9], v[16:17] neg_lo:[0,1] neg_hi:[0,1]
	s_or_b32 s82, s80, 49
	v_rcp_f32_e32 v18, v22
	s_nop 0
	v_pk_add_f32 v[30:31], v[20:21], v[16:17]
	s_ashr_i32 s83, s82, 31
	v_pk_fma_f32 v[16:17], v[18:19], v[30:31], v[8:9] op_sel_hi:[0,1,1] neg_lo:[0,0,1] neg_hi:[0,0,1]
	s_lshl_b64 s[82:83], s[82:83], 12
	v_cvt_pk_bf16_f32 v18, v16, v17
	v_lshl_add_u64 v[16:17], v[4:5], 0, s[82:83]
	global_load_dwordx2 v[16:17], v[16:17], off
	s_or_b32 s82, s80, 50
	s_ashr_i32 s83, s82, 31
	s_lshl_b64 s[82:83], s[82:83], 12
	v_lshl_add_u64 v[32:33], v[4:5], 0, s[82:83]
	s_or_b32 s82, s80, 51
	s_ashr_i32 s83, s82, 31
	s_lshl_b64 s[82:83], s[82:83], 12
	v_lshl_add_u64 v[36:37], v[4:5], 0, s[82:83]
	s_or_b32 s82, s80, 52
	s_ashr_i32 s83, s82, 31
	s_lshl_b64 s[82:83], s[82:83], 12
	v_lshl_add_u64 v[28:29], v[4:5], 0, s[82:83]
	s_or_b32 s82, s80, 53
	s_ashr_i32 s83, s82, 31
	s_lshl_b64 s[82:83], s[82:83], 12
	v_lshl_add_u64 v[24:25], v[4:5], 0, s[82:83]
	s_or_b32 s82, s80, 54
	s_ashr_i32 s83, s82, 31
	s_lshl_b64 s[82:83], s[82:83], 12
	v_lshl_add_u64 v[22:23], v[4:5], 0, s[82:83]
	s_or_b32 s82, s80, 55
	s_ashr_i32 s83, s82, 31
	s_lshl_b64 s[82:83], s[82:83], 12
	v_lshl_add_u64 v[20:21], v[4:5], 0, s[82:83]
	s_or_b32 s82, s80, 56
	s_min_i32 s35, s31, 0xffffffd3
	v_readlane_b32 s12, v254, 51
	s_ashr_i32 s83, s82, 31
	s_add_i32 s35, s35, 49
	v_add3_u32 v19, s12, v69, v68
	s_lshl_b64 s[82:83], s[82:83], 12
	v_cvt_f32_i32_e32 v34, s35
	ds_write_b32 v19, v18
	v_lshl_add_u64 v[18:19], v[4:5], 0, s[82:83]
	s_or_b32 s82, s80, 57
	s_ashr_i32 s83, s82, 31
	s_lshl_b64 s[82:83], s[82:83], 12
	v_lshl_add_u64 v[26:27], v[4:5], 0, s[82:83]
	s_min_i32 s35, s31, 0xffffffd2
	s_add_i32 s35, s35, 50
	v_readlane_b32 s12, v254, 53
	v_rcp_f32_e32 v38, v34
	s_nop 0
	global_load_dwordx2 v[34:35], v[32:33], off
	s_nop 0
	global_load_dwordx2 v[32:33], v[36:37], off
	v_cvt_f32_i32_e32 v36, s35
	s_waitcnt vmcnt(3)
	v_pk_add_f32 v[10:11], v[14:15], v[10:11] neg_lo:[0,1] neg_hi:[0,1]
	s_min_i32 s35, s31, 0xffffffd1
	v_pk_add_f32 v[10:11], v[30:31], v[10:11]
	v_pk_fma_f32 v[30:31], v[38:39], v[10:11], v[14:15] op_sel_hi:[0,1,1] neg_lo:[0,0,1] neg_hi:[0,0,1]
	v_cvt_pk_bf16_f32 v30, v30, v31
	v_add3_u32 v31, s12, v47, v68
	ds_write_b32 v31, v30
	s_add_i32 s35, s35, 51
	v_rcp_f32_e32 v30, v36
	s_nop 0
	v_cvt_f32_i32_e32 v36, s35
	s_min_i32 s35, s31, 0xffffffd0
	s_waitcnt vmcnt(2)
	v_pk_add_f32 v[12:13], v[16:17], v[12:13] neg_lo:[0,1] neg_hi:[0,1]
	s_add_i32 s35, s35, 52
	v_pk_add_f32 v[10:11], v[10:11], v[12:13]
	v_cvt_f32_i32_e32 v38, s35
	v_pk_fma_f32 v[12:13], v[30:31], v[10:11], v[16:17] op_sel_hi:[0,1,1] neg_lo:[0,0,1] neg_hi:[0,0,1]
	v_cvt_pk_bf16_f32 v12, v12, v13
	v_add3_u32 v13, s24, v48, v68
	ds_write_b32 v13, v12
	s_min_i32 s35, s31, 0xffffffcf
	s_add_i32 s35, s35, 53
	v_cvt_f32_i32_e32 v41, s35
	s_min_i32 s35, s31, 0xffffffce
	s_add_i32 s35, s35, 54
	v_cvt_f32_i32_e32 v42, s35
	s_min_i32 s35, s31, 0xffffffcd
	s_add_i32 s35, s35, 55
	v_cvt_f32_i32_e32 v48, s35
	s_min_i32 s35, s31, 0xffffffcc
	s_add_i32 s35, s35, 56
	v_cvt_f32_i32_e32 v58, s35
	s_min_i32 s35, s31, 0xffffffcb
	s_add_i32 s35, s35, 57
	v_cvt_f32_i32_e32 v61, s35
	s_min_i32 s35, s31, 0xffffffca
	s_add_i32 s35, s35, 58
	v_cvt_f32_i32_e32 v62, s35
	s_min_i32 s35, s31, 0xffffffc9
	s_add_i32 s35, s35, 59
	v_cvt_f32_i32_e32 v65, s35
	s_min_i32 s35, s31, 0xffffffc8
	s_add_i32 s35, s35, 60
	v_cvt_f32_i32_e32 v66, s35
	s_min_i32 s35, s31, 0xffffffc7
	s_add_i32 s35, s35, 61
	v_cvt_f32_i32_e32 v71, s35
	s_min_i32 s35, s31, 0xffffffc6
	s_add_i32 s35, s35, 62
	v_cvt_f32_i32_e32 v72, s35
	s_min_i32 s35, s31, 0xffffffc5
	s_add_i32 s35, s35, 63
	global_load_dwordx2 v[12:13], v[28:29], off
	v_cvt_f32_i32_e32 v75, s35
	global_load_dwordx2 v[24:25], v[24:25], off
	global_load_dwordx2 v[26:27], v[26:27], off
	global_load_dwordx2 v[22:23], v[22:23], off
	s_or_b32 s82, s80, 58
	global_load_dwordx2 v[20:21], v[20:21], off
	global_load_dwordx2 v[18:19], v[18:19], off
	s_ashr_i32 s83, s82, 31
	s_lshl_b64 s[82:83], s[82:83], 12
	v_lshl_add_u64 v[28:29], v[4:5], 0, s[82:83]
	s_or_b32 s82, s80, 59
	s_ashr_i32 s83, s82, 31
	global_load_dwordx2 v[28:29], v[28:29], off
	s_lshl_b64 s[82:83], s[82:83], 12
	v_lshl_add_u64 v[30:31], v[4:5], 0, s[82:83]
	s_or_b32 s82, s80, 60
	s_ashr_i32 s83, s82, 31
	global_load_dwordx2 v[30:31], v[30:31], off
	s_lshl_b64 s[82:83], s[82:83], 12
	s_waitcnt vmcnt(9)
	v_pk_add_f32 v[6:7], v[34:35], v[6:7] neg_lo:[0,1] neg_hi:[0,1]
	v_rcp_f32_e32 v36, v36
	s_nop 0
	v_pk_add_f32 v[6:7], v[10:11], v[6:7]
	v_lshl_add_u64 v[10:11], v[4:5], 0, s[82:83]
	s_or_b32 s82, s80, 61
	s_ashr_i32 s83, s82, 31
	v_pk_fma_f32 v[36:37], v[36:37], v[6:7], v[34:35] op_sel_hi:[0,1,1] neg_lo:[0,0,1] neg_hi:[0,0,1]
	global_load_dwordx2 v[10:11], v[10:11], off
	s_lshl_b64 s[82:83], s[82:83], 12
	v_cvt_pk_bf16_f32 v36, v36, v37
	ds_write_b32 v3, v36
	v_lshl_add_u64 v[36:37], v[4:5], 0, s[82:83]
	s_or_b32 s82, s80, 62
	s_ashr_i32 s83, s82, 31
	global_load_dwordx2 v[36:37], v[36:37], off
	s_lshl_b64 s[82:83], s[82:83], 12
	s_waitcnt vmcnt(10)
	v_pk_add_f32 v[8:9], v[32:33], v[8:9] neg_lo:[0,1] neg_hi:[0,1]
	v_rcp_f32_e32 v38, v38
	s_nop 0
	v_pk_add_f32 v[6:7], v[6:7], v[8:9]
	v_lshl_add_u64 v[8:9], v[4:5], 0, s[82:83]
	s_or_b32 s82, s80, 63
	s_ashr_i32 s83, s82, 31
	global_load_dwordx2 v[8:9], v[8:9], off
	s_lshl_b64 s[82:83], s[82:83], 12
	v_lshl_add_u64 v[4:5], v[4:5], 0, s[82:83]
	global_load_dwordx2 v[4:5], v[4:5], off
	v_rcp_f32_e32 v40, v41
	s_nop 0
	v_add3_u32 v41, s27, v45, v68
	v_pk_fma_f32 v[38:39], v[38:39], v[6:7], v[32:33] op_sel_hi:[0,1,1] neg_lo:[0,0,1] neg_hi:[0,0,1]
	v_add3_u32 v3, s26, v44, v68
	v_cvt_pk_bf16_f32 v38, v38, v39
	ds_write_b32 v3, v38
	v_rcp_f32_e32 v42, v42
	s_nop 0
	v_add3_u32 v43, s77, v46, v68
	v_rcp_f32_e32 v44, v48
	s_nop 0
	v_add3_u32 v45, s91, v49, v68
	v_rcp_f32_e32 v46, v58
	s_nop 0
	v_add3_u32 v47, s94, v50, v68
	v_rcp_f32_e32 v48, v61
	s_nop 0
	v_add3_u32 v49, s33, v51, v68
	v_rcp_f32_e32 v50, v62
	s_nop 0
	v_add3_u32 v51, s75, v52, v68
	v_rcp_f32_e32 v52, v65
	s_nop 0
	v_rcp_f32_e32 v58, v66
	s_nop 0
	v_add3_u32 v59, s96, v54, v68
	v_rcp_f32_e32 v54, v71
	s_nop 0
	v_add3_u32 v55, s97, v55, v68
	s_waitcnt vmcnt(11)
	v_pk_add_f32 v[14:15], v[12:13], v[14:15] neg_lo:[0,1] neg_hi:[0,1]
	v_rcp_f32_e32 v60, v72
	s_nop 0
	v_pk_add_f32 v[6:7], v[6:7], v[14:15]
	v_add3_u32 v61, s36, v56, v68
	v_pk_fma_f32 v[14:15], v[40:41], v[6:7], v[12:13] op_sel_hi:[0,1,1] neg_lo:[0,0,1] neg_hi:[0,0,1]
	v_cvt_pk_bf16_f32 v3, v14, v15
	s_waitcnt vmcnt(10)
	v_pk_add_f32 v[14:15], v[24:25], v[16:17] neg_lo:[0,1] neg_hi:[0,1]
	ds_write_b32 v41, v3
	v_pk_add_f32 v[6:7], v[6:7], v[14:15]
	v_rcp_f32_e32 v56, v75
	s_nop 0
	v_pk_fma_f32 v[14:15], v[42:43], v[6:7], v[24:25] op_sel_hi:[0,1,1] neg_lo:[0,0,1] neg_hi:[0,0,1]
	v_cvt_pk_bf16_f32 v3, v14, v15
	s_waitcnt vmcnt(8)
	v_pk_add_f32 v[14:15], v[22:23], v[34:35] neg_lo:[0,1] neg_hi:[0,1]
	ds_write_b32 v43, v3
	v_pk_add_f32 v[6:7], v[6:7], v[14:15]
	s_waitcnt vmcnt(6)
	v_pk_add_f32 v[12:13], v[18:19], v[12:13] neg_lo:[0,1] neg_hi:[0,1]
	v_pk_fma_f32 v[14:15], v[44:45], v[6:7], v[22:23] op_sel_hi:[0,1,1] neg_lo:[0,0,1] neg_hi:[0,0,1]
	v_cvt_pk_bf16_f32 v3, v14, v15
	v_pk_add_f32 v[14:15], v[20:21], v[32:33] neg_lo:[0,1] neg_hi:[0,1]
	ds_write_b32 v45, v3
	v_pk_add_f32 v[6:7], v[6:7], v[14:15]
	v_add3_u32 v57, s37, v57, v68
	v_pk_fma_f32 v[14:15], v[46:47], v[6:7], v[20:21] op_sel_hi:[0,1,1] neg_lo:[0,0,1] neg_hi:[0,0,1]
	v_pk_add_f32 v[6:7], v[6:7], v[12:13]
	v_cvt_pk_bf16_f32 v3, v14, v15
	v_pk_fma_f32 v[12:13], v[48:49], v[6:7], v[18:19] op_sel_hi:[0,1,1] neg_lo:[0,0,1] neg_hi:[0,0,1]
	ds_write_b32 v47, v3
	v_cvt_pk_bf16_f32 v3, v12, v13
	v_pk_add_f32 v[12:13], v[26:27], v[24:25] neg_lo:[0,1] neg_hi:[0,1]
	ds_write_b32 v49, v3
	v_pk_add_f32 v[6:7], v[6:7], v[12:13]
	s_min_i32 s35, s31, 0xffffffc4
	v_pk_fma_f32 v[12:13], v[50:51], v[6:7], v[26:27] op_sel_hi:[0,1,1] neg_lo:[0,0,1] neg_hi:[0,0,1]
	v_cvt_pk_bf16_f32 v3, v12, v13
	s_waitcnt vmcnt(5)
	v_pk_add_f32 v[12:13], v[28:29], v[22:23] neg_lo:[0,1] neg_hi:[0,1]
	ds_write_b32 v51, v3
	v_pk_add_f32 v[6:7], v[6:7], v[12:13]
	s_nop 0
	v_pk_fma_f32 v[12:13], v[52:53], v[6:7], v[28:29] op_sel_hi:[0,1,1] neg_lo:[0,0,1] neg_hi:[0,0,1]
	v_cvt_pk_bf16_f32 v3, v12, v13
	s_waitcnt vmcnt(4)
	v_pk_add_f32 v[12:13], v[30:31], v[20:21] neg_lo:[0,1] neg_hi:[0,1]
	ds_write_b32 v53, v3
	v_pk_add_f32 v[6:7], v[6:7], v[12:13]
	s_nop 0
	v_pk_fma_f32 v[12:13], v[58:59], v[6:7], v[30:31] op_sel_hi:[0,1,1] neg_lo:[0,0,1] neg_hi:[0,0,1]
	v_cvt_pk_bf16_f32 v3, v12, v13
	s_waitcnt vmcnt(3)
	v_pk_add_f32 v[12:13], v[10:11], v[18:19] neg_lo:[0,1] neg_hi:[0,1]
	ds_write_b32 v59, v3
	v_pk_add_f32 v[6:7], v[6:7], v[12:13]
	s_nop 0
	v_pk_fma_f32 v[10:11], v[54:55], v[6:7], v[10:11] op_sel_hi:[0,1,1] neg_lo:[0,0,1] neg_hi:[0,0,1]
	v_cvt_pk_bf16_f32 v3, v10, v11
	s_waitcnt vmcnt(2)
	v_pk_add_f32 v[10:11], v[36:37], v[26:27] neg_lo:[0,1] neg_hi:[0,1]
	ds_write_b32 v55, v3
	v_pk_add_f32 v[6:7], v[6:7], v[10:11]
	s_nop 0
	v_pk_fma_f32 v[10:11], v[60:61], v[6:7], v[36:37] op_sel_hi:[0,1,1] neg_lo:[0,0,1] neg_hi:[0,0,1]
	v_cvt_pk_bf16_f32 v3, v10, v11
	s_waitcnt vmcnt(1)
	v_pk_add_f32 v[10:11], v[8:9], v[28:29] neg_lo:[0,1] neg_hi:[0,1]
	ds_write_b32 v61, v3
	v_pk_add_f32 v[6:7], v[6:7], v[10:11]
	s_nop 0
	v_pk_fma_f32 v[8:9], v[56:57], v[6:7], v[8:9] op_sel_hi:[0,1,1] neg_lo:[0,0,1] neg_hi:[0,0,1]
	v_cvt_pk_bf16_f32 v3, v8, v9
	s_waitcnt vmcnt(0)
	v_pk_add_f32 v[8:9], v[4:5], v[30:31] neg_lo:[0,1] neg_hi:[0,1]
	ds_write_b32 v57, v3
	v_pk_add_f32 v[6:7], v[6:7], v[8:9]
	v_mov_b32_e32 v3, s35

.LBB0_112:
	s_ashr_i32 s81, s80, 31
	v_lshl_add_u64 v[4:5], v[2:3], 2, s[70:71]
	s_lshl_b64 s[8:9], s[80:81], 12
	v_lshl_add_u64 v[6:7], v[4:5], 0, s[8:9]
	global_load_dwordx2 v[6:7], v[6:7], off
	s_or_b32 s8, s80, 1
	s_ashr_i32 s9, s8, 31
	s_lshl_b64 s[8:9], s[8:9], 12
	v_lshl_add_u64 v[8:9], v[4:5], 0, s[8:9]
	global_load_dwordx2 v[8:9], v[8:9], off
	s_or_b32 s8, s80, 2
	s_ashr_i32 s9, s8, 31
	s_lshl_b64 s[8:9], s[8:9], 12
	v_lshl_add_u64 v[10:11], v[4:5], 0, s[8:9]
	global_load_dwordx2 v[10:11], v[10:11], off
	s_or_b32 s8, s80, 3
	s_ashr_i32 s9, s8, 31
	s_lshl_b64 s[8:9], s[8:9], 12
	v_lshl_add_u64 v[14:15], v[4:5], 0, s[8:9]
	s_or_b32 s8, s80, 4
	s_ashr_i32 s9, s8, 31
	s_lshl_b64 s[8:9], s[8:9], 12
	v_lshl_add_u64 v[70:71], v[4:5], 0, s[8:9]
	s_or_b32 s8, s80, 5
	s_ashr_i32 s9, s8, 31
	s_lshl_b64 s[8:9], s[8:9], 12
	v_lshl_add_u64 v[72:73], v[4:5], 0, s[8:9]
	s_or_b32 s8, s80, 6
	s_ashr_i32 s9, s8, 31
	global_load_dwordx2 v[14:15], v[14:15], off
	s_lshl_b64 s[8:9], s[8:9], 12
	v_lshl_add_u64 v[64:65], v[4:5], 0, s[8:9]
	s_or_b32 s8, s80, 7
	s_ashr_i32 s9, s8, 31
	s_lshl_b64 s[8:9], s[8:9], 12
	v_lshl_add_u64 v[62:63], v[4:5], 0, s[8:9]
	s_or_b32 s8, s80, 8
	s_ashr_i32 s9, s8, 31
	s_lshl_b64 s[8:9], s[8:9], 12
	v_lshl_add_u64 v[60:61], v[4:5], 0, s[8:9]
	s_or_b32 s8, s80, 9
	s_ashr_i32 s9, s8, 31
	s_lshl_b64 s[8:9], s[8:9], 12
	v_lshl_add_u64 v[58:59], v[4:5], 0, s[8:9]
	s_or_b32 s8, s80, 10
	s_ashr_i32 s9, s8, 31
	s_lshl_b64 s[8:9], s[8:9], 12
	s_min_i32 s10, s31, 15
	v_lshl_add_u64 v[56:57], v[4:5], 0, s[8:9]
	s_or_b32 s8, s80, 11
	s_add_i32 s10, s10, 1
	s_ashr_i32 s9, s8, 31
	v_cvt_f32_i32_e32 v3, s10
	s_lshl_b64 s[8:9], s[8:9], 12
	v_lshl_add_u64 v[54:55], v[4:5], 0, s[8:9]
	s_or_b32 s8, s80, 12
	s_ashr_i32 s9, s8, 31
	s_lshl_b64 s[8:9], s[8:9], 12
	v_lshl_add_u64 v[52:53], v[4:5], 0, s[8:9]
	s_or_b32 s8, s80, 13
	s_ashr_i32 s9, s8, 31
	s_lshl_b64 s[8:9], s[8:9], 12
	v_lshl_add_u64 v[50:51], v[4:5], 0, s[8:9]
	s_or_b32 s8, s80, 14
	s_ashr_i32 s9, s8, 31
	s_lshl_b64 s[8:9], s[8:9], 12
	v_lshl_add_u64 v[48:49], v[4:5], 0, s[8:9]
	s_or_b32 s8, s80, 15
	s_ashr_i32 s9, s8, 31
	s_lshl_b64 s[8:9], s[8:9], 12
	v_lshl_add_u64 v[46:47], v[4:5], 0, s[8:9]
	s_min_i32 s8, s31, 14
	s_add_i32 s8, s8, 2
	v_rcp_f32_e32 v74, v3
	s_nop 0
	v_cvt_f32_i32_e32 v67, s8
	s_waitcnt vmcnt(3)
	v_pk_add_f32 v[76:77], v[16:17], v[6:7]
	v_lshlrev_b32_e32 v66, 2, v221
	v_pk_fma_f32 v[16:17], v[74:75], v[76:77], v[6:7] op_sel_hi:[0,1,1] neg_lo:[0,0,1] neg_hi:[0,0,1]
	v_and_b32_e32 v68, 12, v66
	v_and_b32_e32 v3, -16, v66
	v_cvt_pk_bf16_f32 v16, v16, v17
	v_add3_u32 v85, 0, v3, v68
	ds_write_b32 v85, v16
	global_load_dwordx2 v[16:17], v[70:71], off
	s_min_i32 s8, s31, 13
	s_add_i32 s8, s8, 3
	v_rcp_f32_e32 v70, v67
	s_nop 0
	v_cvt_f32_i32_e32 v67, s8
	s_waitcnt vmcnt(3)
	v_pk_add_f32 v[18:19], v[8:9], v[18:19] neg_lo:[0,1] neg_hi:[0,1]
	s_waitcnt vmcnt(2)
	v_pk_add_f32 v[20:21], v[10:11], v[20:21] neg_lo:[0,1] neg_hi:[0,1]
	v_pk_add_f32 v[74:75], v[76:77], v[18:19]
	v_pk_fma_f32 v[18:19], v[70:71], v[74:75], v[8:9] op_sel_hi:[0,1,1] neg_lo:[0,0,1] neg_hi:[0,0,1]
	v_bitop3_b32 v70, v66, 16, -16 bitop3:0x6c
	v_cvt_pk_bf16_f32 v18, v18, v19
	v_add3_u32 v86, 0, v70, v68
	ds_write_b32 v86, v18 offset:2048
	global_load_dwordx2 v[18:19], v[72:73], off
	s_min_i32 s8, s31, 12
	s_add_i32 s8, s8, 4
	v_rcp_f32_e32 v72, v67
	s_nop 0
	v_cvt_f32_i32_e32 v67, s8
	v_pk_add_f32 v[74:75], v[74:75], v[20:21]
	v_bitop3_b32 v71, v66, 32, -16 bitop3:0x6c
	v_pk_fma_f32 v[20:21], v[72:73], v[74:75], v[10:11] op_sel_hi:[0,1,1] neg_lo:[0,0,1] neg_hi:[0,0,1]
	v_cvt_pk_bf16_f32 v20, v20, v21
	v_add3_u32 v87, 0, v71, v68
	ds_write_b32 v87, v20 offset:4096
	s_min_i32 s8, s31, 11
	global_load_dwordx2 v[20:21], v[64:65], off
	s_add_i32 s8, s8, 5
	v_cvt_f32_i32_e32 v65, s8
	s_waitcnt vmcnt(3)
	v_pk_add_f32 v[24:25], v[14:15], v[24:25] neg_lo:[0,1] neg_hi:[0,1]
	v_rcp_f32_e32 v64, v67
	s_nop 0
	v_pk_add_f32 v[74:75], v[74:75], v[24:25]
	v_bitop3_b32 v72, v66, 48, -16 bitop3:0x6c
	v_pk_fma_f32 v[24:25], v[64:65], v[74:75], v[14:15] op_sel_hi:[0,1,1] neg_lo:[0,0,1] neg_hi:[0,0,1]
	v_cvt_pk_bf16_f32 v24, v24, v25
	v_add3_u32 v88, 0, v72, v68
	ds_write_b32 v88, v24 offset:6144
	global_load_dwordx2 v[24:25], v[62:63], off
	s_min_i32 s8, s31, 10
	s_add_i32 s8, s8, 6
	v_cvt_f32_i32_e32 v63, s8
	v_rcp_f32_e32 v62, v65
	s_nop 0
	v_bitop3_b32 v73, v66, 64, -16 bitop3:0x6c
	s_waitcnt vmcnt(3)
	v_pk_add_f32 v[28:29], v[16:17], v[28:29] neg_lo:[0,1] neg_hi:[0,1]
	v_add3_u32 v89, 0, v73, v68
	v_pk_add_f32 v[64:65], v[74:75], v[28:29]
	v_pk_fma_f32 v[28:29], v[62:63], v[64:65], v[16:17] op_sel_hi:[0,1,1] neg_lo:[0,0,1] neg_hi:[0,0,1]
	v_cvt_pk_bf16_f32 v28, v28, v29
	ds_write_b32 v89, v28 offset:8192
	s_min_i32 s8, s31, 9
	global_load_dwordx2 v[28:29], v[60:61], off
	s_add_i32 s8, s8, 7
	v_cvt_f32_i32_e32 v61, s8
	v_rcp_f32_e32 v60, v63
	s_nop 0
	s_min_i32 s10, s31, -1
	s_add_i32 s10, s10, 17
	s_waitcnt vmcnt(3)
	v_pk_add_f32 v[34:35], v[18:19], v[34:35] neg_lo:[0,1] neg_hi:[0,1]
	s_waitcnt vmcnt(2)
	v_pk_add_f32 v[36:37], v[20:21], v[36:37] neg_lo:[0,1] neg_hi:[0,1]
	v_pk_add_f32 v[62:63], v[64:65], v[34:35]
	v_pk_fma_f32 v[34:35], v[60:61], v[62:63], v[18:19] op_sel_hi:[0,1,1] neg_lo:[0,0,1] neg_hi:[0,0,1]
	s_movk_i32 s8, 0x50
	v_bitop3_b32 v74, v66, s8, -16 bitop3:0x6c
	v_cvt_pk_bf16_f32 v34, v34, v35
	v_add3_u32 v90, 0, v74, v68
	ds_write_b32 v90, v34 offset:10240
	global_load_dwordx2 v[34:35], v[58:59], off
	s_min_i32 s8, s31, 8
	s_add_i32 s8, s8, 8
	v_cvt_f32_i32_e32 v59, s8
	v_rcp_f32_e32 v58, v61
	s_nop 0
	v_pk_add_f32 v[60:61], v[62:63], v[36:37]
	v_pk_fma_f32 v[36:37], v[58:59], v[60:61], v[20:21] op_sel_hi:[0,1,1] neg_lo:[0,0,1] neg_hi:[0,0,1]
	s_movk_i32 s8, 0x60
	v_bitop3_b32 v75, v66, s8, -16 bitop3:0x6c
	v_cvt_pk_bf16_f32 v36, v36, v37
	v_add3_u32 v91, 0, v75, v68
	ds_write_b32 v91, v36 offset:12288
	s_min_i32 s8, s31, 7
	global_load_dwordx2 v[36:37], v[56:57], off
	s_add_i32 s8, s8, 9
	v_cvt_f32_i32_e32 v57, s8
	s_waitcnt vmcnt(3)
	v_pk_add_f32 v[38:39], v[24:25], v[38:39] neg_lo:[0,1] neg_hi:[0,1]
	v_rcp_f32_e32 v56, v59
	s_nop 0
	v_pk_add_f32 v[58:59], v[60:61], v[38:39]
	v_pk_fma_f32 v[38:39], v[56:57], v[58:59], v[24:25] op_sel_hi:[0,1,1] neg_lo:[0,0,1] neg_hi:[0,0,1]
	s_movk_i32 s8, 0x70
	v_bitop3_b32 v76, v66, s8, -16 bitop3:0x6c
	v_cvt_pk_bf16_f32 v38, v38, v39
	v_add3_u32 v92, 0, v76, v68
	ds_write_b32 v92, v38 offset:14336
	global_load_dwordx2 v[38:39], v[54:55], off
	s_min_i32 s8, s31, 6
	s_add_i32 s8, s8, 10
	v_cvt_f32_i32_e32 v55, s8
	s_waitcnt vmcnt(3)
	v_pk_add_f32 v[40:41], v[28:29], v[40:41] neg_lo:[0,1] neg_hi:[0,1]
	v_rcp_f32_e32 v54, v57
	s_nop 0
	v_pk_add_f32 v[56:57], v[58:59], v[40:41]
	v_pk_fma_f32 v[40:41], v[54:55], v[56:57], v[28:29] op_sel_hi:[0,1,1] neg_lo:[0,0,1] neg_hi:[0,0,1]
	s_movk_i32 s8, 0x80
	v_bitop3_b32 v77, v66, s8, -16 bitop3:0x6c
	v_cvt_pk_bf16_f32 v40, v40, v41
	v_add3_u32 v93, 0, v77, v68
	ds_write_b32 v93, v40 offset:16384
	global_load_dwordx2 v[40:41], v[52:53], off
	s_min_i32 s8, s31, 5
	s_add_i32 s8, s8, 11
	v_cvt_f32_i32_e32 v53, s8
	s_waitcnt vmcnt(3)
	v_pk_add_f32 v[42:43], v[34:35], v[42:43] neg_lo:[0,1] neg_hi:[0,1]
	v_rcp_f32_e32 v52, v55
	s_nop 0
	v_pk_add_f32 v[54:55], v[56:57], v[42:43]
	v_pk_fma_f32 v[42:43], v[52:53], v[54:55], v[34:35] op_sel_hi:[0,1,1] neg_lo:[0,0,1] neg_hi:[0,0,1]
	s_movk_i32 s8, 0x90
	v_bitop3_b32 v78, v66, s8, -16 bitop3:0x6c
	v_cvt_pk_bf16_f32 v42, v42, v43
	v_add3_u32 v94, 0, v78, v68
	ds_write_b32 v94, v42 offset:18432
	global_load_dwordx2 v[42:43], v[50:51], off
	s_min_i32 s8, s31, 4
	s_add_i32 s8, s8, 12
	v_cvt_f32_i32_e32 v51, s8
	s_waitcnt vmcnt(3)
	v_pk_add_f32 v[44:45], v[36:37], v[44:45] neg_lo:[0,1] neg_hi:[0,1]
	v_rcp_f32_e32 v50, v53
	s_nop 0
	v_pk_add_f32 v[52:53], v[54:55], v[44:45]
	v_pk_fma_f32 v[44:45], v[50:51], v[52:53], v[36:37] op_sel_hi:[0,1,1] neg_lo:[0,0,1] neg_hi:[0,0,1]
	s_movk_i32 s8, 0xa0
	v_bitop3_b32 v79, v66, s8, -16 bitop3:0x6c
	v_cvt_pk_bf16_f32 v44, v44, v45
	v_add3_u32 v95, 0, v79, v68
	ds_write_b32 v95, v44 offset:20480
	global_load_dwordx2 v[44:45], v[48:49], off
	s_min_i32 s8, s31, 3
	s_add_i32 s8, s8, 13
	v_cvt_f32_i32_e32 v49, s8
	s_waitcnt vmcnt(3)
	v_pk_add_f32 v[32:33], v[38:39], v[32:33] neg_lo:[0,1] neg_hi:[0,1]
	v_rcp_f32_e32 v48, v51
	s_nop 0
	v_pk_add_f32 v[50:51], v[52:53], v[32:33]
	v_pk_fma_f32 v[32:33], v[48:49], v[50:51], v[38:39] op_sel_hi:[0,1,1] neg_lo:[0,0,1] neg_hi:[0,0,1]
	s_movk_i32 s8, 0xb0
	v_bitop3_b32 v80, v66, s8, -16 bitop3:0x6c
	v_cvt_pk_bf16_f32 v32, v32, v33
	v_add3_u32 v96, 0, v80, v68
	ds_write_b32 v96, v32 offset:22528
	global_load_dwordx2 v[32:33], v[46:47], off
	s_min_i32 s8, s31, 2
	s_add_i32 s8, s8, 14
	v_cvt_f32_i32_e32 v48, s8
	s_waitcnt vmcnt(3)
	v_pk_add_f32 v[30:31], v[40:41], v[30:31] neg_lo:[0,1] neg_hi:[0,1]
	v_rcp_f32_e32 v46, v49
	s_nop 0
	v_pk_add_f32 v[30:31], v[50:51], v[30:31]
	s_waitcnt vmcnt(2)
	v_pk_add_f32 v[26:27], v[42:43], v[26:27] neg_lo:[0,1] neg_hi:[0,1]
	v_pk_fma_f32 v[46:47], v[46:47], v[30:31], v[40:41] op_sel_hi:[0,1,1] neg_lo:[0,0,1] neg_hi:[0,0,1]
	v_cvt_pk_bf16_f32 v46, v46, v47
	s_movk_i32 s8, 0xc0
	v_bitop3_b32 v81, v66, s8, -16 bitop3:0x6c
	v_add3_u32 v97, 0, v81, v68
	ds_write_b32 v97, v46 offset:24576
	s_min_i32 s8, s31, 1
	s_add_i32 s8, s8, 15
	v_cvt_f32_i32_e32 v47, s8
	v_rcp_f32_e32 v46, v48
	s_nop 0
	v_pk_add_f32 v[26:27], v[30:31], v[26:27]
	s_waitcnt vmcnt(1)
	v_pk_add_f32 v[22:23], v[44:45], v[22:23] neg_lo:[0,1] neg_hi:[0,1]
	v_pk_fma_f32 v[30:31], v[46:47], v[26:27], v[42:43] op_sel_hi:[0,1,1] neg_lo:[0,0,1] neg_hi:[0,0,1]
	v_cvt_pk_bf16_f32 v30, v30, v31
	s_movk_i32 s8, 0xd0
	v_bitop3_b32 v82, v66, s8, -16 bitop3:0x6c
	v_add3_u32 v98, 0, v82, v68
	ds_write_b32 v98, v30 offset:26624
	s_min_i32 s8, s31, 0
	s_or_b32 s8, s8, 16
	v_cvt_f32_i32_e32 v31, s8
	v_rcp_f32_e32 v30, v47
	s_nop 0
	v_pk_add_f32 v[22:23], v[26:27], v[22:23]
	s_waitcnt vmcnt(0)
	v_pk_add_f32 v[12:13], v[32:33], v[12:13] neg_lo:[0,1] neg_hi:[0,1]
	v_pk_fma_f32 v[26:27], v[30:31], v[22:23], v[44:45] op_sel_hi:[0,1,1] neg_lo:[0,0,1] neg_hi:[0,0,1]
	v_cvt_pk_bf16_f32 v26, v26, v27
	s_movk_i32 s8, 0xe0
	v_bitop3_b32 v83, v66, s8, -16 bitop3:0x6c
	v_add3_u32 v99, 0, v83, v68
	ds_write_b32 v99, v26 offset:28672
	s_movk_i32 s8, 0xf0
	v_rcp_f32_e32 v30, v31
	s_nop 0
	v_pk_add_f32 v[26:27], v[22:23], v[12:13]
	v_bitop3_b32 v69, v66, s8, -16 bitop3:0x6c
	s_or_b32 s8, s80, 16
	v_pk_fma_f32 v[12:13], v[30:31], v[26:27], v[32:33] op_sel_hi:[0,1,1] neg_lo:[0,0,1] neg_hi:[0,0,1]
	s_ashr_i32 s9, s8, 31
	v_cvt_pk_bf16_f32 v12, v12, v13
	v_add3_u32 v84, 0, v69, v68
	s_lshl_b64 s[8:9], s[8:9], 12
	ds_write_b32 v84, v12 offset:30720
	v_lshl_add_u64 v[12:13], v[4:5], 0, s[8:9]
	global_load_dwordx2 v[56:57], v[12:13], off
	s_or_b32 s8, s80, 17
	s_ashr_i32 s9, s8, 31
	s_lshl_b64 s[8:9], s[8:9], 12
	v_lshl_add_u64 v[22:23], v[4:5], 0, s[8:9]
	global_load_dwordx2 v[54:55], v[22:23], off
	s_or_b32 s8, s80, 18
	s_ashr_i32 s9, s8, 31
	s_lshl_b64 s[8:9], s[8:9], 12
	v_lshl_add_u64 v[30:31], v[4:5], 0, s[8:9]
	global_load_dwordx2 v[52:53], v[30:31], off
	s_or_b32 s8, s80, 19
	s_ashr_i32 s9, s8, 31
	s_lshl_b64 s[8:9], s[8:9], 12
	v_lshl_add_u64 v[58:59], v[4:5], 0, s[8:9]
	s_or_b32 s8, s80, 20
	s_ashr_i32 s9, s8, 31
	s_lshl_b64 s[8:9], s[8:9], 12
	v_lshl_add_u64 v[100:101], v[4:5], 0, s[8:9]
	s_or_b32 s8, s80, 21
	s_ashr_i32 s9, s8, 31
	s_lshl_b64 s[8:9], s[8:9], 12
	v_lshl_add_u64 v[102:103], v[4:5], 0, s[8:9]
	s_or_b32 s8, s80, 22
	s_ashr_i32 s9, s8, 31
	global_load_dwordx2 v[58:59], v[58:59], off
	s_lshl_b64 s[8:9], s[8:9], 12
	v_lshl_add_u64 v[104:105], v[4:5], 0, s[8:9]
	s_or_b32 s8, s80, 23
	s_ashr_i32 s9, s8, 31
	s_lshl_b64 s[8:9], s[8:9], 12
	v_lshl_add_u64 v[66:67], v[4:5], 0, s[8:9]
	s_or_b32 s8, s80, 24
	s_ashr_i32 s9, s8, 31
	s_lshl_b64 s[8:9], s[8:9], 12
	v_lshl_add_u64 v[64:65], v[4:5], 0, s[8:9]
	s_or_b32 s8, s80, 25
	s_ashr_i32 s9, s8, 31
	s_lshl_b64 s[8:9], s[8:9], 12
	v_lshl_add_u64 v[12:13], v[4:5], 0, s[8:9]
	s_or_b32 s8, s80, 26
	s_ashr_i32 s9, s8, 31
	s_lshl_b64 s[8:9], s[8:9], 12
	v_lshl_add_u64 v[62:63], v[4:5], 0, s[8:9]
	s_or_b32 s8, s80, 27
	s_ashr_i32 s9, s8, 31
	v_cvt_f32_i32_e32 v30, s10
	s_lshl_b64 s[8:9], s[8:9], 12
	v_lshl_add_u64 v[60:61], v[4:5], 0, s[8:9]
	s_or_b32 s8, s80, 28
	s_ashr_i32 s9, s8, 31
	s_lshl_b64 s[8:9], s[8:9], 12
	v_lshl_add_u64 v[22:23], v[4:5], 0, s[8:9]
	s_or_b32 s8, s80, 29
	s_ashr_i32 s9, s8, 31
	s_lshl_b64 s[8:9], s[8:9], 12
	v_lshl_add_u64 v[50:51], v[4:5], 0, s[8:9]
	s_or_b32 s8, s80, 30
	s_ashr_i32 s9, s8, 31
	s_lshl_b64 s[8:9], s[8:9], 12
	v_lshl_add_u64 v[48:49], v[4:5], 0, s[8:9]
	s_or_b32 s8, s80, 31
	s_ashr_i32 s9, s8, 31
	s_lshl_b64 s[8:9], s[8:9], 12
	v_lshl_add_u64 v[46:47], v[4:5], 0, s[8:9]
	s_min_i32 s8, s31, -2
	s_add_i32 s8, s8, 18
	v_rcp_f32_e32 v30, v30
	s_nop 0
	v_cvt_f32_i32_e32 v31, s8
	s_waitcnt vmcnt(3)
	v_pk_add_f32 v[6:7], v[56:57], v[6:7] neg_lo:[0,1] neg_hi:[0,1]
	global_load_dwordx2 v[12:13], v[12:13], off
	v_pk_add_f32 v[6:7], v[26:27], v[6:7]
	v_pk_fma_f32 v[26:27], v[30:31], v[6:7], v[56:57] op_sel_hi:[0,1,1] neg_lo:[0,0,1] neg_hi:[0,0,1]
	v_cvt_pk_bf16_f32 v26, v26, v27
	ds_write_b32 v85, v26 offset:32768
	global_load_dwordx2 v[26:27], v[100:101], off
	s_min_i32 s8, s31, -3
	s_add_i32 s8, s8, 19
	v_cvt_f32_i32_e32 v85, s8
	s_waitcnt vmcnt(4)
	v_pk_add_f32 v[8:9], v[54:55], v[8:9] neg_lo:[0,1] neg_hi:[0,1]
	v_rcp_f32_e32 v30, v31
	s_nop 0
	v_pk_add_f32 v[6:7], v[6:7], v[8:9]
	v_pk_fma_f32 v[8:9], v[30:31], v[6:7], v[54:55] op_sel_hi:[0,1,1] neg_lo:[0,0,1] neg_hi:[0,0,1]
	v_cvt_pk_bf16_f32 v8, v8, v9
	ds_write_b32 v86, v8 offset:34816
	global_load_dwordx2 v[30:31], v[102:103], off
	s_min_i32 s8, s31, -4
	s_add_i32 s8, s8, 20
	v_cvt_f32_i32_e32 v9, s8
	v_rcp_f32_e32 v8, v85
	s_nop 0
	s_waitcnt vmcnt(4)
	v_pk_add_f32 v[10:11], v[52:53], v[10:11] neg_lo:[0,1] neg_hi:[0,1]
	global_load_dwordx2 v[22:23], v[22:23], off
	v_pk_add_f32 v[10:11], v[6:7], v[10:11]
	s_min_i32 s8, s31, -5
	v_pk_fma_f32 v[6:7], v[8:9], v[10:11], v[52:53] op_sel_hi:[0,1,1] neg_lo:[0,0,1] neg_hi:[0,0,1]
	v_cvt_pk_bf16_f32 v6, v6, v7
	ds_write_b32 v87, v6 offset:36864
	global_load_dwordx2 v[6:7], v[104:105], off
	s_add_i32 s8, s8, 21
	v_cvt_f32_i32_e32 v85, s8
	s_waitcnt vmcnt(5)
	v_pk_add_f32 v[14:15], v[58:59], v[14:15] neg_lo:[0,1] neg_hi:[0,1]
	v_pk_add_f32 v[10:11], v[10:11], v[14:15]
	v_rcp_f32_e32 v8, v9
	s_nop 0
	v_pk_fma_f32 v[8:9], v[8:9], v[10:11], v[58:59] op_sel_hi:[0,1,1] neg_lo:[0,0,1] neg_hi:[0,0,1]
	v_cvt_pk_bf16_f32 v8, v8, v9
	ds_write_b32 v88, v8 offset:38912
	global_load_dwordx2 v[8:9], v[66:67], off
	s_min_i32 s8, s31, -6
	s_add_i32 s8, s8, 22
	v_cvt_f32_i32_e32 v15, s8
	v_rcp_f32_e32 v14, v85
	s_nop 0
	s_min_i32 s10, s31, 0xffffffef
	s_add_i32 s10, s10, 33
	s_waitcnt vmcnt(4)
	v_pk_add_f32 v[16:17], v[26:27], v[16:17] neg_lo:[0,1] neg_hi:[0,1]
	v_pk_add_f32 v[16:17], v[10:11], v[16:17]
	s_min_i32 s8, s31, -7
	v_pk_fma_f32 v[10:11], v[14:15], v[16:17], v[26:27] op_sel_hi:[0,1,1] neg_lo:[0,0,1] neg_hi:[0,0,1]
	v_cvt_pk_bf16_f32 v10, v10, v11
	ds_write_b32 v89, v10 offset:40960
	global_load_dwordx2 v[10:11], v[64:65], off
	s_add_i32 s8, s8, 23
	v_cvt_f32_i32_e32 v64, s8
	s_waitcnt vmcnt(4)
	v_pk_add_f32 v[18:19], v[30:31], v[18:19] neg_lo:[0,1] neg_hi:[0,1]
	v_rcp_f32_e32 v14, v15
	s_nop 0
	v_pk_add_f32 v[16:17], v[16:17], v[18:19]
	v_pk_fma_f32 v[14:15], v[14:15], v[16:17], v[30:31] op_sel_hi:[0,1,1] neg_lo:[0,0,1] neg_hi:[0,0,1]
	v_cvt_pk_bf16_f32 v14, v14, v15
	ds_write_b32 v90, v14 offset:43008
	s_min_i32 s8, s31, -8
	s_add_i32 s8, s8, 24
	v_rcp_f32_e32 v14, v64
	s_nop 0
	v_cvt_f32_i32_e32 v64, s8
	v_cvt_f32_i32_e32 v66, s10
	s_min_i32 s10, s31, 0xffffffee
	s_waitcnt vmcnt(2)
	v_pk_add_f32 v[18:19], v[6:7], v[20:21] neg_lo:[0,1] neg_hi:[0,1]
	v_pk_add_f32 v[16:17], v[16:17], v[18:19]
	v_pk_fma_f32 v[14:15], v[14:15], v[16:17], v[6:7] op_sel_hi:[0,1,1] neg_lo:[0,0,1] neg_hi:[0,0,1]
	v_cvt_pk_bf16_f32 v14, v14, v15
	ds_write_b32 v91, v14 offset:45056
	global_load_dwordx2 v[14:15], v[62:63], off
	s_min_i32 s8, s31, -9
	s_add_i32 s8, s8, 25
	v_cvt_f32_i32_e32 v19, s8
	s_waitcnt vmcnt(2)
	v_pk_add_f32 v[20:21], v[8:9], v[24:25] neg_lo:[0,1] neg_hi:[0,1]
	v_rcp_f32_e32 v18, v64
	s_nop 0
	v_pk_add_f32 v[20:21], v[16:17], v[20:21]
	v_pk_fma_f32 v[16:17], v[18:19], v[20:21], v[8:9] op_sel_hi:[0,1,1] neg_lo:[0,0,1] neg_hi:[0,0,1]
	v_cvt_pk_bf16_f32 v16, v16, v17
	ds_write_b32 v92, v16 offset:47104
	global_load_dwordx2 v[16:17], v[60:61], off
	s_min_i32 s8, s31, -10
	s_add_i32 s8, s8, 26
	v_cvt_f32_i32_e32 v60, s8
	v_rcp_f32_e32 v18, v19
	s_nop 0
	s_add_i32 s10, s10, 34
	s_waitcnt vmcnt(2)
	v_pk_add_f32 v[24:25], v[10:11], v[28:29] neg_lo:[0,1] neg_hi:[0,1]
	s_nop 0
	v_pk_add_f32 v[20:21], v[20:21], v[24:25]
	v_pk_fma_f32 v[18:19], v[18:19], v[20:21], v[10:11] op_sel_hi:[0,1,1] neg_lo:[0,0,1] neg_hi:[0,0,1]
	v_cvt_pk_bf16_f32 v18, v18, v19
	ds_write_b32 v93, v18 offset:49152
	s_min_i32 s8, s31, -11
	s_add_i32 s8, s8, 27
	v_cvt_f32_i32_e32 v28, s8
	v_pk_add_f32 v[24:25], v[12:13], v[34:35] neg_lo:[0,1] neg_hi:[0,1]
	v_rcp_f32_e32 v18, v60
	s_nop 0
	v_pk_add_f32 v[20:21], v[20:21], v[24:25]
	global_load_dwordx2 v[24:25], v[50:51], off
	v_pk_fma_f32 v[18:19], v[18:19], v[20:21], v[12:13] op_sel_hi:[0,1,1] neg_lo:[0,0,1] neg_hi:[0,0,1]
	v_cvt_pk_bf16_f32 v18, v18, v19
	ds_write_b32 v94, v18 offset:51200
	s_min_i32 s8, s31, -12
	s_add_i32 s8, s8, 28
	v_cvt_f32_i32_e32 v34, s8
	v_rcp_f32_e32 v18, v28
	s_nop 0
	s_waitcnt vmcnt(2)
	v_pk_add_f32 v[28:29], v[14:15], v[36:37] neg_lo:[0,1] neg_hi:[0,1]
	s_nop 0
	v_pk_add_f32 v[28:29], v[20:21], v[28:29]
	global_load_dwordx2 v[20:21], v[48:49], off
	v_pk_fma_f32 v[18:19], v[18:19], v[28:29], v[14:15] op_sel_hi:[0,1,1] neg_lo:[0,0,1] neg_hi:[0,0,1]
	v_cvt_pk_bf16_f32 v18, v18, v19
	ds_write_b32 v95, v18 offset:53248
	s_min_i32 s8, s31, -13
	s_add_i32 s8, s8, 29
	v_cvt_f32_i32_e32 v36, s8
	v_rcp_f32_e32 v18, v34
	s_nop 0
	s_waitcnt vmcnt(2)
	v_pk_add_f32 v[34:35], v[16:17], v[38:39] neg_lo:[0,1] neg_hi:[0,1]
	v_pk_add_f32 v[28:29], v[28:29], v[34:35]
	v_pk_fma_f32 v[18:19], v[18:19], v[28:29], v[16:17] op_sel_hi:[0,1,1] neg_lo:[0,0,1] neg_hi:[0,0,1]
	v_cvt_pk_bf16_f32 v18, v18, v19
	ds_write_b32 v96, v18 offset:55296
	global_load_dwordx2 v[18:19], v[46:47], off
	s_min_i32 s8, s31, -14
	s_add_i32 s8, s8, 30
	v_cvt_f32_i32_e32 v38, s8
	v_rcp_f32_e32 v34, v36
	s_nop 0
	v_pk_add_f32 v[36:37], v[22:23], v[40:41] neg_lo:[0,1] neg_hi:[0,1]
	s_waitcnt vmcnt(0)
	v_pk_add_f32 v[32:33], v[18:19], v[32:33] neg_lo:[0,1] neg_hi:[0,1]
	v_pk_add_f32 v[28:29], v[28:29], v[36:37]
	v_pk_fma_f32 v[34:35], v[34:35], v[28:29], v[22:23] op_sel_hi:[0,1,1] neg_lo:[0,0,1] neg_hi:[0,0,1]
	v_cvt_pk_bf16_f32 v34, v34, v35
	ds_write_b32 v97, v34 offset:57344
	s_min_i32 s8, s31, -15
	s_add_i32 s8, s8, 31
	v_rcp_f32_e32 v34, v38
	s_nop 0
	v_cvt_f32_i32_e32 v38, s8
	v_pk_add_f32 v[36:37], v[24:25], v[42:43] neg_lo:[0,1] neg_hi:[0,1]
	s_nop 0
	v_pk_add_f32 v[28:29], v[28:29], v[36:37]
	v_pk_fma_f32 v[34:35], v[34:35], v[28:29], v[24:25] op_sel_hi:[0,1,1] neg_lo:[0,0,1] neg_hi:[0,0,1]
	v_cvt_pk_bf16_f32 v34, v34, v35
	ds_write_b32 v98, v34 offset:59392
	s_min_i32 s8, s31, -16
	s_add_i32 s8, s8, 32
	v_cvt_f32_i32_e32 v35, s8
	v_rcp_f32_e32 v34, v38
	s_nop 0
	v_pk_add_f32 v[36:37], v[20:21], v[44:45] neg_lo:[0,1] neg_hi:[0,1]
	v_pk_add_f32 v[36:37], v[28:29], v[36:37]
	s_or_b32 s8, s80, 32
	v_pk_fma_f32 v[28:29], v[34:35], v[36:37], v[20:21] op_sel_hi:[0,1,1] neg_lo:[0,0,1] neg_hi:[0,0,1]
	v_cvt_pk_bf16_f32 v28, v28, v29
	ds_write_b32 v99, v28 offset:61440
	s_ashr_i32 s9, s8, 31
	s_lshl_b64 s[8:9], s[8:9], 12
	v_lshl_add_u64 v[28:29], v[4:5], 0, s[8:9]
	global_load_dwordx2 v[28:29], v[28:29], off
	v_rcp_f32_e32 v34, v35
	s_nop 0
	v_pk_add_f32 v[38:39], v[36:37], v[32:33]
	s_or_b32 s8, s80, 33
	v_pk_fma_f32 v[32:33], v[34:35], v[38:39], v[18:19] op_sel_hi:[0,1,1] neg_lo:[0,0,1] neg_hi:[0,0,1]
	s_ashr_i32 s9, s8, 31
	v_cvt_pk_bf16_f32 v32, v32, v33
	s_lshl_b64 s[8:9], s[8:9], 12
	ds_write_b32 v84, v32 offset:63488
	v_lshl_add_u64 v[32:33], v[4:5], 0, s[8:9]
	global_load_dwordx2 v[32:33], v[32:33], off
	s_or_b32 s8, s80, 34
	s_ashr_i32 s9, s8, 31
	s_lshl_b64 s[8:9], s[8:9], 12
	v_lshl_add_u64 v[34:35], v[4:5], 0, s[8:9]
	s_or_b32 s8, s80, 35
	s_ashr_i32 s9, s8, 31
	s_lshl_b64 s[8:9], s[8:9], 12
	v_lshl_add_u64 v[36:37], v[4:5], 0, s[8:9]
	s_or_b32 s8, s80, 36
	s_ashr_i32 s9, s8, 31
	s_lshl_b64 s[8:9], s[8:9], 12
	v_lshl_add_u64 v[40:41], v[4:5], 0, s[8:9]
	s_or_b32 s8, s80, 37
	s_ashr_i32 s9, s8, 31
	s_lshl_b64 s[8:9], s[8:9], 12
	v_lshl_add_u64 v[64:65], v[4:5], 0, s[8:9]
	s_or_b32 s8, s80, 38
	s_ashr_i32 s9, s8, 31
	s_lshl_b64 s[8:9], s[8:9], 12
	v_lshl_add_u64 v[60:61], v[4:5], 0, s[8:9]
	s_or_b32 s8, s80, 39
	s_ashr_i32 s9, s8, 31
	s_lshl_b64 s[8:9], s[8:9], 12
	v_lshl_add_u64 v[62:63], v[4:5], 0, s[8:9]
	s_or_b32 s8, s80, 40
	s_ashr_i32 s9, s8, 31
	s_lshl_b64 s[8:9], s[8:9], 12
	v_lshl_add_u64 v[48:49], v[4:5], 0, s[8:9]
	s_or_b32 s8, s80, 41
	s_ashr_i32 s9, s8, 31
	s_lshl_b64 s[8:9], s[8:9], 12
	v_lshl_add_u64 v[44:45], v[4:5], 0, s[8:9]
	s_or_b32 s8, s80, 42
	s_ashr_i32 s9, s8, 31
	s_lshl_b64 s[8:9], s[8:9], 12
	global_load_dwordx2 v[34:35], v[34:35], off
	v_lshl_add_u64 v[50:51], v[4:5], 0, s[8:9]
	s_or_b32 s8, s80, 43
	s_ashr_i32 s9, s8, 31
	s_lshl_b64 s[8:9], s[8:9], 12
	v_lshl_add_u64 v[46:47], v[4:5], 0, s[8:9]
	s_or_b32 s8, s80, 44
	s_ashr_i32 s9, s8, 31
	s_lshl_b64 s[8:9], s[8:9], 12
	v_lshl_add_u64 v[42:43], v[4:5], 0, s[8:9]
	global_load_dwordx2 v[36:37], v[36:37], off
	s_or_b32 s8, s80, 45
	s_ashr_i32 s9, s8, 31
	v_rcp_f32_e32 v66, v66
	s_nop 0
	v_cvt_f32_i32_e32 v67, s10
	s_lshl_b64 s[8:9], s[8:9], 12
	s_waitcnt vmcnt(3)
	v_pk_add_f32 v[56:57], v[28:29], v[56:57] neg_lo:[0,1] neg_hi:[0,1]
	s_nop 0
	v_pk_add_f32 v[56:57], v[38:39], v[56:57]
	s_waitcnt vmcnt(2)
	v_pk_add_f32 v[54:55], v[32:33], v[54:55] neg_lo:[0,1] neg_hi:[0,1]
	v_pk_fma_f32 v[38:39], v[66:67], v[56:57], v[28:29] op_sel_hi:[0,1,1] neg_lo:[0,0,1] neg_hi:[0,0,1]
	v_readlane_b32 s10, v254, 19
	v_cvt_pk_bf16_f32 v38, v38, v39
	v_pk_add_f32 v[54:55], v[56:57], v[54:55]
	v_add3_u32 v39, s10, v3, v68
	ds_write_b32 v39, v38
	global_load_dwordx2 v[38:39], v[40:41], off
	s_min_i32 s10, s31, 0xffffffed
	s_add_i32 s10, s10, 35
	v_cvt_f32_i32_e32 v66, s10
	v_rcp_f32_e32 v40, v67
	s_nop 0
	v_pk_fma_f32 v[40:41], v[40:41], v[54:55], v[32:33] op_sel_hi:[0,1,1] neg_lo:[0,0,1] neg_hi:[0,0,1]
	v_readlane_b32 s10, v254, 21
	v_cvt_pk_bf16_f32 v40, v40, v41
	s_waitcnt vmcnt(2)
	v_pk_add_f32 v[52:53], v[34:35], v[52:53] neg_lo:[0,1] neg_hi:[0,1]
	v_add3_u32 v41, s10, v70, v68
	ds_write_b32 v41, v40
	global_load_dwordx2 v[40:41], v[64:65], off
	s_min_i32 s10, s31, 0xffffffec
	s_add_i32 s10, s10, 36
	v_cvt_f32_i32_e32 v57, s10
	v_rcp_f32_e32 v56, v66
	s_nop 0
	v_pk_add_f32 v[52:53], v[54:55], v[52:53]
	s_waitcnt vmcnt(1)
	v_pk_add_f32 v[26:27], v[38:39], v[26:27] neg_lo:[0,1] neg_hi:[0,1]
	v_pk_fma_f32 v[54:55], v[56:57], v[52:53], v[34:35] op_sel_hi:[0,1,1] neg_lo:[0,0,1] neg_hi:[0,0,1]
	v_readlane_b32 s10, v254, 23
	v_cvt_pk_bf16_f32 v54, v54, v55
	s_waitcnt vmcnt(0)
	v_pk_add_f32 v[30:31], v[40:41], v[30:31] neg_lo:[0,1] neg_hi:[0,1]
	v_add3_u32 v55, s10, v71, v68
	ds_write_b32 v55, v54
	s_min_i32 s10, s31, 0xffffffeb
	s_add_i32 s10, s10, 37
	v_cvt_f32_i32_e32 v55, s10
	v_rcp_f32_e32 v54, v57
	s_nop 0
	v_pk_add_f32 v[56:57], v[36:37], v[58:59] neg_lo:[0,1] neg_hi:[0,1]
	v_add3_u32 v71, s25, v71, v68
	v_pk_add_f32 v[56:57], v[52:53], v[56:57]
	s_nop 0
	v_pk_fma_f32 v[52:53], v[54:55], v[56:57], v[36:37] op_sel_hi:[0,1,1] neg_lo:[0,0,1] neg_hi:[0,0,1]
	v_readlane_b32 s10, v254, 25
	v_cvt_pk_bf16_f32 v52, v52, v53
	v_pk_add_f32 v[26:27], v[56:57], v[26:27]
	v_add3_u32 v53, s10, v72, v68
	ds_write_b32 v53, v52
	s_min_i32 s10, s31, 0xffffffea
	s_add_i32 s10, s10, 38
	v_cvt_f32_i32_e32 v59, s10
	v_rcp_f32_e32 v58, v55
	s_nop 0
	v_pk_fma_f32 v[56:57], v[58:59], v[26:27], v[38:39] op_sel_hi:[0,1,1] neg_lo:[0,0,1] neg_hi:[0,0,1]
	global_load_dwordx2 v[54:55], v[60:61], off
	global_load_dwordx2 v[52:53], v[62:63], off
	v_readlane_b32 s10, v254, 29
	v_cvt_pk_bf16_f32 v56, v56, v57
	v_pk_add_f32 v[26:27], v[26:27], v[30:31]
	v_add3_u32 v57, s10, v73, v68
	ds_write_b32 v57, v56
	s_min_i32 s10, s31, 0xffffffe9
	s_add_i32 s10, s10, 39
	v_cvt_f32_i32_e32 v60, s10
	v_rcp_f32_e32 v56, v59
	s_nop 0
	v_pk_fma_f32 v[30:31], v[56:57], v[26:27], v[40:41] op_sel_hi:[0,1,1] neg_lo:[0,0,1] neg_hi:[0,0,1]
	v_cvt_pk_bf16_f32 v30, v30, v31
	v_readlane_b32 s10, v254, 31
	global_load_dwordx2 v[44:45], v[44:45], off
	v_add3_u32 v73, s27, v73, v68
	v_add3_u32 v31, s10, v74, v68
	s_min_i32 s10, s31, 0xffffffe8
	s_add_i32 s10, s10, 40
	ds_write_b32 v31, v30
	v_cvt_f32_i32_e32 v61, s10
	s_min_i32 s10, s31, 0xffffffe7
	s_add_i32 s10, s10, 41
	v_cvt_f32_i32_e32 v63, s10
	s_min_i32 s10, s31, 0xffffffe6
	s_add_i32 s10, s10, 42
	v_cvt_f32_i32_e32 v65, s10
	s_min_i32 s10, s31, 0xffffffe5
	s_add_i32 s10, s10, 43
	v_cvt_f32_i32_e32 v67, s10
	s_min_i32 s10, s31, 0xffffffe4
	s_add_i32 s10, s10, 44
	v_cvt_f32_i32_e32 v85, s10
	s_min_i32 s10, s31, 0xffffffe3
	s_add_i32 s10, s10, 45
	v_cvt_f32_i32_e32 v87, s10
	s_min_i32 s10, s31, 0xffffffe2
	s_add_i32 s10, s10, 46
	v_cvt_f32_i32_e32 v89, s10
	s_min_i32 s10, s31, 0xffffffe1
	s_add_i32 s10, s10, 47
	v_cvt_f32_i32_e32 v91, s10
	s_min_i32 s10, s31, 0xffffffe0
	s_add_i32 s10, s10, 48
	v_cvt_f32_i32_e32 v93, s10
	s_min_i32 s10, s31, 0xffffffdf
	s_add_i32 s10, s10, 49
	v_cvt_f32_i32_e32 v95, s10
	s_min_i32 s10, s31, 0xffffffde
	s_add_i32 s10, s10, 50
	v_cvt_f32_i32_e32 v97, s10
	s_min_i32 s10, s31, 0xffffffdd
	s_add_i32 s10, s10, 51
	v_cvt_f32_i32_e32 v99, s10
	s_min_i32 s10, s31, 0xffffffdc
	s_add_i32 s10, s10, 52
	v_cvt_f32_i32_e32 v101, s10
	s_min_i32 s10, s31, 0xffffffdb
	s_add_i32 s10, s10, 53
	v_cvt_f32_i32_e32 v103, s10
	s_min_i32 s10, s31, 0xffffffda
	s_add_i32 s10, s10, 54
	v_cvt_f32_i32_e32 v105, s10
	s_min_i32 s10, s31, 0xffffffd9
	s_add_i32 s10, s10, 55
	v_cvt_f32_i32_e32 v107, s10
	s_min_i32 s10, s31, 0xffffffd8
	s_add_i32 s10, s10, 56
	v_cvt_f32_i32_e32 v109, s10
	s_min_i32 s10, s31, 0xffffffd7
	s_add_i32 s10, s10, 57
	v_cvt_f32_i32_e32 v111, s10
	s_min_i32 s10, s31, 0xffffffd6
	s_add_i32 s10, s10, 58
	v_cvt_f32_i32_e32 v113, s10
	s_min_i32 s10, s31, 0xffffffd5
	s_add_i32 s10, s10, 59
	v_cvt_f32_i32_e32 v115, s10
	s_min_i32 s10, s31, 0xffffffd4
	s_add_i32 s10, s10, 60
	v_cvt_f32_i32_e32 v117, s10
	s_min_i32 s10, s31, 0xffffffd3
	s_add_i32 s10, s10, 61
	v_cvt_f32_i32_e32 v119, s10
	s_min_i32 s10, s31, 0xffffffd2
	global_load_dwordx2 v[30:31], v[48:49], off
	s_add_i32 s10, s10, 62
	v_cvt_f32_i32_e32 v121, s10
	s_min_i32 s10, s31, 0xffffffd1
	s_add_i32 s10, s10, 63
	v_cvt_f32_i32_e32 v123, s10
	global_load_dwordx2 v[46:47], v[46:47], off
	global_load_dwordx2 v[48:49], v[50:51], off
	v_lshl_add_u64 v[50:51], v[4:5], 0, s[8:9]
	s_or_b32 s8, s80, 46
	s_ashr_i32 s9, s8, 31
	s_lshl_b64 s[8:9], s[8:9], 12
	v_lshl_add_u64 v[56:57], v[4:5], 0, s[8:9]
	s_or_b32 s8, s80, 47
	s_ashr_i32 s9, s8, 31
	s_waitcnt vmcnt(5)
	v_pk_add_f32 v[6:7], v[54:55], v[6:7] neg_lo:[0,1] neg_hi:[0,1]
	s_lshl_b64 s[8:9], s[8:9], 12
	v_pk_add_f32 v[26:27], v[26:27], v[6:7]
	v_rcp_f32_e32 v6, v60
	s_nop 0
	v_lshl_add_u64 v[58:59], v[4:5], 0, s[8:9]
	v_pk_fma_f32 v[6:7], v[6:7], v[26:27], v[54:55] op_sel_hi:[0,1,1] neg_lo:[0,0,1] neg_hi:[0,0,1]
	v_readlane_b32 s8, v254, 33
	v_cvt_pk_bf16_f32 v6, v6, v7
	s_waitcnt vmcnt(4)
	v_pk_add_f32 v[8:9], v[52:53], v[8:9] neg_lo:[0,1] neg_hi:[0,1]
	v_add3_u32 v7, s8, v75, v68
	v_readlane_b32 s8, v254, 35
	v_rcp_f32_e32 v60, v61
	s_nop 0
	v_pk_add_f32 v[26:27], v[26:27], v[8:9]
	v_add3_u32 v61, s8, v76, v68
	v_pk_fma_f32 v[8:9], v[60:61], v[26:27], v[52:53] op_sel_hi:[0,1,1] neg_lo:[0,0,1] neg_hi:[0,0,1]
	ds_write_b32 v7, v6
	global_load_dwordx2 v[6:7], v[42:43], off
	v_cvt_pk_bf16_f32 v8, v8, v9
	ds_write_b32 v61, v8
	global_load_dwordx2 v[8:9], v[50:51], off
	v_rcp_f32_e32 v62, v63
	s_nop 0
	s_waitcnt vmcnt(5)
	v_pk_add_f32 v[12:13], v[44:45], v[12:13] neg_lo:[0,1] neg_hi:[0,1]
	v_readlane_b32 s8, v254, 37
	v_rcp_f32_e32 v42, v67
	s_nop 0
	v_rcp_f32_e32 v66, v85
	s_nop 0
	v_add3_u32 v126, s8, v77, v68
	v_readlane_b32 s8, v254, 39
	v_rcp_f32_e32 v60, v87
	s_nop 0
	v_rcp_f32_e32 v64, v65
	s_nop 0
	v_add3_u32 v43, s8, v78, v68
	v_readlane_b32 s8, v254, 41
	v_rcp_f32_e32 v84, v89
	s_nop 0
	global_load_dwordx2 v[58:59], v[58:59], off
	v_add3_u32 v67, s8, v79, v68
	s_waitcnt vmcnt(5)
	v_pk_add_f32 v[10:11], v[30:31], v[10:11] neg_lo:[0,1] neg_hi:[0,1]
	v_readlane_b32 s8, v254, 43
	v_pk_add_f32 v[10:11], v[26:27], v[10:11]
	v_rcp_f32_e32 v26, v93
	s_nop 0
	v_pk_fma_f32 v[62:63], v[62:63], v[10:11], v[30:31] op_sel_hi:[0,1,1] neg_lo:[0,0,1] neg_hi:[0,0,1]
	v_pk_add_f32 v[12:13], v[10:11], v[12:13]
	global_load_dwordx2 v[10:11], v[56:57], off
	v_add3_u32 v85, s8, v80, v68
	v_readlane_b32 s8, v254, 45
	v_cvt_pk_bf16_f32 v51, v62, v63
	v_pk_fma_f32 v[56:57], v[64:65], v[12:13], v[44:45] op_sel_hi:[0,1,1] neg_lo:[0,0,1] neg_hi:[0,0,1]
	v_add3_u32 v90, s8, v81, v68
	v_readlane_b32 s8, v254, 47
	ds_write_b32 v126, v51
	v_cvt_pk_bf16_f32 v51, v56, v57
	v_add3_u32 v92, s8, v82, v68
	v_readlane_b32 s8, v254, 49
	ds_write_b32 v43, v51
	v_rcp_f32_e32 v50, v91
	s_nop 0
	v_add3_u32 v27, s8, v83, v68
	v_readlane_b32 s8, v254, 51
	v_rcp_f32_e32 v94, v97
	s_nop 0
	v_rcp_f32_e32 v96, v101
	s_nop 0
	v_add3_u32 v93, s8, v69, v68
	s_or_b32 s8, s80, 48
	s_ashr_i32 s9, s8, 31
	s_lshl_b64 s[8:9], s[8:9], 12
	v_lshl_add_u64 v[62:63], v[4:5], 0, s[8:9]
	s_or_b32 s8, s80, 49
	s_ashr_i32 s9, s8, 31
	s_lshl_b64 s[8:9], s[8:9], 12
	v_lshl_add_u64 v[86:87], v[4:5], 0, s[8:9]
	s_or_b32 s8, s80, 50
	s_ashr_i32 s9, s8, 31
	s_lshl_b64 s[8:9], s[8:9], 12
	v_lshl_add_u64 v[56:57], v[4:5], 0, s[8:9]
	s_or_b32 s8, s80, 51
	s_ashr_i32 s9, s8, 31
	s_lshl_b64 s[8:9], s[8:9], 12
	v_lshl_add_u64 v[64:65], v[4:5], 0, s[8:9]
	s_or_b32 s8, s80, 52
	s_ashr_i32 s9, s8, 31
	s_lshl_b64 s[8:9], s[8:9], 12
	s_waitcnt vmcnt(4)
	v_pk_add_f32 v[14:15], v[48:49], v[14:15] neg_lo:[0,1] neg_hi:[0,1]
	global_load_dwordx2 v[62:63], v[62:63], off
	v_pk_add_f32 v[12:13], v[12:13], v[14:15]
	v_lshl_add_u64 v[14:15], v[4:5], 0, s[8:9]
	v_pk_fma_f32 v[42:43], v[42:43], v[12:13], v[48:49] op_sel_hi:[0,1,1] neg_lo:[0,0,1] neg_hi:[0,0,1]
	global_load_dwordx2 v[14:15], v[14:15], off
	v_pk_add_f32 v[16:17], v[46:47], v[16:17] neg_lo:[0,1] neg_hi:[0,1]
	v_cvt_pk_bf16_f32 v42, v42, v43
	v_pk_add_f32 v[12:13], v[12:13], v[16:17]
	ds_write_b32 v67, v42
	v_pk_fma_f32 v[66:67], v[66:67], v[12:13], v[46:47] op_sel_hi:[0,1,1] neg_lo:[0,0,1] neg_hi:[0,0,1]
	s_or_b32 s8, s80, 53
	s_ashr_i32 s9, s8, 31
	global_load_dwordx2 v[64:65], v[64:65], off
	s_lshl_b64 s[8:9], s[8:9], 12
	global_load_dwordx2 v[56:57], v[56:57], off
	v_lshl_add_u64 v[42:43], v[4:5], 0, s[8:9]
	s_or_b32 s8, s80, 54
	s_ashr_i32 s9, s8, 31
	s_waitcnt vmcnt(7)
	v_pk_add_f32 v[22:23], v[6:7], v[22:23] neg_lo:[0,1] neg_hi:[0,1]
	s_lshl_b64 s[8:9], s[8:9], 12
	v_pk_add_f32 v[12:13], v[12:13], v[22:23]
	s_waitcnt vmcnt(6)
	v_pk_add_f32 v[24:25], v[8:9], v[24:25] neg_lo:[0,1] neg_hi:[0,1]
	v_pk_fma_f32 v[60:61], v[60:61], v[12:13], v[6:7] op_sel_hi:[0,1,1] neg_lo:[0,0,1] neg_hi:[0,0,1]
	v_pk_add_f32 v[12:13], v[12:13], v[24:25]
	global_load_dwordx2 v[24:25], v[86:87], off
	v_lshl_add_u64 v[16:17], v[4:5], 0, s[8:9]
	s_or_b32 s8, s80, 55
	v_cvt_pk_bf16_f32 v51, v66, v67
	s_ashr_i32 s9, s8, 31
	ds_write_b32 v85, v51
	v_cvt_pk_bf16_f32 v51, v60, v61
	v_pk_fma_f32 v[84:85], v[84:85], v[12:13], v[8:9] op_sel_hi:[0,1,1] neg_lo:[0,0,1] neg_hi:[0,0,1]
	s_lshl_b64 s[8:9], s[8:9], 12
	ds_write_b32 v90, v51
	v_cvt_pk_bf16_f32 v51, v84, v85
	v_lshl_add_u64 v[66:67], v[4:5], 0, s[8:9]
	s_or_b32 s8, s80, 56
	ds_write_b32 v92, v51
	s_ashr_i32 s9, s8, 31
	global_load_dwordx2 v[16:17], v[16:17], off
	s_nop 0
	global_load_dwordx2 v[66:67], v[66:67], off
	s_nop 0
	global_load_dwordx2 v[42:43], v[42:43], off
	s_lshl_b64 s[8:9], s[8:9], 12
	v_lshl_add_u64 v[88:89], v[4:5], 0, s[8:9]
	s_or_b32 s8, s80, 57
	s_ashr_i32 s9, s8, 31
	s_lshl_b64 s[8:9], s[8:9], 12
	v_lshl_add_u64 v[22:23], v[4:5], 0, s[8:9]
	s_or_b32 s8, s80, 58
	s_ashr_i32 s9, s8, 31
	s_lshl_b64 s[8:9], s[8:9], 12
	v_lshl_add_u64 v[60:61], v[4:5], 0, s[8:9]
	s_or_b32 s8, s80, 59
	s_ashr_i32 s9, s8, 31
	global_load_dwordx2 v[88:89], v[88:89], off
	s_lshl_b64 s[8:9], s[8:9], 12
	v_lshl_add_u64 v[86:87], v[4:5], 0, s[8:9]
	s_or_b32 s8, s80, 60
	s_ashr_i32 s9, s8, 31
	global_load_dwordx2 v[22:23], v[22:23], off
	s_lshl_b64 s[8:9], s[8:9], 12
	v_lshl_add_u64 v[84:85], v[4:5], 0, s[8:9]
	s_or_b32 s8, s80, 61
	s_ashr_i32 s9, s8, 31
	global_load_dwordx2 v[60:61], v[60:61], off
	s_lshl_b64 s[8:9], s[8:9], 12
	v_lshl_add_u64 v[90:91], v[4:5], 0, s[8:9]
	global_load_dwordx2 v[90:91], v[90:91], off
	s_or_b32 s8, s80, 62
	global_load_dwordx2 v[86:87], v[86:87], off
	s_ashr_i32 s9, s8, 31
	global_load_dwordx2 v[84:85], v[84:85], off
	s_lshl_b64 s[8:9], s[8:9], 12
	s_waitcnt vmcnt(14)
	v_pk_add_f32 v[20:21], v[10:11], v[20:21] neg_lo:[0,1] neg_hi:[0,1]
	v_pk_add_f32 v[18:19], v[58:59], v[18:19] neg_lo:[0,1] neg_hi:[0,1]
	v_pk_add_f32 v[12:13], v[12:13], v[20:21]
	v_lshl_add_u64 v[20:21], v[4:5], 0, s[8:9]
	s_or_b32 s8, s80, 63
	s_ashr_i32 s9, s8, 31
	global_load_dwordx2 v[20:21], v[20:21], off
	s_lshl_b64 s[8:9], s[8:9], 12
	v_lshl_add_u64 v[4:5], v[4:5], 0, s[8:9]
	global_load_dwordx2 v[4:5], v[4:5], off
	v_pk_fma_f32 v[50:51], v[50:51], v[12:13], v[10:11] op_sel_hi:[0,1,1] neg_lo:[0,0,1] neg_hi:[0,0,1]
	v_pk_add_f32 v[12:13], v[12:13], v[18:19]
	v_cvt_pk_bf16_f32 v50, v50, v51
	v_pk_fma_f32 v[18:19], v[26:27], v[12:13], v[58:59] op_sel_hi:[0,1,1] neg_lo:[0,0,1] neg_hi:[0,0,1]
	v_cvt_pk_bf16_f32 v18, v18, v19
	ds_write_b32 v27, v50
	ds_write_b32 v93, v18
	s_waitcnt vmcnt(15)
	v_pk_add_f32 v[18:19], v[62:63], v[28:29] neg_lo:[0,1] neg_hi:[0,1]
	v_rcp_f32_e32 v92, v95
	s_nop 0
	v_pk_add_f32 v[12:13], v[12:13], v[18:19]
	v_readlane_b32 s8, v254, 53
	v_pk_fma_f32 v[18:19], v[92:93], v[12:13], v[62:63] op_sel_hi:[0,1,1] neg_lo:[0,0,1] neg_hi:[0,0,1]
	v_cvt_pk_bf16_f32 v18, v18, v19
	v_add3_u32 v3, s8, v3, v68
	ds_write_b32 v3, v18
	v_add3_u32 v95, s24, v70, v68
	v_rcp_f32_e32 v70, v99
	s_nop 0
	v_add3_u32 v97, s26, v72, v68
	v_rcp_f32_e32 v72, v103
	s_nop 0
	v_rcp_f32_e32 v98, v105
	s_nop 0
	v_add3_u32 v99, s77, v74, v68
	v_rcp_f32_e32 v74, v107
	s_nop 0
	v_add3_u32 v75, s91, v75, v68
	s_waitcnt vmcnt(11)
	v_pk_add_f32 v[18:19], v[24:25], v[32:33] neg_lo:[0,1] neg_hi:[0,1]
	v_rcp_f32_e32 v100, v109
	s_nop 0
	v_pk_add_f32 v[12:13], v[12:13], v[18:19]
	v_add3_u32 v101, s94, v76, v68
	v_pk_fma_f32 v[18:19], v[94:95], v[12:13], v[24:25] op_sel_hi:[0,1,1] neg_lo:[0,0,1] neg_hi:[0,0,1]
	v_cvt_pk_bf16_f32 v3, v18, v19
	v_pk_add_f32 v[18:19], v[56:57], v[34:35] neg_lo:[0,1] neg_hi:[0,1]
	ds_write_b32 v95, v3
	v_pk_add_f32 v[12:13], v[12:13], v[18:19]
	v_rcp_f32_e32 v76, v111
	s_nop 0
	v_pk_fma_f32 v[18:19], v[70:71], v[12:13], v[56:57] op_sel_hi:[0,1,1] neg_lo:[0,0,1] neg_hi:[0,0,1]
	v_cvt_pk_bf16_f32 v3, v18, v19
	v_pk_add_f32 v[18:19], v[64:65], v[36:37] neg_lo:[0,1] neg_hi:[0,1]
	ds_write_b32 v71, v3
	v_pk_add_f32 v[12:13], v[12:13], v[18:19]
	v_add3_u32 v77, s33, v77, v68
	v_pk_fma_f32 v[18:19], v[96:97], v[12:13], v[64:65] op_sel_hi:[0,1,1] neg_lo:[0,0,1] neg_hi:[0,0,1]
	v_cvt_pk_bf16_f32 v3, v18, v19
	v_pk_add_f32 v[18:19], v[14:15], v[38:39] neg_lo:[0,1] neg_hi:[0,1]
	ds_write_b32 v97, v3
	v_pk_add_f32 v[12:13], v[12:13], v[18:19]
	v_rcp_f32_e32 v102, v113
	s_nop 0
	v_pk_fma_f32 v[14:15], v[72:73], v[12:13], v[14:15] op_sel_hi:[0,1,1] neg_lo:[0,0,1] neg_hi:[0,0,1]
	v_cvt_pk_bf16_f32 v3, v14, v15
	s_waitcnt vmcnt(8)
	v_pk_add_f32 v[14:15], v[42:43], v[40:41] neg_lo:[0,1] neg_hi:[0,1]
	ds_write_b32 v73, v3
	v_pk_add_f32 v[12:13], v[12:13], v[14:15]
	v_add3_u32 v103, s75, v78, v68
	v_pk_fma_f32 v[14:15], v[98:99], v[12:13], v[42:43] op_sel_hi:[0,1,1] neg_lo:[0,0,1] neg_hi:[0,0,1]
	v_cvt_pk_bf16_f32 v3, v14, v15
	v_pk_add_f32 v[14:15], v[16:17], v[54:55] neg_lo:[0,1] neg_hi:[0,1]
	ds_write_b32 v99, v3
	v_pk_add_f32 v[12:13], v[12:13], v[14:15]
	v_rcp_f32_e32 v78, v115
	s_nop 0
	v_pk_fma_f32 v[14:15], v[74:75], v[12:13], v[16:17] op_sel_hi:[0,1,1] neg_lo:[0,0,1] neg_hi:[0,0,1]
	v_cvt_pk_bf16_f32 v3, v14, v15
	v_pk_add_f32 v[14:15], v[66:67], v[52:53] neg_lo:[0,1] neg_hi:[0,1]
	ds_write_b32 v75, v3
	v_pk_add_f32 v[12:13], v[12:13], v[14:15]
	v_add3_u32 v79, s95, v79, v68
	v_pk_fma_f32 v[14:15], v[100:101], v[12:13], v[66:67] op_sel_hi:[0,1,1] neg_lo:[0,0,1] neg_hi:[0,0,1]
	v_cvt_pk_bf16_f32 v3, v14, v15
	s_waitcnt vmcnt(7)
	v_pk_add_f32 v[14:15], v[88:89], v[30:31] neg_lo:[0,1] neg_hi:[0,1]
	ds_write_b32 v101, v3
	v_pk_add_f32 v[12:13], v[12:13], v[14:15]
	v_rcp_f32_e32 v104, v117
	s_nop 0
	v_pk_fma_f32 v[14:15], v[76:77], v[12:13], v[88:89] op_sel_hi:[0,1,1] neg_lo:[0,0,1] neg_hi:[0,0,1]
	v_cvt_pk_bf16_f32 v3, v14, v15
	s_waitcnt vmcnt(6)
	v_pk_add_f32 v[14:15], v[22:23], v[44:45] neg_lo:[0,1] neg_hi:[0,1]
	ds_write_b32 v77, v3
	v_pk_add_f32 v[12:13], v[12:13], v[14:15]
	v_add3_u32 v105, s96, v80, v68
	v_pk_fma_f32 v[14:15], v[102:103], v[12:13], v[22:23] op_sel_hi:[0,1,1] neg_lo:[0,0,1] neg_hi:[0,0,1]
	v_cvt_pk_bf16_f32 v3, v14, v15
	s_waitcnt vmcnt(5)
	v_pk_add_f32 v[14:15], v[60:61], v[48:49] neg_lo:[0,1] neg_hi:[0,1]
	ds_write_b32 v103, v3
	v_pk_add_f32 v[12:13], v[12:13], v[14:15]
	s_waitcnt vmcnt(2)
	v_pk_add_f32 v[6:7], v[84:85], v[6:7] neg_lo:[0,1] neg_hi:[0,1]
	v_pk_fma_f32 v[14:15], v[78:79], v[12:13], v[60:61] op_sel_hi:[0,1,1] neg_lo:[0,0,1] neg_hi:[0,0,1]
	v_cvt_pk_bf16_f32 v3, v14, v15
	v_pk_add_f32 v[14:15], v[86:87], v[46:47] neg_lo:[0,1] neg_hi:[0,1]
	v_rcp_f32_e32 v80, v119
	s_nop 0
	v_pk_add_f32 v[12:13], v[12:13], v[14:15]
	v_add3_u32 v81, s97, v81, v68
	v_pk_fma_f32 v[14:15], v[104:105], v[12:13], v[86:87] op_sel_hi:[0,1,1] neg_lo:[0,0,1] neg_hi:[0,0,1]
	v_pk_add_f32 v[6:7], v[12:13], v[6:7]
	v_pk_add_f32 v[8:9], v[90:91], v[8:9] neg_lo:[0,1] neg_hi:[0,1]
	v_rcp_f32_e32 v106, v121
	s_nop 0
	v_add3_u32 v107, s36, v82, v68
	ds_write_b32 v79, v3
	v_cvt_pk_bf16_f32 v3, v14, v15
	v_pk_fma_f32 v[12:13], v[80:81], v[6:7], v[84:85] op_sel_hi:[0,1,1] neg_lo:[0,0,1] neg_hi:[0,0,1]
	v_pk_add_f32 v[6:7], v[6:7], v[8:9]
	ds_write_b32 v105, v3
	v_cvt_pk_bf16_f32 v3, v12, v13
	v_pk_fma_f32 v[8:9], v[106:107], v[6:7], v[90:91] op_sel_hi:[0,1,1] neg_lo:[0,0,1] neg_hi:[0,0,1]
	ds_write_b32 v81, v3
	v_cvt_pk_bf16_f32 v3, v8, v9
	s_waitcnt vmcnt(1)
	v_pk_add_f32 v[8:9], v[20:21], v[10:11] neg_lo:[0,1] neg_hi:[0,1]
	v_rcp_f32_e32 v82, v123
	s_nop 0
	v_add3_u32 v83, s37, v83, v68
	v_pk_add_f32 v[6:7], v[6:7], v[8:9]
	ds_write_b32 v107, v3
	v_pk_fma_f32 v[8:9], v[82:83], v[6:7], v[20:21] op_sel_hi:[0,1,1] neg_lo:[0,0,1] neg_hi:[0,0,1]
	v_cvt_pk_bf16_f32 v3, v8, v9
	s_waitcnt vmcnt(0)
	v_pk_add_f32 v[8:9], v[4:5], v[58:59] neg_lo:[0,1] neg_hi:[0,1]
	s_min_i32 s10, s31, 0xffffffd0
	ds_write_b32 v83, v3
	v_pk_add_f32 v[6:7], v[6:7], v[8:9]
	v_mov_b32_e32 v3, s10
	s_branch .LBB0_118

.LBB0_117:
	s_ashr_i32 s81, s80, 31
	v_lshl_add_u64 v[2:3], v[2:3], 2, s[70:71]
	s_lshl_b64 s[4:5], s[80:81], 12
	v_lshl_add_u64 v[4:5], v[2:3], 0, s[4:5]
	global_load_dwordx2 v[32:33], v[4:5], off
	s_or_b32 s4, s80, 1
	s_ashr_i32 s5, s4, 31
	s_lshl_b64 s[4:5], s[4:5], 12
	v_lshl_add_u64 v[4:5], v[2:3], 0, s[4:5]
	global_load_dwordx2 v[42:43], v[4:5], off
	s_or_b32 s4, s80, 2
	s_ashr_i32 s5, s4, 31
	s_lshl_b64 s[4:5], s[4:5], 12
	v_lshl_add_u64 v[6:7], v[2:3], 0, s[4:5]
	s_or_b32 s4, s80, 3
	s_ashr_i32 s5, s4, 31
	global_load_dwordx2 v[44:45], v[6:7], off
	s_lshl_b64 s[4:5], s[4:5], 12
	v_lshl_add_u64 v[30:31], v[2:3], 0, s[4:5]
	s_or_b32 s4, s80, 4
	s_ashr_i32 s5, s4, 31
	s_lshl_b64 s[4:5], s[4:5], 12
	v_lshl_add_u64 v[34:35], v[2:3], 0, s[4:5]
	s_or_b32 s4, s80, 5
	s_ashr_i32 s5, s4, 31
	s_lshl_b64 s[4:5], s[4:5], 12
	v_lshl_add_u64 v[36:37], v[2:3], 0, s[4:5]
	s_or_b32 s4, s80, 6
	s_ashr_i32 s5, s4, 31
	s_lshl_b64 s[4:5], s[4:5], 12
	v_lshl_add_u64 v[26:27], v[2:3], 0, s[4:5]
	s_or_b32 s4, s80, 7
	s_ashr_i32 s5, s4, 31
	s_lshl_b64 s[4:5], s[4:5], 12
	v_lshl_add_u64 v[24:25], v[2:3], 0, s[4:5]
	s_or_b32 s4, s80, 8
	s_ashr_i32 s5, s4, 31
	s_lshl_b64 s[4:5], s[4:5], 12
	v_lshl_add_u64 v[20:21], v[2:3], 0, s[4:5]
	s_or_b32 s4, s80, 9
	s_ashr_i32 s5, s4, 31
	s_lshl_b64 s[4:5], s[4:5], 12
	v_lshl_add_u64 v[16:17], v[2:3], 0, s[4:5]
	s_or_b32 s4, s80, 10
	s_ashr_i32 s5, s4, 31
	s_lshl_b64 s[4:5], s[4:5], 12
	s_min_i32 s8, s31, 1
	v_lshl_add_u64 v[14:15], v[2:3], 0, s[4:5]
	s_or_b32 s4, s80, 11
	s_add_i32 s8, s8, 1
	s_ashr_i32 s5, s4, 31
	v_cvt_f32_i32_e32 v29, s8
	s_lshl_b64 s[4:5], s[4:5], 12
	v_lshl_add_u64 v[12:13], v[2:3], 0, s[4:5]
	s_or_b32 s4, s80, 12
	s_ashr_i32 s5, s4, 31
	s_lshl_b64 s[4:5], s[4:5], 12
	v_lshl_add_u64 v[10:11], v[2:3], 0, s[4:5]
	s_or_b32 s4, s80, 13
	s_ashr_i32 s5, s4, 31
	s_lshl_b64 s[4:5], s[4:5], 12
	v_lshl_add_u64 v[8:9], v[2:3], 0, s[4:5]
	s_or_b32 s4, s80, 14
	s_ashr_i32 s5, s4, 31
	s_lshl_b64 s[4:5], s[4:5], 12
	global_load_dwordx2 v[12:13], v[12:13], off
	global_load_dwordx2 v[8:9], v[8:9], off
	v_lshl_add_u64 v[6:7], v[2:3], 0, s[4:5]
	s_or_b32 s4, s80, 15
	s_ashr_i32 s5, s4, 31
	s_lshl_b64 s[4:5], s[4:5], 12
	v_lshl_add_u64 v[4:5], v[2:3], 0, s[4:5]
	global_load_dwordx2 v[46:47], v[30:31], off
	global_load_dwordx2 v[50:51], v[36:37], off
	s_min_i32 s4, s31, 0
	s_or_b32 s4, s4, 2
	v_rcp_f32_e32 v30, v29
	s_nop 0
	v_cvt_f32_i32_e32 v29, s4
	v_lshlrev_b32_e32 v28, 2, v221
	s_waitcnt vmcnt(6)
	v_pk_add_f32 v[22:23], v[22:23], v[32:33]
	v_and_b32_e32 v68, 12, v28
	v_pk_fma_f32 v[30:31], v[30:31], v[22:23], v[32:33] op_sel_hi:[0,1,1] neg_lo:[0,0,1] neg_hi:[0,0,1]
	v_and_b32_e32 v38, -16, v28
	v_cvt_pk_bf16_f32 v31, v30, v31
	v_add3_u32 v30, 0, v38, v68
	ds_write_b32 v30, v31
	global_load_dwordx2 v[48:49], v[34:35], off
	s_min_i32 s4, s31, -1
	s_add_i32 s4, s4, 3
	v_rcp_f32_e32 v34, v29
	s_nop 0
	v_cvt_f32_i32_e32 v29, s4
	s_waitcnt vmcnt(6)
	v_pk_add_f32 v[18:19], v[42:43], v[18:19] neg_lo:[0,1] neg_hi:[0,1]
	v_bitop3_b32 v40, v28, 16, -16 bitop3:0x6c
	v_pk_add_f32 v[18:19], v[22:23], v[18:19]
	v_pk_fma_f32 v[22:23], v[34:35], v[18:19], v[42:43] op_sel_hi:[0,1,1] neg_lo:[0,0,1] neg_hi:[0,0,1]
	v_cvt_pk_bf16_f32 v22, v22, v23
	v_add3_u32 v23, 0, v40, v68
	ds_write_b32 v23, v22 offset:2048
	s_min_i32 s4, s31, -2
	s_add_i32 s4, s4, 4
	v_cvt_f32_i32_e32 v31, s4
	s_waitcnt vmcnt(5)
	v_pk_add_f32 v[32:33], v[44:45], v[32:33] neg_lo:[0,1] neg_hi:[0,1]
	v_rcp_f32_e32 v22, v29
	s_nop 0
	v_pk_add_f32 v[18:19], v[18:19], v[32:33]
	v_bitop3_b32 v41, v28, 32, -16 bitop3:0x6c
	v_pk_fma_f32 v[32:33], v[22:23], v[18:19], v[44:45] op_sel_hi:[0,1,1] neg_lo:[0,0,1] neg_hi:[0,0,1]
	v_cvt_pk_bf16_f32 v22, v32, v33
	v_add3_u32 v29, 0, v41, v68
	ds_write_b32 v29, v22 offset:4096
	global_load_dwordx2 v[32:33], v[26:27], off
	global_load_dwordx2 v[52:53], v[24:25], off
	s_min_i32 s4, s31, -3
	s_add_i32 s4, s4, 5
	v_rcp_f32_e32 v22, v31
	s_nop 0
	v_cvt_f32_i32_e32 v31, s4
	global_load_dwordx2 v[20:21], v[20:21], off
	s_waitcnt vmcnt(5)
	v_pk_add_f32 v[26:27], v[46:47], v[42:43] neg_lo:[0,1] neg_hi:[0,1]
	v_bitop3_b32 v43, v28, 48, -16 bitop3:0x6c
	v_pk_add_f32 v[18:19], v[18:19], v[26:27]
	global_load_dwordx2 v[16:17], v[16:17], off
	v_pk_fma_f32 v[26:27], v[22:23], v[18:19], v[46:47] op_sel_hi:[0,1,1] neg_lo:[0,0,1] neg_hi:[0,0,1]
	v_cvt_pk_bf16_f32 v26, v26, v27
	v_add3_u32 v22, 0, v43, v68
	ds_write_b32 v22, v26 offset:6144
	s_min_i32 s4, s31, -4
	s_add_i32 s4, s4, 6
	v_rcp_f32_e32 v24, v31
	s_nop 0
	v_bitop3_b32 v34, v28, 64, -16 bitop3:0x6c
	s_waitcnt vmcnt(4)
	v_pk_add_f32 v[26:27], v[48:49], v[44:45] neg_lo:[0,1] neg_hi:[0,1]
	global_load_dwordx2 v[14:15], v[14:15], off
	v_pk_add_f32 v[18:19], v[18:19], v[26:27]
	v_cvt_f32_i32_e32 v26, s4
	v_pk_fma_f32 v[24:25], v[24:25], v[18:19], v[48:49] op_sel_hi:[0,1,1] neg_lo:[0,0,1] neg_hi:[0,0,1]
	v_cvt_pk_bf16_f32 v25, v24, v25
	v_add3_u32 v24, 0, v34, v68
	ds_write_b32 v24, v25 offset:8192
	s_min_i32 s4, s31, -5
	s_add_i32 s4, s4, 7
	v_cvt_f32_i32_e32 v31, s4
	v_pk_add_f32 v[36:37], v[50:51], v[46:47] neg_lo:[0,1] neg_hi:[0,1]
	v_rcp_f32_e32 v26, v26
	s_nop 0
	v_pk_add_f32 v[18:19], v[18:19], v[36:37]
	global_load_dwordx2 v[10:11], v[10:11], off
	v_pk_fma_f32 v[26:27], v[26:27], v[18:19], v[50:51] op_sel_hi:[0,1,1] neg_lo:[0,0,1] neg_hi:[0,0,1]
	v_cvt_pk_bf16_f32 v26, v26, v27
	s_movk_i32 s4, 0x50
	v_bitop3_b32 v35, v28, s4, -16 bitop3:0x6c
	v_add3_u32 v25, 0, v35, v68
	ds_write_b32 v25, v26 offset:10240
	s_min_i32 s4, s31, -6
	s_add_i32 s4, s4, 8
	v_rcp_f32_e32 v26, v31
	s_nop 0
	v_cvt_f32_i32_e32 v31, s4
	s_waitcnt vmcnt(5)
	v_pk_add_f32 v[36:37], v[32:33], v[48:49] neg_lo:[0,1] neg_hi:[0,1]
	global_load_dwordx2 v[6:7], v[6:7], off
	v_pk_add_f32 v[18:19], v[18:19], v[36:37]
	s_movk_i32 s4, 0x60
	v_pk_fma_f32 v[26:27], v[26:27], v[18:19], v[32:33] op_sel_hi:[0,1,1] neg_lo:[0,0,1] neg_hi:[0,0,1]
	v_bitop3_b32 v36, v28, s4, -16 bitop3:0x6c
	v_cvt_pk_bf16_f32 v27, v26, v27
	v_add3_u32 v26, 0, v36, v68
	ds_write_b32 v26, v27 offset:12288
	s_min_i32 s4, s31, -7
	s_add_i32 s4, s4, 9
	v_rcp_f32_e32 v42, v31
	s_nop 0
	v_cvt_f32_i32_e32 v27, s4
	s_waitcnt vmcnt(5)
	v_pk_add_f32 v[44:45], v[52:53], v[50:51] neg_lo:[0,1] neg_hi:[0,1]
	s_waitcnt vmcnt(4)
	v_pk_add_f32 v[32:33], v[20:21], v[32:33] neg_lo:[0,1] neg_hi:[0,1]
	v_pk_add_f32 v[18:19], v[18:19], v[44:45]
	global_load_dwordx2 v[4:5], v[4:5], off
	v_pk_fma_f32 v[44:45], v[42:43], v[18:19], v[52:53] op_sel_hi:[0,1,1] neg_lo:[0,0,1] neg_hi:[0,0,1]
	v_cvt_pk_bf16_f32 v39, v44, v45
	s_movk_i32 s4, 0x70
	v_bitop3_b32 v37, v28, s4, -16 bitop3:0x6c
	v_add3_u32 v31, 0, v37, v68
	ds_write_b32 v31, v39 offset:14336
	s_min_i32 s4, s31, -8
	s_add_i32 s4, s4, 10
	v_rcp_f32_e32 v42, v27
	s_nop 0
	v_cvt_f32_i32_e32 v27, s4
	v_pk_add_f32 v[18:19], v[18:19], v[32:33]
	s_min_i32 s8, s31, -15
	v_pk_fma_f32 v[32:33], v[42:43], v[18:19], v[20:21] op_sel_hi:[0,1,1] neg_lo:[0,0,1] neg_hi:[0,0,1]
	s_movk_i32 s4, 0x80
	v_bitop3_b32 v39, v28, s4, -16 bitop3:0x6c
	v_cvt_pk_bf16_f32 v33, v32, v33
	v_add3_u32 v32, 0, v39, v68
	ds_write_b32 v32, v33 offset:16384
	s_min_i32 s4, s31, -9
	s_add_i32 s4, s4, 11
	v_rcp_f32_e32 v42, v27
	s_nop 0
	v_cvt_f32_i32_e32 v27, s4
	s_waitcnt vmcnt(4)
	v_pk_add_f32 v[44:45], v[16:17], v[52:53] neg_lo:[0,1] neg_hi:[0,1]
	s_waitcnt vmcnt(3)
	v_pk_add_f32 v[20:21], v[14:15], v[20:21] neg_lo:[0,1] neg_hi:[0,1]
	v_pk_add_f32 v[18:19], v[18:19], v[44:45]
	s_add_i32 s8, s8, 17
	v_pk_fma_f32 v[44:45], v[42:43], v[18:19], v[16:17] op_sel_hi:[0,1,1] neg_lo:[0,0,1] neg_hi:[0,0,1]
	v_cvt_pk_bf16_f32 v44, v44, v45
	s_movk_i32 s4, 0x90
	v_bitop3_b32 v42, v28, s4, -16 bitop3:0x6c
	v_add3_u32 v33, 0, v42, v68
	ds_write_b32 v33, v44 offset:18432
	s_min_i32 s4, s31, -10
	s_add_i32 s4, s4, 12
	v_rcp_f32_e32 v44, v27
	s_nop 0
	v_cvt_f32_i32_e32 v27, s4
	v_pk_add_f32 v[18:19], v[18:19], v[20:21]
	v_pk_add_f32 v[16:17], v[12:13], v[16:17] neg_lo:[0,1] neg_hi:[0,1]
	v_pk_fma_f32 v[20:21], v[44:45], v[18:19], v[14:15] op_sel_hi:[0,1,1] neg_lo:[0,0,1] neg_hi:[0,0,1]
	v_cvt_pk_bf16_f32 v20, v20, v21
	s_movk_i32 s4, 0xa0
	v_bitop3_b32 v44, v28, s4, -16 bitop3:0x6c
	v_add3_u32 v49, 0, v44, v68
	ds_write_b32 v49, v20 offset:20480
	s_min_i32 s4, s31, -11
	s_add_i32 s4, s4, 13
	v_cvt_f32_i32_e32 v21, s4
	v_rcp_f32_e32 v20, v27
	s_nop 0
	v_pk_add_f32 v[16:17], v[18:19], v[16:17]
	s_waitcnt vmcnt(2)
	v_pk_add_f32 v[14:15], v[10:11], v[14:15] neg_lo:[0,1] neg_hi:[0,1]
	v_pk_fma_f32 v[18:19], v[20:21], v[16:17], v[12:13] op_sel_hi:[0,1,1] neg_lo:[0,0,1] neg_hi:[0,0,1]
	v_cvt_pk_bf16_f32 v18, v18, v19
	s_movk_i32 s4, 0xb0
	v_bitop3_b32 v45, v28, s4, -16 bitop3:0x6c
	v_add3_u32 v27, 0, v45, v68
	ds_write_b32 v27, v18 offset:22528
	s_min_i32 s4, s31, -12
	s_add_i32 s4, s4, 14
	v_cvt_f32_i32_e32 v19, s4
	v_rcp_f32_e32 v18, v21
	s_nop 0
	v_pk_add_f32 v[14:15], v[16:17], v[14:15]
	v_pk_add_f32 v[12:13], v[8:9], v[12:13] neg_lo:[0,1] neg_hi:[0,1]
	v_pk_fma_f32 v[16:17], v[18:19], v[14:15], v[10:11] op_sel_hi:[0,1,1] neg_lo:[0,0,1] neg_hi:[0,0,1]
	v_cvt_pk_bf16_f32 v16, v16, v17
	s_movk_i32 s4, 0xc0
	v_bitop3_b32 v46, v28, s4, -16 bitop3:0x6c
	v_add3_u32 v50, 0, v46, v68
	ds_write_b32 v50, v16 offset:24576
	s_min_i32 s4, s31, -13
	s_add_i32 s4, s4, 15
	v_cvt_f32_i32_e32 v17, s4
	v_rcp_f32_e32 v16, v19
	s_nop 0
	v_pk_add_f32 v[12:13], v[14:15], v[12:13]
	s_waitcnt vmcnt(1)
	v_pk_add_f32 v[10:11], v[6:7], v[10:11] neg_lo:[0,1] neg_hi:[0,1]
	v_pk_fma_f32 v[14:15], v[16:17], v[12:13], v[8:9] op_sel_hi:[0,1,1] neg_lo:[0,0,1] neg_hi:[0,0,1]
	v_cvt_pk_bf16_f32 v14, v14, v15
	s_movk_i32 s4, 0xd0
	v_bitop3_b32 v47, v28, s4, -16 bitop3:0x6c
	v_add3_u32 v51, 0, v47, v68
	ds_write_b32 v51, v14 offset:26624
	s_min_i32 s4, s31, -14
	s_add_i32 s4, s4, 16
	v_cvt_f32_i32_e32 v15, s4
	v_rcp_f32_e32 v14, v17
	s_nop 0
	v_pk_add_f32 v[10:11], v[12:13], v[10:11]
	v_pk_fma_f32 v[12:13], v[14:15], v[10:11], v[6:7] op_sel_hi:[0,1,1] neg_lo:[0,0,1] neg_hi:[0,0,1]
	s_movk_i32 s4, 0xe0
	v_bitop3_b32 v48, v28, s4, -16 bitop3:0x6c
	s_or_b32 s4, s80, 16
	v_cvt_pk_bf16_f32 v12, v12, v13
	v_add3_u32 v52, 0, v48, v68
	s_ashr_i32 s5, s4, 31
	ds_write_b32 v52, v12 offset:28672
	s_lshl_b64 s[4:5], s[4:5], 12
	v_lshl_add_u64 v[12:13], v[2:3], 0, s[4:5]
	global_load_dwordx2 v[54:55], v[12:13], off
	s_waitcnt vmcnt(1)
	v_pk_add_f32 v[8:9], v[4:5], v[8:9] neg_lo:[0,1] neg_hi:[0,1]
	s_movk_i32 s4, 0xf0
	v_rcp_f32_e32 v12, v15
	s_nop 0
	v_pk_add_f32 v[8:9], v[10:11], v[8:9]
	v_bitop3_b32 v69, v28, s4, -16 bitop3:0x6c
	s_or_b32 s4, s80, 17
	v_pk_fma_f32 v[10:11], v[12:13], v[8:9], v[4:5] op_sel_hi:[0,1,1] neg_lo:[0,0,1] neg_hi:[0,0,1]
	s_ashr_i32 s5, s4, 31
	v_cvt_pk_bf16_f32 v10, v10, v11
	v_add3_u32 v28, 0, v69, v68
	s_lshl_b64 s[4:5], s[4:5], 12
	ds_write_b32 v28, v10 offset:30720
	v_lshl_add_u64 v[10:11], v[2:3], 0, s[4:5]
	global_load_dwordx2 v[58:59], v[10:11], off
	s_or_b32 s4, s80, 18
	s_ashr_i32 s5, s4, 31
	s_lshl_b64 s[4:5], s[4:5], 12
	v_lshl_add_u64 v[12:13], v[2:3], 0, s[4:5]
	v_cvt_f32_i32_e32 v53, s8
	global_load_dwordx2 v[62:63], v[12:13], off
	s_or_b32 s4, s80, 19
	s_ashr_i32 s5, s4, 31
	s_lshl_b64 s[4:5], s[4:5], 12
	v_lshl_add_u64 v[14:15], v[2:3], 0, s[4:5]
	s_or_b32 s4, s80, 20
	s_ashr_i32 s5, s4, 31
	s_lshl_b64 s[4:5], s[4:5], 12
	v_lshl_add_u64 v[56:57], v[2:3], 0, s[4:5]
	s_or_b32 s4, s80, 21
	global_load_dwordx2 v[56:57], v[56:57], off
	s_ashr_i32 s5, s4, 31
	s_lshl_b64 s[4:5], s[4:5], 12
	v_lshl_add_u64 v[10:11], v[2:3], 0, s[4:5]
	s_or_b32 s4, s80, 22
	s_ashr_i32 s5, s4, 31
	s_lshl_b64 s[4:5], s[4:5], 12
	s_min_i32 s8, s31, -16
	v_lshl_add_u64 v[60:61], v[2:3], 0, s[4:5]
	s_or_b32 s4, s80, 23
	s_add_i32 s8, s8, 18
	s_ashr_i32 s5, s4, 31
	v_rcp_f32_e32 v64, v53
	s_nop 0
	v_cvt_f32_i32_e32 v53, s8
	s_lshl_b64 s[4:5], s[4:5], 12
	v_lshl_add_u64 v[20:21], v[2:3], 0, s[4:5]
	s_or_b32 s4, s80, 24
	s_ashr_i32 s5, s4, 31
	global_load_dwordx2 v[66:67], v[14:15], off
	s_lshl_b64 s[4:5], s[4:5], 12
	v_lshl_add_u64 v[18:19], v[2:3], 0, s[4:5]
	s_or_b32 s4, s80, 25
	s_ashr_i32 s5, s4, 31
	s_lshl_b64 s[4:5], s[4:5], 12
	v_lshl_add_u64 v[16:17], v[2:3], 0, s[4:5]
	s_or_b32 s4, s80, 26
	s_ashr_i32 s5, s4, 31
	s_lshl_b64 s[4:5], s[4:5], 12
	v_lshl_add_u64 v[12:13], v[2:3], 0, s[4:5]
	global_load_dwordx2 v[20:21], v[20:21], off
	s_waitcnt vmcnt(5)
	v_pk_add_f32 v[6:7], v[54:55], v[6:7] neg_lo:[0,1] neg_hi:[0,1]
	global_load_dwordx2 v[16:17], v[16:17], off
	v_pk_add_f32 v[8:9], v[8:9], v[6:7]
	global_load_dwordx2 v[12:13], v[12:13], off
	v_pk_fma_f32 v[6:7], v[64:65], v[8:9], v[54:55] op_sel_hi:[0,1,1] neg_lo:[0,0,1] neg_hi:[0,0,1]
	v_cvt_pk_bf16_f32 v6, v6, v7
	ds_write_b32 v30, v6 offset:32768
	s_min_i32 s8, s31, 0xffffffef
	s_add_i32 s8, s8, 19
	v_rcp_f32_e32 v30, v53
	s_nop 0
	v_cvt_f32_i32_e32 v53, s8
	s_waitcnt vmcnt(6)
	v_pk_add_f32 v[4:5], v[58:59], v[4:5] neg_lo:[0,1] neg_hi:[0,1]
	global_load_dwordx2 v[60:61], v[60:61], off
	v_pk_add_f32 v[4:5], v[8:9], v[4:5]
	v_pk_fma_f32 v[8:9], v[30:31], v[4:5], v[58:59] op_sel_hi:[0,1,1] neg_lo:[0,0,1] neg_hi:[0,0,1]
	v_cvt_pk_bf16_f32 v8, v8, v9
	ds_write_b32 v23, v8 offset:34816
	global_load_dwordx2 v[64:65], v[10:11], off
	s_or_b32 s4, s80, 27
	s_ashr_i32 s5, s4, 31
	s_lshl_b64 s[4:5], s[4:5], 12
	v_lshl_add_u64 v[14:15], v[2:3], 0, s[4:5]
	s_or_b32 s4, s80, 28
	s_ashr_i32 s5, s4, 31
	s_lshl_b64 s[4:5], s[4:5], 12
	v_lshl_add_u64 v[6:7], v[2:3], 0, s[4:5]
	s_or_b32 s4, s80, 29
	s_ashr_i32 s5, s4, 31
	s_lshl_b64 s[4:5], s[4:5], 12
	s_min_i32 s8, s31, 0xffffffee
	v_lshl_add_u64 v[8:9], v[2:3], 0, s[4:5]
	s_add_i32 s8, s8, 20
	global_load_dwordx2 v[6:7], v[6:7], off
	s_waitcnt vmcnt(8)
	v_pk_add_f32 v[54:55], v[62:63], v[54:55] neg_lo:[0,1] neg_hi:[0,1]
	global_load_dwordx2 v[8:9], v[8:9], off
	v_cvt_f32_i32_e32 v23, s8
	v_rcp_f32_e32 v10, v53
	s_nop 0
	v_pk_add_f32 v[54:55], v[4:5], v[54:55]
	s_or_b32 s4, s80, 30
	v_pk_fma_f32 v[4:5], v[10:11], v[54:55], v[62:63] op_sel_hi:[0,1,1] neg_lo:[0,0,1] neg_hi:[0,0,1]
	v_cvt_pk_bf16_f32 v4, v4, v5
	ds_write_b32 v29, v4 offset:36864
	s_ashr_i32 s5, s4, 31
	s_lshl_b64 s[4:5], s[4:5], 12
	global_load_dwordx2 v[18:19], v[18:19], off
	v_lshl_add_u64 v[10:11], v[2:3], 0, s[4:5]
	s_or_b32 s4, s80, 31
	s_ashr_i32 s5, s4, 31
	s_lshl_b64 s[4:5], s[4:5], 12
	v_lshl_add_u64 v[4:5], v[2:3], 0, s[4:5]
	s_min_i32 s4, s31, 0xffffffed
	s_add_i32 s4, s4, 21
	v_rcp_f32_e32 v30, v23
	s_nop 0
	v_cvt_f32_i32_e32 v23, s4
	s_waitcnt vmcnt(8)
	v_pk_add_f32 v[58:59], v[66:67], v[58:59] neg_lo:[0,1] neg_hi:[0,1]
	global_load_dwordx2 v[14:15], v[14:15], off
	v_pk_add_f32 v[54:55], v[54:55], v[58:59]
	v_pk_fma_f32 v[58:59], v[30:31], v[54:55], v[66:67] op_sel_hi:[0,1,1] neg_lo:[0,0,1] neg_hi:[0,0,1]
	v_cvt_pk_bf16_f32 v30, v58, v59
	ds_write_b32 v22, v30 offset:38912
	s_min_i32 s4, s31, 0xffffffec
	s_add_i32 s4, s4, 22
	v_cvt_f32_i32_e32 v29, s4
	v_pk_add_f32 v[58:59], v[56:57], v[62:63] neg_lo:[0,1] neg_hi:[0,1]
	v_rcp_f32_e32 v22, v23
	s_nop 0
	v_pk_add_f32 v[54:55], v[54:55], v[58:59]
	s_min_i32 s4, s31, 0xffffffeb
	v_pk_fma_f32 v[22:23], v[22:23], v[54:55], v[56:57] op_sel_hi:[0,1,1] neg_lo:[0,0,1] neg_hi:[0,0,1]
	v_cvt_pk_bf16_f32 v22, v22, v23
	ds_write_b32 v24, v22 offset:40960
	s_add_i32 s4, s4, 23
	v_cvt_f32_i32_e32 v24, s4
	v_rcp_f32_e32 v22, v29
	s_nop 0
	s_waitcnt vmcnt(4)
	v_pk_add_f32 v[58:59], v[64:65], v[66:67] neg_lo:[0,1] neg_hi:[0,1]
	v_pk_add_f32 v[54:55], v[54:55], v[58:59]
	s_min_i32 s4, s31, 0xffffffea
	v_pk_fma_f32 v[22:23], v[22:23], v[54:55], v[64:65] op_sel_hi:[0,1,1] neg_lo:[0,0,1] neg_hi:[0,0,1]
	v_cvt_pk_bf16_f32 v22, v22, v23
	ds_write_b32 v25, v22 offset:43008
	s_add_i32 s4, s4, 24
	v_cvt_f32_i32_e32 v29, s4
	v_rcp_f32_e32 v22, v24
	s_nop 0
	v_pk_add_f32 v[24:25], v[60:61], v[56:57] neg_lo:[0,1] neg_hi:[0,1]
	v_pk_add_f32 v[24:25], v[54:55], v[24:25]
	s_min_i32 s4, s31, 0xffffffe9
	v_pk_fma_f32 v[22:23], v[22:23], v[24:25], v[60:61] op_sel_hi:[0,1,1] neg_lo:[0,0,1] neg_hi:[0,0,1]
	v_cvt_pk_bf16_f32 v22, v22, v23
	ds_write_b32 v26, v22 offset:45056
	s_add_i32 s4, s4, 25
	v_cvt_f32_i32_e32 v26, s4
	v_rcp_f32_e32 v22, v29
	s_nop 0
	v_pk_add_f32 v[54:55], v[20:21], v[64:65] neg_lo:[0,1] neg_hi:[0,1]
	v_pk_add_f32 v[24:25], v[24:25], v[54:55]
	s_min_i32 s4, s31, 0xffffffe8
	v_pk_fma_f32 v[22:23], v[22:23], v[24:25], v[20:21] op_sel_hi:[0,1,1] neg_lo:[0,0,1] neg_hi:[0,0,1]
	v_cvt_pk_bf16_f32 v22, v22, v23
	ds_write_b32 v31, v22 offset:47104
	s_add_i32 s4, s4, 26
	v_rcp_f32_e32 v22, v26
	s_nop 0
	v_cvt_f32_i32_e32 v26, s4
	s_waitcnt vmcnt(1)
	v_pk_add_f32 v[30:31], v[18:19], v[60:61] neg_lo:[0,1] neg_hi:[0,1]
	v_pk_add_f32 v[20:21], v[16:17], v[20:21] neg_lo:[0,1] neg_hi:[0,1]
	v_pk_add_f32 v[24:25], v[24:25], v[30:31]
	v_pk_fma_f32 v[22:23], v[22:23], v[24:25], v[18:19] op_sel_hi:[0,1,1] neg_lo:[0,0,1] neg_hi:[0,0,1]
	v_cvt_pk_bf16_f32 v22, v22, v23
	ds_write_b32 v32, v22 offset:49152
	s_min_i32 s4, s31, 0xffffffe7
	s_add_i32 s4, s4, 27
	v_rcp_f32_e32 v22, v26
	s_nop 0
	v_cvt_f32_i32_e32 v26, s4
	v_pk_add_f32 v[20:21], v[24:25], v[20:21]
	v_pk_add_f32 v[18:19], v[12:13], v[18:19] neg_lo:[0,1] neg_hi:[0,1]
	v_pk_fma_f32 v[22:23], v[22:23], v[20:21], v[16:17] op_sel_hi:[0,1,1] neg_lo:[0,0,1] neg_hi:[0,0,1]
	v_cvt_pk_bf16_f32 v22, v22, v23
	ds_write_b32 v33, v22 offset:51200
	s_min_i32 s4, s31, 0xffffffe6
	s_add_i32 s4, s4, 28
	v_cvt_f32_i32_e32 v23, s4
	v_rcp_f32_e32 v22, v26
	s_nop 0
	v_pk_add_f32 v[20:21], v[20:21], v[18:19]
	s_min_i32 s8, s31, 0xffffffe1
	v_pk_fma_f32 v[18:19], v[22:23], v[20:21], v[12:13] op_sel_hi:[0,1,1] neg_lo:[0,0,1] neg_hi:[0,0,1]
	v_cvt_pk_bf16_f32 v18, v18, v19
	ds_write_b32 v49, v18 offset:53248
	global_load_dwordx2 v[18:19], v[10:11], off
	s_waitcnt vmcnt(1)
	v_pk_add_f32 v[16:17], v[14:15], v[16:17] neg_lo:[0,1] neg_hi:[0,1]
	v_pk_add_f32 v[20:21], v[20:21], v[16:17]
	global_load_dwordx2 v[16:17], v[4:5], off
	s_min_i32 s4, s31, 0xffffffe5
	s_add_i32 s4, s4, 29
	v_cvt_f32_i32_e32 v22, s4
	v_rcp_f32_e32 v10, v23
	s_nop 0
	v_pk_fma_f32 v[10:11], v[10:11], v[20:21], v[14:15] op_sel_hi:[0,1,1] neg_lo:[0,0,1] neg_hi:[0,0,1]
	v_cvt_pk_bf16_f32 v4, v10, v11
	ds_write_b32 v27, v4 offset:55296
	s_min_i32 s4, s31, 0xffffffe4
	s_add_i32 s4, s4, 30
	v_rcp_f32_e32 v4, v22
	s_nop 0
	v_cvt_f32_i32_e32 v22, s4
	v_pk_add_f32 v[10:11], v[6:7], v[12:13] neg_lo:[0,1] neg_hi:[0,1]
	s_add_i32 s8, s8, 33
	v_pk_add_f32 v[10:11], v[20:21], v[10:11]
	v_pk_fma_f32 v[4:5], v[4:5], v[10:11], v[6:7] op_sel_hi:[0,1,1] neg_lo:[0,0,1] neg_hi:[0,0,1]
	v_cvt_pk_bf16_f32 v4, v4, v5
	ds_write_b32 v50, v4 offset:57344
	s_min_i32 s4, s31, 0xffffffe3
	s_add_i32 s4, s4, 31
	v_cvt_f32_i32_e32 v20, s4
	v_pk_add_f32 v[12:13], v[8:9], v[14:15] neg_lo:[0,1] neg_hi:[0,1]
	v_rcp_f32_e32 v4, v22
	s_nop 0
	v_pk_add_f32 v[10:11], v[10:11], v[12:13]
	v_pk_fma_f32 v[4:5], v[4:5], v[10:11], v[8:9] op_sel_hi:[0,1,1] neg_lo:[0,0,1] neg_hi:[0,0,1]
	v_cvt_pk_bf16_f32 v4, v4, v5
	ds_write_b32 v51, v4 offset:59392
	s_min_i32 s4, s31, 0xffffffe2
	s_add_i32 s4, s4, 32
	v_cvt_f32_i32_e32 v12, s4
	v_rcp_f32_e32 v4, v20
	s_nop 0
	v_cvt_f32_i32_e32 v49, s8
	s_waitcnt vmcnt(1)
	v_pk_add_f32 v[6:7], v[18:19], v[6:7] neg_lo:[0,1] neg_hi:[0,1]
	s_nop 0
	v_pk_add_f32 v[6:7], v[10:11], v[6:7]
	v_pk_fma_f32 v[4:5], v[4:5], v[6:7], v[18:19] op_sel_hi:[0,1,1] neg_lo:[0,0,1] neg_hi:[0,0,1]
	v_cvt_pk_bf16_f32 v4, v4, v5
	ds_write_b32 v52, v4 offset:61440
	s_waitcnt vmcnt(0)
	v_pk_add_f32 v[8:9], v[16:17], v[8:9] neg_lo:[0,1] neg_hi:[0,1]
	v_rcp_f32_e32 v4, v12
	s_nop 0
	v_pk_add_f32 v[26:27], v[6:7], v[8:9]
	s_or_b32 s4, s80, 32
	v_pk_fma_f32 v[4:5], v[4:5], v[26:27], v[16:17] op_sel_hi:[0,1,1] neg_lo:[0,0,1] neg_hi:[0,0,1]
	s_ashr_i32 s5, s4, 31
	v_cvt_pk_bf16_f32 v4, v4, v5
	s_lshl_b64 s[4:5], s[4:5], 12
	ds_write_b32 v28, v4 offset:63488
	v_lshl_add_u64 v[4:5], v[2:3], 0, s[4:5]
	global_load_dwordx2 v[30:31], v[4:5], off
	s_or_b32 s4, s80, 33
	s_ashr_i32 s5, s4, 31
	s_lshl_b64 s[4:5], s[4:5], 12
	v_lshl_add_u64 v[4:5], v[2:3], 0, s[4:5]
	global_load_dwordx2 v[54:55], v[4:5], off
	s_or_b32 s4, s80, 34
	s_ashr_i32 s5, s4, 31
	s_lshl_b64 s[4:5], s[4:5], 12
	v_lshl_add_u64 v[6:7], v[2:3], 0, s[4:5]
	s_or_b32 s4, s80, 35
	s_ashr_i32 s5, s4, 31
	s_lshl_b64 s[4:5], s[4:5], 12
	v_lshl_add_u64 v[32:33], v[2:3], 0, s[4:5]
	s_or_b32 s4, s80, 36
	s_ashr_i32 s5, s4, 31
	s_lshl_b64 s[4:5], s[4:5], 12
	v_lshl_add_u64 v[50:51], v[2:3], 0, s[4:5]
	s_or_b32 s4, s80, 37
	s_ashr_i32 s5, s4, 31
	s_lshl_b64 s[4:5], s[4:5], 12
	v_lshl_add_u64 v[52:53], v[2:3], 0, s[4:5]
	s_or_b32 s4, s80, 38
	s_ashr_i32 s5, s4, 31
	s_lshl_b64 s[4:5], s[4:5], 12
	v_lshl_add_u64 v[28:29], v[2:3], 0, s[4:5]
	s_or_b32 s4, s80, 39
	s_ashr_i32 s5, s4, 31
	s_lshl_b64 s[4:5], s[4:5], 12
	v_lshl_add_u64 v[24:25], v[2:3], 0, s[4:5]
	s_or_b32 s4, s80, 40
	s_ashr_i32 s5, s4, 31
	s_lshl_b64 s[4:5], s[4:5], 12
	v_lshl_add_u64 v[22:23], v[2:3], 0, s[4:5]
	s_or_b32 s4, s80, 41
	global_load_dwordx2 v[56:57], v[6:7], off
	s_ashr_i32 s5, s4, 31
	s_lshl_b64 s[4:5], s[4:5], 12
	v_lshl_add_u64 v[20:21], v[2:3], 0, s[4:5]
	s_or_b32 s4, s80, 42
	s_ashr_i32 s5, s4, 31
	s_lshl_b64 s[4:5], s[4:5], 12
	v_lshl_add_u64 v[14:15], v[2:3], 0, s[4:5]
	s_or_b32 s4, s80, 43
	s_ashr_i32 s5, s4, 31
	s_lshl_b64 s[4:5], s[4:5], 12
	v_lshl_add_u64 v[12:13], v[2:3], 0, s[4:5]
	s_or_b32 s4, s80, 44
	s_ashr_i32 s5, s4, 31
	s_lshl_b64 s[4:5], s[4:5], 12
	v_lshl_add_u64 v[10:11], v[2:3], 0, s[4:5]
	s_or_b32 s4, s80, 45
	s_ashr_i32 s5, s4, 31
	s_lshl_b64 s[4:5], s[4:5], 12
	v_lshl_add_u64 v[8:9], v[2:3], 0, s[4:5]
	s_or_b32 s4, s80, 46
	s_ashr_i32 s5, s4, 31
	s_lshl_b64 s[4:5], s[4:5], 12
	global_load_dwordx2 v[32:33], v[32:33], off
	global_load_dwordx2 v[12:13], v[12:13], off
	global_load_dwordx2 v[8:9], v[8:9], off
	v_lshl_add_u64 v[6:7], v[2:3], 0, s[4:5]
	s_or_b32 s4, s80, 47
	s_ashr_i32 s5, s4, 31
	s_lshl_b64 s[4:5], s[4:5], 12
	v_lshl_add_u64 v[4:5], v[2:3], 0, s[4:5]
	s_min_i32 s4, s31, 0xffffffe0
	s_add_i32 s4, s4, 34
	v_rcp_f32_e32 v58, v49
	s_nop 0
	v_cvt_f32_i32_e32 v49, s4
	s_waitcnt vmcnt(5)
	v_pk_add_f32 v[18:19], v[30:31], v[18:19] neg_lo:[0,1] neg_hi:[0,1]
	global_load_dwordx2 v[28:29], v[28:29], off
	v_pk_add_f32 v[18:19], v[26:27], v[18:19]
	v_pk_fma_f32 v[26:27], v[58:59], v[18:19], v[30:31] op_sel_hi:[0,1,1] neg_lo:[0,0,1] neg_hi:[0,0,1]
	v_readlane_b32 s4, v254, 19
	v_cvt_pk_bf16_f32 v26, v26, v27
	s_waitcnt vmcnt(5)
	v_pk_add_f32 v[16:17], v[54:55], v[16:17] neg_lo:[0,1] neg_hi:[0,1]
	v_add3_u32 v27, s4, v38, v68
	ds_write_b32 v27, v26
	global_load_dwordx2 v[26:27], v[50:51], off
	s_min_i32 s4, s31, 0xffffffdf
	s_add_i32 s4, s4, 35
	v_rcp_f32_e32 v50, v49
	s_nop 0
	v_cvt_f32_i32_e32 v49, s4
	v_pk_add_f32 v[16:17], v[18:19], v[16:17]
	global_load_dwordx2 v[24:25], v[24:25], off
	v_pk_fma_f32 v[18:19], v[50:51], v[16:17], v[54:55] op_sel_hi:[0,1,1] neg_lo:[0,0,1] neg_hi:[0,0,1]
	v_readlane_b32 s4, v254, 21
	v_cvt_pk_bf16_f32 v18, v18, v19
	s_nop 1
	v_add3_u32 v19, s4, v40, v68
	ds_write_b32 v19, v18
	global_load_dwordx2 v[18:19], v[52:53], off
	s_min_i32 s4, s31, 0xffffffde
	s_add_i32 s4, s4, 36
	v_rcp_f32_e32 v50, v49
	s_nop 0
	v_cvt_f32_i32_e32 v49, s4
	s_waitcnt vmcnt(7)
	v_pk_add_f32 v[30:31], v[56:57], v[30:31] neg_lo:[0,1] neg_hi:[0,1]
	global_load_dwordx2 v[22:23], v[22:23], off
	v_pk_add_f32 v[16:17], v[16:17], v[30:31]
	global_load_dwordx2 v[20:21], v[20:21], off
	v_pk_fma_f32 v[30:31], v[50:51], v[16:17], v[56:57] op_sel_hi:[0,1,1] neg_lo:[0,0,1] neg_hi:[0,0,1]
	v_readlane_b32 s4, v254, 23
	v_cvt_pk_bf16_f32 v30, v30, v31
	global_load_dwordx2 v[14:15], v[14:15], off
	v_add3_u32 v31, s4, v41, v68
	ds_write_b32 v31, v30
	s_min_i32 s4, s31, 0xffffffdd
	s_add_i32 s4, s4, 37
	v_rcp_f32_e32 v30, v49
	s_nop 0
	v_cvt_f32_i32_e32 v49, s4
	s_waitcnt vmcnt(9)
	v_pk_add_f32 v[50:51], v[32:33], v[54:55] neg_lo:[0,1] neg_hi:[0,1]
	global_load_dwordx2 v[10:11], v[10:11], off
	v_pk_add_f32 v[16:17], v[16:17], v[50:51]
	v_pk_fma_f32 v[30:31], v[30:31], v[16:17], v[32:33] op_sel_hi:[0,1,1] neg_lo:[0,0,1] neg_hi:[0,0,1]
	v_readlane_b32 s4, v254, 25
	v_cvt_pk_bf16_f32 v30, v30, v31
	s_min_i32 s8, s31, 0xffffffd1
	v_add3_u32 v31, s4, v43, v68
	ds_write_b32 v31, v30
	s_min_i32 s4, s31, 0xffffffdc
	s_add_i32 s4, s4, 38
	v_rcp_f32_e32 v30, v49
	s_nop 0
	v_cvt_f32_i32_e32 v49, s4
	s_waitcnt vmcnt(6)
	v_pk_add_f32 v[50:51], v[26:27], v[56:57] neg_lo:[0,1] neg_hi:[0,1]
	s_add_i32 s8, s8, 49
	v_pk_add_f32 v[16:17], v[16:17], v[50:51]
	v_pk_fma_f32 v[30:31], v[30:31], v[16:17], v[26:27] op_sel_hi:[0,1,1] neg_lo:[0,0,1] neg_hi:[0,0,1]
	v_readlane_b32 s4, v254, 29
	v_cvt_pk_bf16_f32 v30, v30, v31
	v_pk_add_f32 v[26:27], v[28:29], v[26:27] neg_lo:[0,1] neg_hi:[0,1]
	v_add3_u32 v31, s4, v34, v68
	ds_write_b32 v31, v30
	s_min_i32 s4, s31, 0xffffffdb
	s_add_i32 s4, s4, 39
	v_rcp_f32_e32 v30, v49
	s_nop 0
	v_cvt_f32_i32_e32 v49, s4
	s_waitcnt vmcnt(4)
	v_pk_add_f32 v[32:33], v[18:19], v[32:33] neg_lo:[0,1] neg_hi:[0,1]
	s_nop 0
	v_pk_add_f32 v[16:17], v[16:17], v[32:33]
	v_pk_fma_f32 v[30:31], v[30:31], v[16:17], v[18:19] op_sel_hi:[0,1,1] neg_lo:[0,0,1] neg_hi:[0,0,1]
	v_readlane_b32 s4, v254, 31
	v_cvt_pk_bf16_f32 v30, v30, v31
	v_pk_add_f32 v[16:17], v[16:17], v[26:27]
	v_add3_u32 v31, s4, v35, v68
	ds_write_b32 v31, v30
	s_min_i32 s4, s31, 0xffffffda
	s_add_i32 s4, s4, 40
	v_cvt_f32_i32_e32 v31, s4
	v_rcp_f32_e32 v30, v49
	s_nop 0
	v_pk_add_f32 v[18:19], v[24:25], v[18:19] neg_lo:[0,1] neg_hi:[0,1]
	v_cvt_f32_i32_e32 v49, s8
	v_pk_fma_f32 v[26:27], v[30:31], v[16:17], v[28:29] op_sel_hi:[0,1,1] neg_lo:[0,0,1] neg_hi:[0,0,1]
	v_readlane_b32 s4, v254, 33
	v_cvt_pk_bf16_f32 v26, v26, v27
	v_pk_add_f32 v[16:17], v[16:17], v[18:19]
	v_add3_u32 v27, s4, v36, v68
	ds_write_b32 v27, v26
	s_min_i32 s4, s31, 0xffffffd9
	s_add_i32 s4, s4, 41
	v_cvt_f32_i32_e32 v27, s4
	v_rcp_f32_e32 v26, v31
	s_nop 0
	s_min_i32 s8, s31, 0xffffffd0
	s_add_i32 s8, s8, 50
	v_pk_fma_f32 v[18:19], v[26:27], v[16:17], v[24:25] op_sel_hi:[0,1,1] neg_lo:[0,0,1] neg_hi:[0,0,1]
	v_readlane_b32 s4, v254, 35
	v_cvt_pk_bf16_f32 v18, v18, v19
	s_waitcnt vmcnt(2)
	v_pk_add_f32 v[24:25], v[20:21], v[24:25] neg_lo:[0,1] neg_hi:[0,1]
	v_add3_u32 v19, s4, v37, v68
	ds_write_b32 v19, v18
	s_min_i32 s4, s31, 0xffffffd8
	s_add_i32 s4, s4, 42
	v_rcp_f32_e32 v18, v27
	s_nop 0
	v_pk_add_f32 v[26:27], v[22:23], v[28:29] neg_lo:[0,1] neg_hi:[0,1]
	v_cvt_f32_i32_e32 v28, s4
	v_pk_add_f32 v[16:17], v[16:17], v[26:27]
	global_load_dwordx2 v[30:31], v[4:5], off
	v_pk_fma_f32 v[18:19], v[18:19], v[16:17], v[22:23] op_sel_hi:[0,1,1] neg_lo:[0,0,1] neg_hi:[0,0,1]
	v_readlane_b32 s4, v254, 37
	v_cvt_pk_bf16_f32 v18, v18, v19
	v_pk_add_f32 v[16:17], v[16:17], v[24:25]
	v_add3_u32 v19, s4, v39, v68
	ds_write_b32 v19, v18
	v_rcp_f32_e32 v18, v28
	s_nop 0
	global_load_dwordx2 v[28:29], v[6:7], off
	s_min_i32 s4, s31, 0xffffffd7
	s_add_i32 s4, s4, 43
	v_cvt_f32_i32_e32 v26, s4
	v_pk_fma_f32 v[18:19], v[18:19], v[16:17], v[20:21] op_sel_hi:[0,1,1] neg_lo:[0,0,1] neg_hi:[0,0,1]
	v_cvt_pk_bf16_f32 v18, v18, v19
	s_waitcnt vmcnt(3)
	v_pk_add_f32 v[22:23], v[14:15], v[22:23] neg_lo:[0,1] neg_hi:[0,1]
	v_readlane_b32 s4, v254, 39
	v_pk_add_f32 v[16:17], v[16:17], v[22:23]
	v_add3_u32 v35, s77, v35, v68
	v_add3_u32 v19, s4, v42, v68
	ds_write_b32 v19, v18
	s_min_i32 s4, s31, 0xffffffd6
	s_add_i32 s4, s4, 44
	v_cvt_f32_i32_e32 v24, s4
	v_rcp_f32_e32 v18, v26
	s_nop 0
	v_pk_fma_f32 v[18:19], v[18:19], v[16:17], v[14:15] op_sel_hi:[0,1,1] neg_lo:[0,0,1] neg_hi:[0,0,1]
	v_readlane_b32 s4, v254, 41
	v_cvt_pk_bf16_f32 v18, v18, v19
	s_nop 1
	v_add3_u32 v19, s4, v44, v68
	ds_write_b32 v19, v18
	s_min_i32 s4, s31, 0xffffffd5
	s_add_i32 s4, s4, 45
	v_pk_add_f32 v[18:19], v[12:13], v[20:21] neg_lo:[0,1] neg_hi:[0,1]
	v_cvt_f32_i32_e32 v20, s4
	v_pk_add_f32 v[16:17], v[16:17], v[18:19]
	v_rcp_f32_e32 v6, v24
	s_nop 0
	v_pk_fma_f32 v[6:7], v[6:7], v[16:17], v[12:13] op_sel_hi:[0,1,1] neg_lo:[0,0,1] neg_hi:[0,0,1]
	v_readlane_b32 s4, v254, 43
	v_cvt_pk_bf16_f32 v6, v6, v7
	s_nop 1
	v_add3_u32 v7, s4, v45, v68
	ds_write_b32 v7, v6
	s_min_i32 s4, s31, 0xffffffd4
	s_add_i32 s4, s4, 46
	s_waitcnt vmcnt(2)
	v_pk_add_f32 v[6:7], v[10:11], v[14:15] neg_lo:[0,1] neg_hi:[0,1]
	v_cvt_f32_i32_e32 v14, s4
	v_pk_add_f32 v[6:7], v[16:17], v[6:7]
	v_rcp_f32_e32 v4, v20
	s_nop 0
	v_pk_fma_f32 v[4:5], v[4:5], v[6:7], v[10:11] op_sel_hi:[0,1,1] neg_lo:[0,0,1] neg_hi:[0,0,1]
	v_readlane_b32 s4, v254, 45
	v_cvt_pk_bf16_f32 v4, v4, v5
	v_pk_add_f32 v[12:13], v[8:9], v[12:13] neg_lo:[0,1] neg_hi:[0,1]
	v_add3_u32 v5, s4, v46, v68
	ds_write_b32 v5, v4
	s_min_i32 s4, s31, 0xffffffd3
	s_add_i32 s4, s4, 47
	v_rcp_f32_e32 v4, v14
	s_nop 0
	v_cvt_f32_i32_e32 v14, s4
	v_pk_add_f32 v[6:7], v[6:7], v[12:13]
	s_waitcnt vmcnt(0)
	v_pk_add_f32 v[10:11], v[28:29], v[10:11] neg_lo:[0,1] neg_hi:[0,1]
	v_pk_fma_f32 v[4:5], v[4:5], v[6:7], v[8:9] op_sel_hi:[0,1,1] neg_lo:[0,0,1] neg_hi:[0,0,1]
	v_readlane_b32 s4, v254, 47
	v_cvt_pk_bf16_f32 v4, v4, v5
	v_pk_add_f32 v[6:7], v[6:7], v[10:11]
	v_add3_u32 v5, s4, v47, v68
	ds_write_b32 v5, v4
	s_min_i32 s4, s31, 0xffffffd2
	s_add_i32 s4, s4, 48
	v_cvt_f32_i32_e32 v12, s4
	v_rcp_f32_e32 v4, v14
	s_nop 0
	v_pk_fma_f32 v[4:5], v[4:5], v[6:7], v[28:29] op_sel_hi:[0,1,1] neg_lo:[0,0,1] neg_hi:[0,0,1]
	v_readlane_b32 s4, v254, 49
	v_cvt_pk_bf16_f32 v4, v4, v5
	v_pk_add_f32 v[8:9], v[30:31], v[8:9] neg_lo:[0,1] neg_hi:[0,1]
	v_add3_u32 v5, s4, v48, v68
	ds_write_b32 v5, v4
	s_or_b32 s4, s80, 48
	s_ashr_i32 s5, s4, 31
	v_rcp_f32_e32 v4, v12
	s_nop 0
	v_pk_add_f32 v[32:33], v[6:7], v[8:9]
	s_lshl_b64 s[4:5], s[4:5], 12
	v_lshl_add_u64 v[6:7], v[2:3], 0, s[4:5]
	v_pk_fma_f32 v[4:5], v[4:5], v[32:33], v[30:31] op_sel_hi:[0,1,1] neg_lo:[0,0,1] neg_hi:[0,0,1]
	v_readlane_b32 s4, v254, 51
	v_cvt_pk_bf16_f32 v4, v4, v5
	global_load_dwordx2 v[50:51], v[6:7], off
	v_add3_u32 v5, s4, v69, v68
	s_or_b32 s4, s80, 49
	s_ashr_i32 s5, s4, 31
	s_lshl_b64 s[4:5], s[4:5], 12
	v_lshl_add_u64 v[6:7], v[2:3], 0, s[4:5]
	s_or_b32 s4, s80, 50
	s_ashr_i32 s5, s4, 31
	s_lshl_b64 s[4:5], s[4:5], 12
	v_lshl_add_u64 v[20:21], v[2:3], 0, s[4:5]
	s_or_b32 s4, s80, 51
	s_ashr_i32 s5, s4, 31
	s_lshl_b64 s[4:5], s[4:5], 12
	v_lshl_add_u64 v[52:53], v[2:3], 0, s[4:5]
	s_or_b32 s4, s80, 52
	s_ashr_i32 s5, s4, 31
	s_lshl_b64 s[4:5], s[4:5], 12
	ds_write_b32 v5, v4
	v_lshl_add_u64 v[4:5], v[2:3], 0, s[4:5]
	s_or_b32 s4, s80, 53
	s_ashr_i32 s5, s4, 31
	s_lshl_b64 s[4:5], s[4:5], 12
	v_lshl_add_u64 v[18:19], v[2:3], 0, s[4:5]
	s_or_b32 s4, s80, 54
	s_ashr_i32 s5, s4, 31
	s_lshl_b64 s[4:5], s[4:5], 12
	v_lshl_add_u64 v[14:15], v[2:3], 0, s[4:5]
	s_or_b32 s4, s80, 55
	s_ashr_i32 s5, s4, 31
	s_lshl_b64 s[4:5], s[4:5], 12
	global_load_dwordx2 v[54:55], v[6:7], off
	v_lshl_add_u64 v[16:17], v[2:3], 0, s[4:5]
	s_or_b32 s4, s80, 56
	s_ashr_i32 s5, s4, 31
	s_lshl_b64 s[4:5], s[4:5], 12
	v_lshl_add_u64 v[10:11], v[2:3], 0, s[4:5]
	s_or_b32 s4, s80, 57
	s_ashr_i32 s5, s4, 31
	s_lshl_b64 s[4:5], s[4:5], 12
	v_lshl_add_u64 v[12:13], v[2:3], 0, s[4:5]
	s_or_b32 s4, s80, 58
	s_ashr_i32 s5, s4, 31
	s_lshl_b64 s[4:5], s[4:5], 12
	v_lshl_add_u64 v[8:9], v[2:3], 0, s[4:5]
	s_or_b32 s4, s80, 59
	s_ashr_i32 s5, s4, 31
	s_lshl_b64 s[4:5], s[4:5], 12
	v_lshl_add_u64 v[24:25], v[2:3], 0, s[4:5]
	s_or_b32 s4, s80, 60
	s_ashr_i32 s5, s4, 31
	s_lshl_b64 s[4:5], s[4:5], 12
	v_lshl_add_u64 v[22:23], v[2:3], 0, s[4:5]
	global_load_dwordx2 v[14:15], v[14:15], off
	s_or_b32 s4, s80, 61
	global_load_dwordx2 v[22:23], v[22:23], off
	s_ashr_i32 s5, s4, 31
	global_load_dwordx2 v[6:7], v[20:21], off
	s_lshl_b64 s[4:5], s[4:5], 12
	global_load_dwordx2 v[12:13], v[12:13], off
	v_lshl_add_u64 v[26:27], v[2:3], 0, s[4:5]
	global_load_dwordx2 v[20:21], v[52:53], off
	global_load_dwordx2 v[18:19], v[18:19], off
	v_rcp_f32_e32 v52, v49
	s_nop 0
	v_cvt_f32_i32_e32 v49, s8
	global_load_dwordx2 v[16:17], v[16:17], off
	s_or_b32 s4, s80, 62
	global_load_dwordx2 v[26:27], v[26:27], off
	s_ashr_i32 s5, s4, 31
	s_waitcnt vmcnt(9)
	v_pk_add_f32 v[28:29], v[50:51], v[28:29] neg_lo:[0,1] neg_hi:[0,1]
	global_load_dwordx2 v[10:11], v[10:11], off
	v_pk_add_f32 v[28:29], v[32:33], v[28:29]
	global_load_dwordx2 v[24:25], v[24:25], off
	v_pk_fma_f32 v[32:33], v[52:53], v[28:29], v[50:51] op_sel_hi:[0,1,1] neg_lo:[0,0,1] neg_hi:[0,0,1]
	v_readlane_b32 s8, v254, 53
	v_cvt_pk_bf16_f32 v32, v32, v33
	global_load_dwordx2 v[8:9], v[8:9], off
	v_add3_u32 v33, s8, v38, v68
	ds_write_b32 v33, v32
	s_min_i32 s8, s31, 0xffffffcf
	s_add_i32 s8, s8, 51
	v_cvt_f32_i32_e32 v33, s8
	v_rcp_f32_e32 v32, v49
	s_nop 0
	s_lshl_b64 s[4:5], s[4:5], 12
	v_add3_u32 v39, s33, v39, v68
	v_add3_u32 v37, s94, v37, v68
	v_add3_u32 v45, s96, v45, v68
	s_waitcnt vmcnt(11)
	v_pk_add_f32 v[30:31], v[54:55], v[30:31] neg_lo:[0,1] neg_hi:[0,1]
	v_add3_u32 v47, s36, v47, v68
	v_pk_add_f32 v[28:29], v[28:29], v[30:31]
	v_add3_u32 v48, s37, v48, v68
	v_pk_fma_f32 v[30:31], v[32:33], v[28:29], v[54:55] op_sel_hi:[0,1,1] neg_lo:[0,0,1] neg_hi:[0,0,1]
	v_cvt_pk_bf16_f32 v30, v30, v31
	v_add3_u32 v31, s24, v40, v68
	ds_write_b32 v31, v30
	s_min_i32 s8, s31, 0xffffffce
	s_add_i32 s8, s8, 52
	v_cvt_f32_i32_e32 v38, s8
	v_rcp_f32_e32 v30, v33
	s_nop 0
	s_waitcnt vmcnt(8)
	v_pk_add_f32 v[32:33], v[6:7], v[50:51] neg_lo:[0,1] neg_hi:[0,1]
	s_nop 0
	v_pk_add_f32 v[28:29], v[28:29], v[32:33]
	v_pk_fma_f32 v[30:31], v[30:31], v[28:29], v[6:7] op_sel_hi:[0,1,1] neg_lo:[0,0,1] neg_hi:[0,0,1]
	v_cvt_pk_bf16_f32 v30, v30, v31
	v_add3_u32 v31, s25, v41, v68
	ds_write_b32 v31, v30
	s_min_i32 s8, s31, 0xffffffcd
	s_add_i32 s8, s8, 53
	v_rcp_f32_e32 v30, v38
	s_nop 0
	v_cvt_f32_i32_e32 v38, s8
	s_waitcnt vmcnt(6)
	v_pk_add_f32 v[32:33], v[20:21], v[54:55] neg_lo:[0,1] neg_hi:[0,1]
	s_nop 0
	v_pk_add_f32 v[28:29], v[28:29], v[32:33]
	v_pk_fma_f32 v[30:31], v[30:31], v[28:29], v[20:21] op_sel_hi:[0,1,1] neg_lo:[0,0,1] neg_hi:[0,0,1]
	s_min_i32 s8, s31, 0xffffffcc
	v_cvt_pk_bf16_f32 v30, v30, v31
	v_add3_u32 v31, s26, v43, v68
	s_add_i32 s8, s8, 54
	ds_write_b32 v31, v30
	v_cvt_f32_i32_e32 v40, s8
	s_min_i32 s8, s31, 0xffffffcb
	s_add_i32 s8, s8, 55
	v_cvt_f32_i32_e32 v50, s8
	s_min_i32 s8, s31, 0xffffffca
	s_add_i32 s8, s8, 56
	v_cvt_f32_i32_e32 v43, s8
	s_min_i32 s8, s31, 0xffffffc9
	s_add_i32 s8, s8, 57
	v_cvt_f32_i32_e32 v54, s8
	s_min_i32 s8, s31, 0xffffffc8
	s_add_i32 s8, s8, 58
	v_cvt_f32_i32_e32 v52, s8
	s_min_i32 s8, s31, 0xffffffc7
	s_add_i32 s8, s8, 59
	v_cvt_f32_i32_e32 v58, s8
	s_min_i32 s8, s31, 0xffffffc6
	s_add_i32 s8, s8, 60
	v_cvt_f32_i32_e32 v56, s8
	s_min_i32 s8, s31, 0xffffffc5
	global_load_dwordx2 v[30:31], v[4:5], off
	s_add_i32 s8, s8, 61
	v_cvt_f32_i32_e32 v62, s8
	s_min_i32 s8, s31, 0xffffffc4
	s_add_i32 s8, s8, 62
	v_cvt_f32_i32_e32 v63, s8
	s_min_i32 s8, s31, 0xffffffc3
	s_add_i32 s8, s8, 63
	v_cvt_f32_i32_e32 v66, s8
	v_lshl_add_u64 v[4:5], v[2:3], 0, s[4:5]
	global_load_dwordx2 v[32:33], v[4:5], off
	s_or_b32 s4, s80, 63
	s_ashr_i32 s5, s4, 31
	s_lshl_b64 s[4:5], s[4:5], 12
	v_lshl_add_u64 v[2:3], v[2:3], 0, s[4:5]
	global_load_dwordx2 v[4:5], v[2:3], off
	v_rcp_f32_e32 v2, v38
	s_nop 0
	v_add3_u32 v49, s27, v34, v68
	v_rcp_f32_e32 v34, v40
	s_nop 0
	v_rcp_f32_e32 v40, v54
	s_nop 0
	v_rcp_f32_e32 v54, v66
	s_nop 0
	v_rcp_f32_e32 v38, v50
	s_nop 0
	v_add3_u32 v41, s91, v36, v68
	v_rcp_f32_e32 v36, v43
	s_nop 0
	v_rcp_f32_e32 v50, v52
	s_nop 0
	v_add3_u32 v51, s95, v44, v68
	v_add3_u32 v43, s75, v42, v68
	v_rcp_f32_e32 v42, v58
	s_nop 0
	v_rcp_f32_e32 v44, v56
	s_nop 0
	v_rcp_f32_e32 v52, v62
	s_nop 0
	v_add3_u32 v53, s97, v46, v68
	v_rcp_f32_e32 v46, v63
	s_nop 0
	s_min_i32 s4, s31, 0xffffffc2
	s_waitcnt vmcnt(2)
	v_pk_add_f32 v[6:7], v[30:31], v[6:7] neg_lo:[0,1] neg_hi:[0,1]
	s_nop 0
	v_pk_add_f32 v[6:7], v[28:29], v[6:7]
	s_nop 0
	v_pk_fma_f32 v[2:3], v[2:3], v[6:7], v[30:31] op_sel_hi:[0,1,1] neg_lo:[0,0,1] neg_hi:[0,0,1]
	v_cvt_pk_bf16_f32 v2, v2, v3
	ds_write_b32 v49, v2
	v_pk_add_f32 v[2:3], v[18:19], v[20:21] neg_lo:[0,1] neg_hi:[0,1]
	s_nop 0
	v_pk_add_f32 v[2:3], v[6:7], v[2:3]
	s_nop 0
	v_pk_fma_f32 v[6:7], v[34:35], v[2:3], v[18:19] op_sel_hi:[0,1,1] neg_lo:[0,0,1] neg_hi:[0,0,1]
	v_cvt_pk_bf16_f32 v6, v6, v7
	ds_write_b32 v35, v6
	v_pk_add_f32 v[6:7], v[14:15], v[30:31] neg_lo:[0,1] neg_hi:[0,1]
	s_nop 0
	v_pk_add_f32 v[2:3], v[2:3], v[6:7]
	s_nop 0
	v_pk_fma_f32 v[6:7], v[38:39], v[2:3], v[14:15] op_sel_hi:[0,1,1] neg_lo:[0,0,1] neg_hi:[0,0,1]
	v_cvt_pk_bf16_f32 v6, v6, v7
	ds_write_b32 v41, v6
	v_pk_add_f32 v[6:7], v[16:17], v[18:19] neg_lo:[0,1] neg_hi:[0,1]
	s_nop 0
	v_pk_add_f32 v[2:3], v[2:3], v[6:7]
	s_nop 0
	v_pk_fma_f32 v[6:7], v[36:37], v[2:3], v[16:17] op_sel_hi:[0,1,1] neg_lo:[0,0,1] neg_hi:[0,0,1]
	v_cvt_pk_bf16_f32 v6, v6, v7
	ds_write_b32 v37, v6
	v_pk_add_f32 v[6:7], v[10:11], v[14:15] neg_lo:[0,1] neg_hi:[0,1]
	s_nop 0
	v_pk_add_f32 v[2:3], v[2:3], v[6:7]
	s_nop 0
	v_pk_fma_f32 v[6:7], v[40:41], v[2:3], v[10:11] op_sel_hi:[0,1,1] neg_lo:[0,0,1] neg_hi:[0,0,1]
	v_cvt_pk_bf16_f32 v6, v6, v7
	ds_write_b32 v39, v6
	v_pk_add_f32 v[6:7], v[12:13], v[16:17] neg_lo:[0,1] neg_hi:[0,1]
	s_nop 0
	v_pk_add_f32 v[2:3], v[2:3], v[6:7]
	s_nop 0
	v_pk_fma_f32 v[6:7], v[50:51], v[2:3], v[12:13] op_sel_hi:[0,1,1] neg_lo:[0,0,1] neg_hi:[0,0,1]
	v_cvt_pk_bf16_f32 v6, v6, v7
	ds_write_b32 v43, v6
	v_pk_add_f32 v[6:7], v[8:9], v[10:11] neg_lo:[0,1] neg_hi:[0,1]
	s_nop 0
	v_pk_add_f32 v[2:3], v[2:3], v[6:7]
	s_nop 0
	v_pk_fma_f32 v[6:7], v[42:43], v[2:3], v[8:9] op_sel_hi:[0,1,1] neg_lo:[0,0,1] neg_hi:[0,0,1]
	v_cvt_pk_bf16_f32 v6, v6, v7
	ds_write_b32 v51, v6
	v_pk_add_f32 v[6:7], v[24:25], v[12:13] neg_lo:[0,1] neg_hi:[0,1]
	s_nop 0
	v_pk_add_f32 v[2:3], v[2:3], v[6:7]
	s_nop 0
	v_pk_fma_f32 v[6:7], v[44:45], v[2:3], v[24:25] op_sel_hi:[0,1,1] neg_lo:[0,0,1] neg_hi:[0,0,1]
	v_cvt_pk_bf16_f32 v6, v6, v7
	ds_write_b32 v45, v6
	v_pk_add_f32 v[6:7], v[22:23], v[8:9] neg_lo:[0,1] neg_hi:[0,1]
	s_nop 0
	v_pk_add_f32 v[2:3], v[2:3], v[6:7]
	s_nop 0
	v_pk_fma_f32 v[6:7], v[52:53], v[2:3], v[22:23] op_sel_hi:[0,1,1] neg_lo:[0,0,1] neg_hi:[0,0,1]
	v_cvt_pk_bf16_f32 v6, v6, v7
	ds_write_b32 v53, v6
	v_pk_add_f32 v[6:7], v[26:27], v[24:25] neg_lo:[0,1] neg_hi:[0,1]
	s_nop 0
	v_pk_add_f32 v[2:3], v[2:3], v[6:7]
	s_nop 0
	v_pk_fma_f32 v[6:7], v[46:47], v[2:3], v[26:27] op_sel_hi:[0,1,1] neg_lo:[0,0,1] neg_hi:[0,0,1]
	v_cvt_pk_bf16_f32 v6, v6, v7
	ds_write_b32 v47, v6
	s_waitcnt vmcnt(1)
	v_pk_add_f32 v[6:7], v[32:33], v[22:23] neg_lo:[0,1] neg_hi:[0,1]
	s_nop 0
	v_pk_add_f32 v[2:3], v[2:3], v[6:7]
	s_nop 0
	v_pk_fma_f32 v[6:7], v[54:55], v[2:3], v[32:33] op_sel_hi:[0,1,1] neg_lo:[0,0,1] neg_hi:[0,0,1]
	v_cvt_pk_bf16_f32 v6, v6, v7
	ds_write_b32 v48, v6
	s_waitcnt vmcnt(0)
	v_pk_add_f32 v[6:7], v[4:5], v[26:27] neg_lo:[0,1] neg_hi:[0,1]
	s_nop 0
	v_pk_add_f32 v[6:7], v[2:3], v[6:7]
	v_mov_b32_e32 v3, s4
.LBB0_118:
	v_add_u32_e32 v2, 64, v3
	v_cvt_f32_i32_e32 v2, v2
	s_bfe_u32 s10, s29, 0x10006
	s_lshl_b32 s11, s65, 5
	v_and_b32_e32 v214, 63, v221
	v_readlane_b32 s4, v254, 55
	s_nop 1
	v_add3_u32 v9, s4, v69, v68
	s_lshl_b32 s4, s65, 16
	s_lshl_b32 s5, s10, 15
	s_or_b32 s4, s5, s4
	s_ashr_i32 s5, s4, 31
	s_lshl_b64 s[4:5], s[4:5], 1
	v_rcp_f32_e32 v2, v2
	s_nop 0
	s_waitcnt lgkmcnt(0)
	s_add_u32 s8, s16, s4
	v_pk_fma_f32 v[2:3], v[6:7], v[2:3], v[4:5] op_sel_hi:[1,0,1] neg_lo:[0,0,1] neg_hi:[0,0,1]
	s_addc_u32 s9, s17, s5
	v_lshlrev_b32_e32 v212, 4, v214
	v_cvt_pk_bf16_f32 v2, v2, v3
	v_lshl_add_u64 v[146:147], s[8:9], 0, v[212:213]
	s_mov_b32 s29, s23
	ds_write_b32 v9, v2
	v_lshl_add_u64 v[2:3], v[146:147], 0, s[28:29]
	s_mov_b32 s31, s23
	s_mov_b32 s35, s23
	s_waitcnt lgkmcnt(0)
	s_barrier
	v_lshl_add_u64 v[4:5], v[146:147], 0, s[30:31]
	global_load_dwordx4 v[70:73], v[2:3], off
	global_load_dwordx4 v[74:77], v[4:5], off
	v_lshl_add_u64 v[2:3], v[146:147], 0, s[34:35]
	s_mov_b32 s39, s23
	s_mov_b32 s41, s23
	v_lshl_add_u64 v[4:5], v[146:147], 0, s[38:39]
	global_load_dwordx4 v[78:81], v[2:3], off
	global_load_dwordx4 v[66:69], v[4:5], off
	v_lshl_add_u64 v[2:3], v[146:147], 0, s[40:41]
	s_mov_b32 s43, s23
	s_mov_b32 s45, s23
	v_lshl_add_u64 v[4:5], v[146:147], 0, s[42:43]
	global_load_dwordx4 v[82:85], v[2:3], off
	global_load_dwordx4 v[86:89], v[4:5], off
	v_lshl_add_u64 v[2:3], v[146:147], 0, s[44:45]
	s_mov_b32 s47, s23
	s_mov_b32 s49, s23
	v_lshl_add_u64 v[4:5], v[146:147], 0, s[46:47]
	global_load_dwordx4 v[94:97], v[2:3], off
	global_load_dwordx4 v[90:93], v[4:5], off
	v_lshl_add_u64 v[2:3], v[146:147], 0, s[48:49]
	s_mov_b32 s51, s23
	s_mov_b32 s53, s23
	v_lshl_add_u64 v[4:5], v[146:147], 0, s[50:51]
	global_load_dwordx4 v[98:101], v[2:3], off
	global_load_dwordx4 v[102:105], v[4:5], off
	v_lshl_add_u64 v[2:3], v[146:147], 0, s[52:53]
	s_mov_b32 s55, s23
	s_mov_b32 s57, s23
	v_lshl_add_u64 v[4:5], v[146:147], 0, s[54:55]
	global_load_dwordx4 v[110:113], v[2:3], off
	global_load_dwordx4 v[106:109], v[4:5], off
	v_lshl_add_u64 v[2:3], v[146:147], 0, s[56:57]
	s_mov_b32 s59, s23
	s_mov_b32 s61, s23
	v_lshl_add_u64 v[4:5], v[146:147], 0, s[58:59]
	global_load_dwordx4 v[114:117], v[2:3], off
	global_load_dwordx4 v[118:121], v[4:5], off
	v_lshl_add_u64 v[2:3], v[146:147], 0, s[60:61]
	s_mov_b32 s63, s23
	v_lshl_add_u64 v[4:5], v[146:147], 0, s[62:63]
	global_load_dwordx4 v[126:129], v[2:3], off
	global_load_dwordx4 v[122:125], v[4:5], off
	v_readlane_b32 s4, v254, 13
	v_and_b32_e32 v222, 15, v221
	v_bfe_u32 v2, v221, 4, 2
	s_or_b32 s4, s11, s4
	v_lshl_add_u32 v223, v222, 11, 0
	v_bitop3_b32 v3, s4, v222, v2 bitop3:0x36
	v_lshl_add_u32 v148, v3, 4, v223
	v_add_u32_e32 v149, 0x10000, v148
	ds_read_b128 v[130:133], v148
	ds_read_b128 v[134:137], v148 offset:32768
	v_add_u32_e32 v150, 0x18000, v148
	ds_read_b128 v[142:145], v149
	ds_read_b128 v[138:141], v150
	v_or_b32_e32 v224, s11, v2
	v_mov_b32_e32 v2, 0
	s_mov_b32 s11, 0
	s_mov_b64 s[4:5], -1
	v_mov_b32_e32 v3, v2
	v_mov_b32_e32 v4, v2
	v_mov_b32_e32 v5, v2
	v_mov_b32_e32 v6, v2
	v_mov_b32_e32 v7, v2
	v_mov_b32_e32 v8, v2
	v_mov_b32_e32 v9, v2
	v_mov_b32_e32 v10, v2
	v_mov_b32_e32 v11, v2
	v_mov_b32_e32 v12, v2
	v_mov_b32_e32 v13, v2
	v_mov_b32_e32 v14, v2
	v_mov_b32_e32 v15, v2
	v_mov_b32_e32 v16, v2
	v_mov_b32_e32 v17, v2
	v_mov_b32_e32 v18, v2
	v_mov_b32_e32 v19, v2
	v_mov_b32_e32 v20, v2
	v_mov_b32_e32 v21, v2
	v_mov_b32_e32 v22, v2
	v_mov_b32_e32 v23, v2
	v_mov_b32_e32 v24, v2
	v_mov_b32_e32 v25, v2
	v_mov_b32_e32 v26, v2
	v_mov_b32_e32 v27, v2
	v_mov_b32_e32 v28, v2
	v_mov_b32_e32 v29, v2
	v_mov_b32_e32 v30, v2
	v_mov_b32_e32 v31, v2
	v_mov_b32_e32 v32, v2
	v_mov_b32_e32 v33, v2
	v_mov_b32_e32 v34, v2
	v_mov_b32_e32 v35, v2
	v_mov_b32_e32 v36, v2
	v_mov_b32_e32 v37, v2
	v_mov_b32_e32 v38, v2
	v_mov_b32_e32 v39, v2
	v_mov_b32_e32 v40, v2
	v_mov_b32_e32 v41, v2
	v_mov_b32_e32 v42, v2
	v_mov_b32_e32 v43, v2
	v_mov_b32_e32 v44, v2
	v_mov_b32_e32 v45, v2
	v_mov_b32_e32 v46, v2
	v_mov_b32_e32 v47, v2
	v_mov_b32_e32 v48, v2
	v_mov_b32_e32 v49, v2
	v_mov_b32_e32 v50, v2
	v_mov_b32_e32 v51, v2
	v_mov_b32_e32 v52, v2
	v_mov_b32_e32 v53, v2
	v_mov_b32_e32 v54, v2
	v_mov_b32_e32 v55, v2
	v_mov_b32_e32 v56, v2
	v_mov_b32_e32 v57, v2
	v_mov_b32_e32 v58, v2
	v_mov_b32_e32 v59, v2
	v_mov_b32_e32 v60, v2
	v_mov_b32_e32 v61, v2
	v_mov_b32_e32 v62, v2
	v_mov_b32_e32 v63, v2
	v_mov_b32_e32 v64, v2
	v_mov_b32_e32 v65, v2

.LBB0_285:
	s_nop 0
	v_readfirstlane_b32 s6, v162
	s_ashr_i32 s6, s6, 6
	s_mul_i32 s66, s66, s6
	s_waitcnt vmcnt(1)
	v_and_or_b32 v131, v162, 15, s64
	s_waitcnt vmcnt(0)
	v_lshrrev_b32_e32 v130, 2, v162
	s_lshl_b32 s50, s66, 4
	v_and_b32_e32 v130, 12, v130
	v_add_u32_e32 v132, s50, v131
	v_cmp_gt_i32_e32 vcc, s65, v132
	v_lshlrev_b32_e32 v162, 1, v130
	s_and_saveexec_b64 s[48:49], vcc
	s_cbranch_execz .LBB0_287
	v_ashrrev_i32_e32 v133, 31, v132
	v_lshl_add_u64 v[134:135], v[132:133], 2, s[26:27]
	global_load_dword v130, v[134:135], off
	v_mul_f32_e32 v134, 0xbfb8aa3b, v94
	v_mul_f32_e32 v135, 0xbfb8aa3b, v95
	v_exp_f32_e32 v134, v134
	v_exp_f32_e32 v135, v135
	v_mul_f32_e32 v136, 0xbfb8aa3b, v96
	v_mul_f32_e32 v137, 0xbfb8aa3b, v97
	v_exp_f32_e32 v136, v136
	v_exp_f32_e32 v137, v137
	v_pk_add_f32 v[134:135], v[134:135], 1.0 op_sel_hi:[1,0]
	v_mul_f32_e32 v138, 0xbfb8aa3b, v90
	v_pk_add_f32 v[136:137], v[136:137], 1.0 op_sel_hi:[1,0]
	v_mul_f32_e32 v139, 0xbfb8aa3b, v91
	v_exp_f32_e32 v138, v138
	v_exp_f32_e32 v139, v139
	v_rcp_f32_e32 v140, v135
	s_nop 0
	v_mul_f32_e32 v95, v95, v140
	v_rcp_f32_e32 v135, v134
	s_nop 0
	v_mul_f32_e32 v94, v94, v135
	v_pk_mul_f32 v[86:87], v[86:87], v[94:95]
	v_pk_add_f32 v[138:139], v[138:139], 1.0 op_sel_hi:[1,0]
	v_rcp_f32_e32 v134, v137
	s_nop 0
	v_mul_f32_e32 v95, v97, v134
	v_rcp_f32_e32 v94, v136
	s_nop 0
	v_mul_f32_e32 v94, v96, v94
	v_add_u32_e32 v132, s63, v132
	v_pk_mul_f32 v[88:89], v[88:89], v[94:95]
	v_ashrrev_i32_e32 v133, 31, v132
	v_lshlrev_b64 v[132:133], 9, v[132:133]
	v_lshl_add_u64 v[132:133], s[20:21], 0, v[132:133]
	s_waitcnt vmcnt(0)
	v_pk_mul_f32 v[86:87], v[86:87], v[130:131] op_sel_hi:[1,0]
	v_pk_mul_f32 v[88:89], v[88:89], v[130:131] op_sel_hi:[1,0]
	v_lshl_add_u64 v[132:133], v[132:133], 0, v[162:163]
	v_cvt_pk_bf16_f32 v86, v86, v87
	v_cvt_pk_bf16_f32 v87, v88, v89
	global_store_dwordx2 v[132:133], v[86:87], off
	v_rcp_f32_e32 v86, v139
	s_nop 0
	v_mul_f32_e32 v87, v91, v86
	v_mul_f32_e32 v88, 0xbfb8aa3b, v92
	v_mul_f32_e32 v89, 0xbfb8aa3b, v93
	v_exp_f32_e32 v88, v88
	v_exp_f32_e32 v89, v89
	v_rcp_f32_e32 v86, v138
	s_nop 0
	v_mul_f32_e32 v86, v90, v86
	v_pk_mul_f32 v[62:63], v[62:63], v[86:87]
	v_pk_add_f32 v[88:89], v[88:89], 1.0 op_sel_hi:[1,0]
	v_pk_mul_f32 v[62:63], v[62:63], v[130:131] op_sel_hi:[1,0]
	v_cvt_pk_bf16_f32 v62, v62, v63
	v_rcp_f32_e32 v63, v89
	s_nop 0
	v_mul_f32_e32 v87, v93, v63
	v_mul_f32_e32 v89, 0xbfb8aa3b, v70
	v_exp_f32_e32 v90, v89
	v_mul_f32_e32 v89, 0xbfb8aa3b, v71
	v_exp_f32_e32 v91, v89
	v_rcp_f32_e32 v63, v88
	s_nop 0
	v_mul_f32_e32 v86, v92, v63
	v_pk_mul_f32 v[64:65], v[64:65], v[86:87]
	v_pk_add_f32 v[86:87], v[90:91], 1.0 op_sel_hi:[1,0]
	v_pk_mul_f32 v[64:65], v[64:65], v[130:131] op_sel_hi:[1,0]
	v_cvt_pk_bf16_f32 v63, v64, v65
	global_store_dwordx2 v[132:133], v[62:63], off offset:32
	v_rcp_f32_e32 v62, v87
	s_nop 0
	v_mul_f32_e32 v63, v71, v62
	v_mul_f32_e32 v64, 0xbfb8aa3b, v72
	v_mul_f32_e32 v65, 0xbfb8aa3b, v73
	v_exp_f32_e32 v64, v64
	v_exp_f32_e32 v65, v65
	v_rcp_f32_e32 v62, v86
	s_nop 0
	v_mul_f32_e32 v62, v70, v62
	v_pk_mul_f32 v[30:31], v[30:31], v[62:63]
	v_pk_add_f32 v[64:65], v[64:65], 1.0 op_sel_hi:[1,0]
	v_pk_mul_f32 v[30:31], v[30:31], v[130:131] op_sel_hi:[1,0]
	v_cvt_pk_bf16_f32 v30, v30, v31
	v_rcp_f32_e32 v31, v65
	s_nop 0
	v_mul_f32_e32 v63, v73, v31
	v_mul_f32_e32 v65, 0xbfb8aa3b, v42
	v_exp_f32_e32 v70, v65
	v_mul_f32_e32 v65, 0xbfb8aa3b, v43
	v_exp_f32_e32 v71, v65
	v_rcp_f32_e32 v31, v64
	s_nop 0
	v_mul_f32_e32 v62, v72, v31
	v_pk_mul_f32 v[32:33], v[32:33], v[62:63]
	v_pk_add_f32 v[62:63], v[70:71], 1.0 op_sel_hi:[1,0]
	v_pk_mul_f32 v[32:33], v[32:33], v[130:131] op_sel_hi:[1,0]
	v_cvt_pk_bf16_f32 v31, v32, v33
	global_store_dwordx2 v[132:133], v[30:31], off offset:64
	v_rcp_f32_e32 v30, v63
	s_nop 0
	v_mul_f32_e32 v31, v43, v30
	v_mul_f32_e32 v32, 0xbfb8aa3b, v44
	v_mul_f32_e32 v33, 0xbfb8aa3b, v45
	v_exp_f32_e32 v32, v32
	v_exp_f32_e32 v33, v33
	v_rcp_f32_e32 v30, v62
	s_nop 0
	v_mul_f32_e32 v30, v42, v30
	v_pk_mul_f32 v[10:11], v[10:11], v[30:31]
	v_pk_add_f32 v[32:33], v[32:33], 1.0 op_sel_hi:[1,0]
	v_pk_mul_f32 v[10:11], v[10:11], v[130:131] op_sel_hi:[1,0]
	v_cvt_pk_bf16_f32 v10, v10, v11
	v_rcp_f32_e32 v11, v33
	s_nop 0
	v_mul_f32_e32 v31, v45, v11
	v_rcp_f32_e32 v11, v32
	s_nop 0
	v_mul_f32_e32 v30, v44, v11
	v_pk_mul_f32 v[12:13], v[12:13], v[30:31]
	s_nop 0
	v_pk_mul_f32 v[12:13], v[12:13], v[130:131] op_sel_hi:[1,0]
	s_nop 0
	v_cvt_pk_bf16_f32 v11, v12, v13
	global_store_dwordx2 v[132:133], v[10:11], off offset:96
.LBB0_287:
	s_or_b64 exec, exec, s[48:49]
	v_or_b32_e32 v10, 16, v131
	v_add_u32_e32 v12, s50, v10
	v_cmp_gt_i32_e32 vcc, s65, v12
	s_and_b64 s[6:7], s[46:47], vcc
	s_and_saveexec_b64 s[46:47], s[6:7]
	s_cbranch_execz .LBB0_289
	v_ashrrev_i32_e32 v13, 31, v12
	v_lshl_add_u64 v[10:11], v[12:13], 2, s[26:27]
	global_load_dword v10, v[10:11], off
	v_mul_f32_e32 v11, 0xbfb8aa3b, v74
	v_mul_f32_e32 v31, 0xbfb8aa3b, v75
	v_exp_f32_e32 v30, v11
	v_exp_f32_e32 v31, v31
	v_mul_f32_e32 v32, 0xbfb8aa3b, v76
	v_mul_f32_e32 v33, 0xbfb8aa3b, v77
	v_exp_f32_e32 v32, v32
	v_exp_f32_e32 v33, v33
	v_pk_add_f32 v[30:31], v[30:31], 1.0 op_sel_hi:[1,0]
	v_mul_f32_e32 v42, 0xbfb8aa3b, v46
	v_pk_add_f32 v[32:33], v[32:33], 1.0 op_sel_hi:[1,0]
	v_mul_f32_e32 v43, 0xbfb8aa3b, v47
	v_exp_f32_e32 v42, v42
	v_exp_f32_e32 v43, v43
	v_rcp_f32_e32 v11, v31
	s_nop 0
	v_mul_f32_e32 v31, v75, v11
	v_rcp_f32_e32 v11, v30
	s_nop 0
	v_mul_f32_e32 v30, v74, v11
	v_pk_add_f32 v[42:43], v[42:43], 1.0 op_sel_hi:[1,0]
	v_pk_mul_f32 v[30:31], v[54:55], v[30:31]
	v_rcp_f32_e32 v11, v33
	s_nop 0
	v_mul_f32_e32 v33, v77, v11
	v_add_u32_e32 v12, s63, v12
	v_rcp_f32_e32 v11, v32
	s_nop 0
	v_mul_f32_e32 v32, v76, v11
	v_ashrrev_i32_e32 v13, 31, v12
	v_lshlrev_b64 v[12:13], 9, v[12:13]
	v_pk_mul_f32 v[32:33], v[56:57], v[32:33]
	v_lshl_add_u64 v[12:13], s[20:21], 0, v[12:13]
	v_lshl_add_u64 v[12:13], v[12:13], 0, v[162:163]
	s_waitcnt vmcnt(0)
	v_pk_mul_f32 v[30:31], v[30:31], v[10:11] op_sel_hi:[1,0]
	v_pk_mul_f32 v[32:33], v[32:33], v[10:11] op_sel_hi:[1,0]
	v_cvt_pk_bf16_f32 v30, v30, v31
	v_cvt_pk_bf16_f32 v31, v32, v33
	global_store_dwordx2 v[12:13], v[30:31], off
	v_rcp_f32_e32 v11, v43
	s_nop 0
	v_mul_f32_e32 v31, v47, v11
	v_mul_f32_e32 v30, 0xbfb8aa3b, v48
	v_exp_f32_e32 v32, v30
	v_mul_f32_e32 v30, 0xbfb8aa3b, v49
	v_exp_f32_e32 v33, v30
	v_rcp_f32_e32 v11, v42
	s_nop 0
	v_mul_f32_e32 v30, v46, v11
	v_pk_mul_f32 v[30:31], v[34:35], v[30:31]
	v_pk_add_f32 v[32:33], v[32:33], 1.0 op_sel_hi:[1,0]
	s_nop 0
	v_pk_mul_f32 v[30:31], v[30:31], v[10:11] op_sel_hi:[1,0]
	s_nop 0
	v_cvt_pk_bf16_f32 v30, v30, v31
	v_rcp_f32_e32 v11, v33
	s_nop 0
	v_mul_f32_e32 v33, v49, v11
	v_mul_f32_e32 v31, 0xbfb8aa3b, v18
	v_exp_f32_e32 v34, v31
	v_mul_f32_e32 v31, 0xbfb8aa3b, v19
	v_exp_f32_e32 v35, v31
	v_rcp_f32_e32 v11, v32
	s_nop 0
	v_mul_f32_e32 v32, v48, v11
	v_pk_mul_f32 v[32:33], v[36:37], v[32:33]
	v_pk_add_f32 v[34:35], v[34:35], 1.0 op_sel_hi:[1,0]
	s_nop 0
	v_pk_mul_f32 v[32:33], v[32:33], v[10:11] op_sel_hi:[1,0]
	s_nop 0
	v_cvt_pk_bf16_f32 v31, v32, v33
	global_store_dwordx2 v[12:13], v[30:31], off offset:32
	v_rcp_f32_e32 v11, v35
	s_nop 0
	v_mul_f32_e32 v19, v19, v11
	v_mul_f32_e32 v30, 0xbfb8aa3b, v20
	v_mul_f32_e32 v31, 0xbfb8aa3b, v21
	v_exp_f32_e32 v30, v30
	v_exp_f32_e32 v31, v31
	v_rcp_f32_e32 v11, v34
	s_nop 0
	v_mul_f32_e32 v18, v18, v11
	v_pk_mul_f32 v[14:15], v[14:15], v[18:19]
	v_pk_add_f32 v[30:31], v[30:31], 1.0 op_sel_hi:[1,0]
	s_nop 0
	v_pk_mul_f32 v[14:15], v[14:15], v[10:11] op_sel_hi:[1,0]
	s_nop 0
	v_cvt_pk_bf16_f32 v14, v14, v15
	v_rcp_f32_e32 v11, v31
	s_nop 0
	v_mul_f32_e32 v19, v21, v11
	v_mul_f32_e32 v15, 0xbfb8aa3b, v6
	v_exp_f32_e32 v32, v15
	v_mul_f32_e32 v15, 0xbfb8aa3b, v7
	v_exp_f32_e32 v33, v15
	v_rcp_f32_e32 v11, v30
	s_nop 0
	v_mul_f32_e32 v18, v20, v11
	v_pk_mul_f32 v[16:17], v[16:17], v[18:19]
	v_pk_add_f32 v[18:19], v[32:33], 1.0 op_sel_hi:[1,0]
	s_nop 0
	v_pk_mul_f32 v[16:17], v[16:17], v[10:11] op_sel_hi:[1,0]
	s_nop 0
	v_cvt_pk_bf16_f32 v15, v16, v17
	global_store_dwordx2 v[12:13], v[14:15], off offset:64
	v_rcp_f32_e32 v11, v19
	s_nop 0
	v_mul_f32_e32 v7, v7, v11
	v_mul_f32_e32 v14, 0xbfb8aa3b, v8
	v_mul_f32_e32 v15, 0xbfb8aa3b, v9
	v_exp_f32_e32 v14, v14
	v_exp_f32_e32 v15, v15
	v_rcp_f32_e32 v11, v18
	s_nop 0
	v_mul_f32_e32 v6, v6, v11
	v_pk_mul_f32 v[2:3], v[2:3], v[6:7]
	v_pk_add_f32 v[14:15], v[14:15], 1.0 op_sel_hi:[1,0]
	s_nop 0
	v_pk_mul_f32 v[2:3], v[2:3], v[10:11] op_sel_hi:[1,0]
	s_nop 0
	v_cvt_pk_bf16_f32 v2, v2, v3
	v_rcp_f32_e32 v3, v15
	s_nop 0
	v_mul_f32_e32 v7, v9, v3
	v_rcp_f32_e32 v3, v14
	s_nop 0
	v_mul_f32_e32 v6, v8, v3
	v_pk_mul_f32 v[4:5], v[4:5], v[6:7]
	s_nop 0
	v_pk_mul_f32 v[4:5], v[4:5], v[10:11] op_sel_hi:[1,0]
	s_nop 0
	v_cvt_pk_bf16_f32 v3, v4, v5
	global_store_dwordx2 v[12:13], v[2:3], off offset:96
.LBB0_289:
	s_or_b64 exec, exec, s[46:47]
	v_or_b32_e32 v2, 32, v131
	v_add_u32_e32 v4, s50, v2
	v_cmp_gt_i32_e32 vcc, s65, v4
	s_and_b64 s[6:7], s[44:45], vcc
	s_and_saveexec_b64 s[44:45], s[6:7]
	s_cbranch_execz .LBB0_291
	v_ashrrev_i32_e32 v5, 31, v4
	v_lshl_add_u64 v[2:3], v[4:5], 2, s[26:27]
	global_load_dword v2, v[2:3], off
	v_mul_f32_e32 v3, 0xbfb8aa3b, v78
	v_mul_f32_e32 v7, 0xbfb8aa3b, v79
	v_exp_f32_e32 v6, v3
	v_exp_f32_e32 v7, v7
	v_mul_f32_e32 v8, 0xbfb8aa3b, v80
	v_mul_f32_e32 v9, 0xbfb8aa3b, v81
	v_exp_f32_e32 v8, v8
	v_exp_f32_e32 v9, v9
	v_pk_add_f32 v[6:7], v[6:7], 1.0 op_sel_hi:[1,0]
	v_mul_f32_e32 v10, 0xbfb8aa3b, v58
	v_pk_add_f32 v[8:9], v[8:9], 1.0 op_sel_hi:[1,0]
	v_mul_f32_e32 v11, 0xbfb8aa3b, v59
	v_exp_f32_e32 v10, v10
	v_exp_f32_e32 v11, v11
	v_rcp_f32_e32 v3, v7
	s_nop 0
	v_mul_f32_e32 v7, v79, v3
	v_rcp_f32_e32 v3, v6
	s_nop 0
	v_mul_f32_e32 v6, v78, v3
	v_pk_add_f32 v[10:11], v[10:11], 1.0 op_sel_hi:[1,0]
	v_pk_mul_f32 v[6:7], v[82:83], v[6:7]
	v_rcp_f32_e32 v3, v9
	s_nop 0
	v_mul_f32_e32 v9, v81, v3
	v_add_u32_e32 v4, s63, v4
	v_rcp_f32_e32 v3, v8
	s_nop 0
	v_mul_f32_e32 v8, v80, v3
	v_ashrrev_i32_e32 v5, 31, v4
	v_lshlrev_b64 v[4:5], 9, v[4:5]
	v_pk_mul_f32 v[8:9], v[84:85], v[8:9]
	v_lshl_add_u64 v[4:5], s[20:21], 0, v[4:5]
	v_lshl_add_u64 v[4:5], v[4:5], 0, v[162:163]
	s_waitcnt vmcnt(0)
	v_pk_mul_f32 v[6:7], v[6:7], v[2:3] op_sel_hi:[1,0]
	v_pk_mul_f32 v[8:9], v[8:9], v[2:3] op_sel_hi:[1,0]
	v_cvt_pk_bf16_f32 v6, v6, v7
	v_cvt_pk_bf16_f32 v7, v8, v9
	global_store_dwordx2 v[4:5], v[6:7], off
	v_rcp_f32_e32 v3, v11
	s_nop 0
	v_mul_f32_e32 v7, v59, v3
	v_mul_f32_e32 v6, 0xbfb8aa3b, v60
	v_exp_f32_e32 v8, v6
	v_mul_f32_e32 v6, 0xbfb8aa3b, v61
	v_exp_f32_e32 v9, v6
	v_rcp_f32_e32 v3, v10
	s_nop 0
	v_mul_f32_e32 v6, v58, v3
	v_pk_mul_f32 v[6:7], v[66:67], v[6:7]
	v_pk_add_f32 v[8:9], v[8:9], 1.0 op_sel_hi:[1,0]
	s_nop 0
	v_pk_mul_f32 v[6:7], v[6:7], v[2:3] op_sel_hi:[1,0]
	s_nop 0
	v_cvt_pk_bf16_f32 v6, v6, v7
	v_rcp_f32_e32 v3, v9
	s_nop 0
	v_mul_f32_e32 v9, v61, v3
	v_mul_f32_e32 v7, 0xbfb8aa3b, v38
	v_exp_f32_e32 v10, v7
	v_mul_f32_e32 v7, 0xbfb8aa3b, v39
	v_exp_f32_e32 v11, v7
	v_rcp_f32_e32 v3, v8
	s_nop 0
	v_mul_f32_e32 v8, v60, v3
	v_pk_mul_f32 v[8:9], v[68:69], v[8:9]
	v_pk_add_f32 v[10:11], v[10:11], 1.0 op_sel_hi:[1,0]
	s_nop 0
	v_pk_mul_f32 v[8:9], v[8:9], v[2:3] op_sel_hi:[1,0]
	s_nop 0
	v_cvt_pk_bf16_f32 v7, v8, v9
	global_store_dwordx2 v[4:5], v[6:7], off offset:32
	v_rcp_f32_e32 v3, v11
	s_nop 0
	v_mul_f32_e32 v7, v39, v3
	v_mul_f32_e32 v6, 0xbfb8aa3b, v40
	v_exp_f32_e32 v8, v6
	v_mul_f32_e32 v6, 0xbfb8aa3b, v41
	v_exp_f32_e32 v9, v6
	v_rcp_f32_e32 v3, v10
	s_nop 0
	v_mul_f32_e32 v6, v38, v3
	v_pk_mul_f32 v[6:7], v[50:51], v[6:7]
	v_pk_add_f32 v[8:9], v[8:9], 1.0 op_sel_hi:[1,0]
	s_nop 0
	v_pk_mul_f32 v[6:7], v[6:7], v[2:3] op_sel_hi:[1,0]
	s_nop 0
	v_cvt_pk_bf16_f32 v6, v6, v7
	v_rcp_f32_e32 v3, v9
	s_nop 0
	v_mul_f32_e32 v9, v41, v3
	v_mul_f32_e32 v7, 0xbfb8aa3b, v22
	v_exp_f32_e32 v10, v7
	v_mul_f32_e32 v7, 0xbfb8aa3b, v23
	v_exp_f32_e32 v11, v7
	v_rcp_f32_e32 v3, v8
	s_nop 0
	v_mul_f32_e32 v8, v40, v3
	v_pk_mul_f32 v[8:9], v[52:53], v[8:9]
	v_pk_add_f32 v[10:11], v[10:11], 1.0 op_sel_hi:[1,0]
	s_nop 0
	v_pk_mul_f32 v[8:9], v[8:9], v[2:3] op_sel_hi:[1,0]
	s_nop 0
	v_cvt_pk_bf16_f32 v7, v8, v9
	global_store_dwordx2 v[4:5], v[6:7], off offset:64
	v_rcp_f32_e32 v3, v11
	s_nop 0
	v_mul_f32_e32 v7, v23, v3
	v_mul_f32_e32 v6, 0xbfb8aa3b, v24
	v_exp_f32_e32 v8, v6
	v_mul_f32_e32 v6, 0xbfb8aa3b, v25
	v_exp_f32_e32 v9, v6
	v_rcp_f32_e32 v3, v10
	s_nop 0
	v_mul_f32_e32 v6, v22, v3
	v_pk_mul_f32 v[6:7], v[26:27], v[6:7]
	v_pk_add_f32 v[8:9], v[8:9], 1.0 op_sel_hi:[1,0]
	s_nop 0
	v_pk_mul_f32 v[6:7], v[6:7], v[2:3] op_sel_hi:[1,0]
	s_nop 0
	v_cvt_pk_bf16_f32 v6, v6, v7
	v_rcp_f32_e32 v3, v9
	s_nop 0
	v_mul_f32_e32 v9, v25, v3
	v_rcp_f32_e32 v3, v8
	s_nop 0
	v_mul_f32_e32 v8, v24, v3
	v_pk_mul_f32 v[8:9], v[28:29], v[8:9]
	s_nop 0
	v_pk_mul_f32 v[2:3], v[8:9], v[2:3] op_sel_hi:[1,0]
	s_nop 0
	v_cvt_pk_bf16_f32 v7, v2, v3
	global_store_dwordx2 v[4:5], v[6:7], off offset:96
.LBB0_291:
	s_or_b64 exec, exec, s[44:45]
	v_or_b32_e32 v2, 48, v131
	v_add_u32_e32 v4, s50, v2
	v_cmp_gt_i32_e32 vcc, s65, v4
	s_and_b64 s[6:7], s[42:43], vcc
	s_and_saveexec_b64 s[42:43], s[6:7]
	s_cbranch_execz .LBB0_262
	v_ashrrev_i32_e32 v5, 31, v4
	v_lshl_add_u64 v[2:3], v[4:5], 2, s[26:27]
	global_load_dword v2, v[2:3], off
	v_mul_f32_e32 v3, 0xbfb8aa3b, v122
	v_mul_f32_e32 v7, 0xbfb8aa3b, v123
	v_exp_f32_e32 v6, v3
	v_exp_f32_e32 v7, v7
	v_mul_f32_e32 v8, 0xbfb8aa3b, v124
	v_mul_f32_e32 v9, 0xbfb8aa3b, v125
	v_exp_f32_e32 v8, v8
	v_exp_f32_e32 v9, v9
	v_pk_add_f32 v[6:7], v[6:7], 1.0 op_sel_hi:[1,0]
	v_mul_f32_e32 v10, 0xbfb8aa3b, v114
	v_pk_add_f32 v[8:9], v[8:9], 1.0 op_sel_hi:[1,0]
	v_mul_f32_e32 v11, 0xbfb8aa3b, v115
	v_exp_f32_e32 v10, v10
	v_exp_f32_e32 v11, v11
	v_rcp_f32_e32 v3, v7
	s_nop 0
	v_mul_f32_e32 v7, v123, v3
	v_rcp_f32_e32 v3, v6
	s_nop 0
	v_mul_f32_e32 v6, v122, v3
	v_pk_add_f32 v[10:11], v[10:11], 1.0 op_sel_hi:[1,0]
	v_pk_mul_f32 v[6:7], v[126:127], v[6:7]
	v_rcp_f32_e32 v3, v9
	s_nop 0
	v_mul_f32_e32 v9, v125, v3
	v_add_u32_e32 v4, s63, v4
	v_rcp_f32_e32 v3, v8
	s_nop 0
	v_mul_f32_e32 v8, v124, v3
	v_ashrrev_i32_e32 v5, 31, v4
	v_lshlrev_b64 v[4:5], 9, v[4:5]
	v_pk_mul_f32 v[8:9], v[128:129], v[8:9]
	v_lshl_add_u64 v[4:5], s[20:21], 0, v[4:5]
	v_lshl_add_u64 v[4:5], v[4:5], 0, v[162:163]
	s_waitcnt vmcnt(0)
	v_pk_mul_f32 v[6:7], v[6:7], v[2:3] op_sel_hi:[1,0]
	v_pk_mul_f32 v[8:9], v[8:9], v[2:3] op_sel_hi:[1,0]
	v_cvt_pk_bf16_f32 v6, v6, v7
	v_cvt_pk_bf16_f32 v7, v8, v9
	global_store_dwordx2 v[4:5], v[6:7], off
	v_rcp_f32_e32 v3, v11
	s_nop 0
	v_mul_f32_e32 v7, v115, v3
	v_mul_f32_e32 v6, 0xbfb8aa3b, v116
	v_exp_f32_e32 v8, v6
	v_mul_f32_e32 v6, 0xbfb8aa3b, v117
	v_exp_f32_e32 v9, v6
	v_rcp_f32_e32 v3, v10
	s_nop 0
	v_mul_f32_e32 v6, v114, v3
	v_pk_mul_f32 v[6:7], v[118:119], v[6:7]
	v_pk_add_f32 v[8:9], v[8:9], 1.0 op_sel_hi:[1,0]
	s_nop 0
	v_pk_mul_f32 v[6:7], v[6:7], v[2:3] op_sel_hi:[1,0]
	s_nop 0
	v_cvt_pk_bf16_f32 v6, v6, v7
	v_rcp_f32_e32 v3, v9
	s_nop 0
	v_mul_f32_e32 v9, v117, v3
	v_mul_f32_e32 v7, 0xbfb8aa3b, v106
	v_exp_f32_e32 v10, v7
	v_mul_f32_e32 v7, 0xbfb8aa3b, v107
	v_exp_f32_e32 v11, v7
	v_rcp_f32_e32 v3, v8
	s_nop 0
	v_mul_f32_e32 v8, v116, v3
	v_pk_mul_f32 v[8:9], v[120:121], v[8:9]
	v_pk_add_f32 v[10:11], v[10:11], 1.0 op_sel_hi:[1,0]
	s_nop 0
	v_pk_mul_f32 v[8:9], v[8:9], v[2:3] op_sel_hi:[1,0]
	s_nop 0
	v_cvt_pk_bf16_f32 v7, v8, v9
	global_store_dwordx2 v[4:5], v[6:7], off offset:32
	v_rcp_f32_e32 v3, v11
	s_nop 0
	v_mul_f32_e32 v7, v107, v3
	v_mul_f32_e32 v6, 0xbfb8aa3b, v108
	v_exp_f32_e32 v8, v6
	v_mul_f32_e32 v6, 0xbfb8aa3b, v109
	v_exp_f32_e32 v9, v6
	v_rcp_f32_e32 v3, v10
	s_nop 0
	v_mul_f32_e32 v6, v106, v3
	v_pk_mul_f32 v[6:7], v[110:111], v[6:7]
	v_pk_add_f32 v[8:9], v[8:9], 1.0 op_sel_hi:[1,0]
	s_nop 0
	v_pk_mul_f32 v[6:7], v[6:7], v[2:3] op_sel_hi:[1,0]
	s_nop 0
	v_cvt_pk_bf16_f32 v6, v6, v7
	v_rcp_f32_e32 v3, v9
	s_nop 0
	v_mul_f32_e32 v9, v109, v3
	v_mul_f32_e32 v7, 0xbfb8aa3b, v102
	v_exp_f32_e32 v10, v7
	v_mul_f32_e32 v7, 0xbfb8aa3b, v103
	v_exp_f32_e32 v11, v7
	v_rcp_f32_e32 v3, v8
	s_nop 0
	v_mul_f32_e32 v8, v108, v3
	v_pk_mul_f32 v[8:9], v[112:113], v[8:9]
	v_pk_add_f32 v[10:11], v[10:11], 1.0 op_sel_hi:[1,0]
	s_nop 0
	v_pk_mul_f32 v[8:9], v[8:9], v[2:3] op_sel_hi:[1,0]
	s_nop 0
	v_cvt_pk_bf16_f32 v7, v8, v9
	global_store_dwordx2 v[4:5], v[6:7], off offset:64
	v_rcp_f32_e32 v3, v11
	s_nop 0
	v_mul_f32_e32 v7, v103, v3
	v_mul_f32_e32 v6, 0xbfb8aa3b, v104
	v_exp_f32_e32 v8, v6
	v_mul_f32_e32 v6, 0xbfb8aa3b, v105
	v_exp_f32_e32 v9, v6
	v_rcp_f32_e32 v3, v10
	s_nop 0
	v_mul_f32_e32 v6, v102, v3
	v_pk_mul_f32 v[6:7], v[98:99], v[6:7]
	v_pk_add_f32 v[8:9], v[8:9], 1.0 op_sel_hi:[1,0]
	s_nop 0
	v_pk_mul_f32 v[6:7], v[6:7], v[2:3] op_sel_hi:[1,0]
	s_nop 0
	v_cvt_pk_bf16_f32 v6, v6, v7
	v_rcp_f32_e32 v3, v9
	s_nop 0
	v_mul_f32_e32 v9, v105, v3
	v_rcp_f32_e32 v3, v8
	s_nop 0
	v_mul_f32_e32 v8, v104, v3
	v_pk_mul_f32 v[8:9], v[100:101], v[8:9]
	s_nop 0
	v_pk_mul_f32 v[2:3], v[8:9], v[2:3] op_sel_hi:[1,0]
	s_nop 0
	v_cvt_pk_bf16_f32 v7, v2, v3
	global_store_dwordx2 v[4:5], v[6:7], off offset:96
	s_branch .LBB0_262

.LBB0_467:
	s_add_i32 s16, s18, -8
	s_add_i32 s19, s5, -3
	s_and_b32 s16, s16, 0x7c
	s_cmp_lt_u32 s19, 28
	v_bitop3_b32 v114, s16, v230, v231 bitop3:0x36
	s_cselect_b64 s[16:17], -1, 0
	s_min_u32 s19, s19, 27
	s_add_i32 s19, s19, s33
	s_lshl_b32 s19, s19, 6
	s_and_b32 s19, s19, 0x7c0
	v_cndmask_b32_e64 v132, v212, 0, s[16:17]
	s_waitcnt vmcnt(7) lgkmcnt(3)
	v_mfma_f32_16x16x32_bf16 v[94:97], v[78:81], v[102:105], v[94:97]
	v_lshl_add_u32 v126, v114, 4, v232
	ds_read_b128 v[114:117], v126
	ds_read_b128 v[118:121], v126 offset:32768
	v_add_u32_e32 v122, 0x10000, v126
	s_waitcnt lgkmcnt(4)
	v_mfma_f32_16x16x32_bf16 v[58:61], v[78:81], v[106:109], v[58:61]
	v_add_u32_e32 v126, 0x18000, v126
	ds_read_b128 v[122:125], v122
	ds_read_b128 v[126:129], v126
	s_waitcnt lgkmcnt(5)
	v_mfma_f32_16x16x32_bf16 v[54:57], v[78:81], v[110:113], v[54:57]
	s_waitcnt lgkmcnt(4)
	v_mfma_f32_16x16x32_bf16 v[46:49], v[78:81], v[98:101], v[46:49]
	v_sub_u32_e32 v78, s19, v132
	v_ashrrev_i32_e32 v79, 31, v78
	s_waitcnt vmcnt(6)
	v_mfma_f32_16x16x32_bf16 v[38:41], v[82:85], v[102:105], v[38:41]
	v_mfma_f32_16x16x32_bf16 v[30:33], v[82:85], v[106:109], v[30:33]
	v_mfma_f32_16x16x32_bf16 v[22:25], v[82:85], v[110:113], v[22:25]
	v_mfma_f32_16x16x32_bf16 v[14:17], v[82:85], v[98:101], v[14:17]
	v_lshl_add_u64 v[82:83], v[78:79], 4, v[130:131]
	global_load_dwordx4 v[78:81], v[82:83], off
	v_add_co_u32_e32 v82, vcc, s40, v82
	s_nop 1
	v_addc_co_u32_e32 v83, vcc, 0, v83, vcc
	global_load_dwordx4 v[82:85], v[82:83], off
	s_add_i32 s19, s5, -2
	s_min_u32 s19, s19, 27
	s_add_i32 s19, s19, s33
	s_lshl_b32 s19, s19, 6
	s_and_b32 s19, s19, 0x7c0
	s_waitcnt vmcnt(7) lgkmcnt(3)
	v_mfma_f32_16x16x32_bf16 v[94:97], v[62:65], v[114:117], v[94:97]
	s_waitcnt lgkmcnt(2)
	v_mfma_f32_16x16x32_bf16 v[58:61], v[62:65], v[118:121], v[58:61]
	s_waitcnt lgkmcnt(1)
	v_mfma_f32_16x16x32_bf16 v[54:57], v[62:65], v[122:125], v[54:57]
	s_waitcnt lgkmcnt(0)
	v_mfma_f32_16x16x32_bf16 v[46:49], v[62:65], v[126:129], v[46:49]
	v_sub_u32_e32 v62, s19, v132
	v_ashrrev_i32_e32 v63, 31, v62
	v_lshl_add_u64 v[62:63], v[62:63], 4, v[130:131]
	s_waitcnt vmcnt(6)
	v_mfma_f32_16x16x32_bf16 v[38:41], v[66:69], v[114:117], v[38:41]
	s_add_i32 s19, s18, -4
	s_and_b32 s19, s19, 0x7c
	v_bitop3_b32 v98, s19, v230, v231 bitop3:0x36
	v_mfma_f32_16x16x32_bf16 v[30:33], v[66:69], v[118:121], v[30:33]
	v_lshl_add_u32 v106, v98, 4, v232
	v_add_u32_e32 v107, 0x10000, v106
	v_add_u32_e32 v110, 0x18000, v106
	v_mfma_f32_16x16x32_bf16 v[22:25], v[66:69], v[122:125], v[22:25]
	v_mfma_f32_16x16x32_bf16 v[14:17], v[66:69], v[126:129], v[14:17]
	v_add_co_u32_e32 v66, vcc, s40, v62
	s_nop 1
	v_addc_co_u32_e32 v67, vcc, 0, v63, vcc
	global_load_dwordx4 v[62:65], v[62:63], off
	s_nop 0
	global_load_dwordx4 v[66:69], v[66:67], off
	ds_read_b128 v[98:101], v106
	ds_read_b128 v[102:105], v106 offset:32768
	ds_read_b128 v[106:109], v107
	ds_read_b128 v[110:113], v110
	s_add_i32 s19, s5, -1
	s_min_u32 s19, s19, 27
	s_add_i32 s19, s19, s33
	s_lshl_b32 s19, s19, 6
	s_and_b32 s19, s19, 0x7c0
	s_waitcnt vmcnt(7) lgkmcnt(3)
	v_mfma_f32_16x16x32_bf16 v[94:97], v[70:73], v[98:101], v[94:97]
	s_waitcnt lgkmcnt(2)
	v_mfma_f32_16x16x32_bf16 v[58:61], v[70:73], v[102:105], v[58:61]
	s_waitcnt lgkmcnt(1)
	v_mfma_f32_16x16x32_bf16 v[54:57], v[70:73], v[106:109], v[54:57]
	s_waitcnt lgkmcnt(0)
	v_mfma_f32_16x16x32_bf16 v[46:49], v[70:73], v[110:113], v[46:49]
	v_sub_u32_e32 v70, s19, v132
	v_ashrrev_i32_e32 v71, 31, v70
	v_lshl_add_u64 v[70:71], v[70:71], 4, v[130:131]
	s_waitcnt vmcnt(6)
	v_mfma_f32_16x16x32_bf16 v[38:41], v[74:77], v[98:101], v[38:41]
	s_and_b32 s19, s18, 0x7c
	v_bitop3_b32 v98, s19, v230, v231 bitop3:0x36
	v_mfma_f32_16x16x32_bf16 v[30:33], v[74:77], v[102:105], v[30:33]
	v_mfma_f32_16x16x32_bf16 v[22:25], v[74:77], v[106:109], v[22:25]
	v_lshl_add_u32 v106, v98, 4, v232
	v_add_u32_e32 v107, 0x10000, v106
	v_mfma_f32_16x16x32_bf16 v[14:17], v[74:77], v[110:113], v[14:17]
	v_add_co_u32_e32 v74, vcc, s40, v70
	v_add_u32_e32 v110, 0x18000, v106
	s_nop 0
	v_addc_co_u32_e32 v75, vcc, 0, v71, vcc
	global_load_dwordx4 v[70:73], v[70:71], off
	s_nop 0
	global_load_dwordx4 v[74:77], v[74:75], off
	ds_read_b128 v[98:101], v106
	ds_read_b128 v[102:105], v106 offset:32768
	ds_read_b128 v[106:109], v107
	ds_read_b128 v[110:113], v110
	s_min_u32 s19, s5, 27
	s_add_i32 s19, s19, s33
	s_lshl_b32 s19, s19, 6
	s_and_b32 s19, s19, 0x7c0
	s_waitcnt vmcnt(7) lgkmcnt(3)
	v_mfma_f32_16x16x32_bf16 v[94:97], v[86:89], v[98:101], v[94:97]
	s_waitcnt lgkmcnt(2)
	v_mfma_f32_16x16x32_bf16 v[58:61], v[86:89], v[102:105], v[58:61]
	s_waitcnt lgkmcnt(1)
	v_mfma_f32_16x16x32_bf16 v[54:57], v[86:89], v[106:109], v[54:57]
	s_waitcnt lgkmcnt(0)
	v_mfma_f32_16x16x32_bf16 v[46:49], v[86:89], v[110:113], v[46:49]
	v_sub_u32_e32 v86, s19, v132
	v_ashrrev_i32_e32 v87, 31, v86
	v_lshl_add_u64 v[86:87], v[86:87], 4, v[130:131]
	s_waitcnt vmcnt(6)
	v_mfma_f32_16x16x32_bf16 v[38:41], v[90:93], v[98:101], v[38:41]
	s_min_u32 s19, s5, 30
	s_add_i32 s19, s19, s81
	s_lshl_b32 s19, s19, 2
	v_mfma_f32_16x16x32_bf16 v[30:33], v[90:93], v[102:105], v[30:33]
	s_and_b32 s19, s19, 0x7c
	v_bitop3_b32 v98, s19, v230, v231 bitop3:0x36
	v_lshl_add_u32 v98, v98, 4, v232
	v_mfma_f32_16x16x32_bf16 v[22:25], v[90:93], v[106:109], v[22:25]
	v_add_u32_e32 v99, 0x10000, v98
	v_mfma_f32_16x16x32_bf16 v[14:17], v[90:93], v[110:113], v[14:17]
	v_add_co_u32_e32 v90, vcc, s40, v86
	s_nop 1
	v_addc_co_u32_e32 v91, vcc, 0, v87, vcc
	global_load_dwordx4 v[86:89], v[86:87], off
	s_nop 0
	global_load_dwordx4 v[90:93], v[90:91], off
	ds_read_b128 v[102:105], v98
	ds_read_b128 v[106:109], v98 offset:32768
	v_add_u32_e32 v98, 0x18000, v98
	ds_read_b128 v[110:113], v99
	ds_read_b128 v[98:101], v98
	s_add_i32 s5, s5, 4
	s_add_i32 s18, s18, 16
	s_and_b64 vcc, exec, s[16:17]
	s_cbranch_vccnz .LBB0_467
	s_waitcnt vmcnt(5)
	v_mul_f32_e32 v65, 0xbfb8aa3b, v50
	s_waitcnt vmcnt(4)
	v_exp_f32_e32 v66, v65
	v_mul_f32_e32 v65, 0xbfb8aa3b, v51
	v_exp_f32_e32 v67, v65
	s_lshl_b32 s5, s3, 5
	v_lshlrev_b32_e32 v236, 2, v231
	v_or_b32_e32 v63, s5, v236
	v_pk_add_f32 v[66:67], v[66:67], 1.0 op_sel_hi:[1,0]
	v_lshlrev_b32_e32 v62, 3, v231
	v_lshl_add_u32 v219, v230, 9, 0
	v_and_b32_e32 v218, 8, v62
	v_lshrrev_b32_e32 v63, 3, v63
	s_waitcnt vmcnt(3)
	v_rcp_f32_e32 v65, v67
	s_nop 0
	v_mul_f32_e32 v51, v51, v65
	v_add_u32_e32 v62, v219, v218
	v_xor_b32_e32 v64, v63, v230
	v_lshl_add_u32 v64, v64, 4, v62
	v_rcp_f32_e32 v65, v66
	s_nop 0
	v_mul_f32_e32 v50, v50, v65
	v_pk_mul_f32 v[50:51], v[50:51], v[94:95]
	s_waitcnt lgkmcnt(0)
	v_cvt_pk_bf16_f32 v50, v50, v51
	v_mul_f32_e32 v51, 0xbfb8aa3b, v52
	v_exp_f32_e32 v66, v51
	v_mul_f32_e32 v51, 0xbfb8aa3b, v53
	v_exp_f32_e32 v67, v51
	s_barrier
	v_pk_add_f32 v[66:67], v[66:67], 1.0 op_sel_hi:[1,0]
	s_nop 0
	s_nop 0
	v_rcp_f32_e32 v51, v67
	s_nop 0
	v_mul_f32_e32 v53, v53, v51
	s_nop 0
	v_rcp_f32_e32 v51, v66
	s_nop 0
	v_mul_f32_e32 v52, v52, v51
	v_pk_mul_f32 v[52:53], v[52:53], v[96:97]
	s_nop 0
	v_cvt_pk_bf16_f32 v51, v52, v53
	v_mul_f32_e32 v52, 0xbfb8aa3b, v42
	v_mul_f32_e32 v53, 0xbfb8aa3b, v43
	v_exp_f32_e32 v52, v52
	v_exp_f32_e32 v53, v53
	s_nop 0
	v_pk_add_f32 v[52:53], v[52:53], 1.0 op_sel_hi:[1,0]
	s_nop 0
	s_nop 0
	v_rcp_f32_e32 v65, v53
	s_nop 0
	v_mul_f32_e32 v43, v43, v65
	s_nop 0
	v_rcp_f32_e32 v53, v52
	s_nop 0
	v_mul_f32_e32 v42, v42, v53
	v_pk_mul_f32 v[42:43], v[42:43], v[58:59]
	s_nop 0
	v_cvt_pk_bf16_f32 v42, v42, v43
	v_mul_f32_e32 v43, 0xbfb8aa3b, v44
	v_exp_f32_e32 v52, v43
	v_mul_f32_e32 v43, 0xbfb8aa3b, v45
	v_exp_f32_e32 v53, v43
	s_nop 0
	v_pk_add_f32 v[52:53], v[52:53], 1.0 op_sel_hi:[1,0]
	s_nop 0
	s_nop 0
	v_rcp_f32_e32 v43, v53
	s_nop 0
	v_mul_f32_e32 v45, v45, v43
	s_nop 0
	v_rcp_f32_e32 v43, v52
	s_nop 0
	v_mul_f32_e32 v44, v44, v43
	v_pk_mul_f32 v[44:45], v[44:45], v[60:61]
	s_nop 0
	v_cvt_pk_bf16_f32 v43, v44, v45
	ds_write2st64_b64 v64, v[50:51], v[42:43] offset1:16
	v_mul_f32_e32 v42, 0xbfb8aa3b, v34
	v_mul_f32_e32 v43, 0xbfb8aa3b, v35
	v_exp_f32_e32 v42, v42
	v_exp_f32_e32 v43, v43
	s_nop 0
	v_pk_add_f32 v[42:43], v[42:43], 1.0 op_sel_hi:[1,0]
	s_nop 0
	s_nop 0
	v_rcp_f32_e32 v44, v43
	s_nop 0
	v_mul_f32_e32 v35, v35, v44
	s_nop 0
	v_rcp_f32_e32 v43, v42
	s_nop 0
	v_mul_f32_e32 v34, v34, v43
	v_pk_mul_f32 v[34:35], v[34:35], v[54:55]
	s_nop 0
	v_cvt_pk_bf16_f32 v34, v34, v35
	v_mul_f32_e32 v35, 0xbfb8aa3b, v36
	v_exp_f32_e32 v42, v35
	v_mul_f32_e32 v35, 0xbfb8aa3b, v37
	v_exp_f32_e32 v43, v35
	s_nop 0
	v_pk_add_f32 v[42:43], v[42:43], 1.0 op_sel_hi:[1,0]
	s_nop 0
	s_nop 0
	v_rcp_f32_e32 v35, v43
	s_nop 0
	v_mul_f32_e32 v37, v37, v35
	s_nop 0
	v_rcp_f32_e32 v35, v42
	s_nop 0
	v_mul_f32_e32 v36, v36, v35
	v_pk_mul_f32 v[36:37], v[36:37], v[56:57]
	s_nop 0
	v_cvt_pk_bf16_f32 v35, v36, v37
	v_mul_f32_e32 v36, 0xbfb8aa3b, v26
	v_mul_f32_e32 v37, 0xbfb8aa3b, v27
	v_exp_f32_e32 v36, v36
	v_exp_f32_e32 v37, v37
	s_nop 0
	v_pk_add_f32 v[36:37], v[36:37], 1.0 op_sel_hi:[1,0]
	s_nop 0
	s_nop 0
	v_rcp_f32_e32 v42, v37
	s_nop 0
	v_mul_f32_e32 v27, v27, v42
	s_nop 0
	v_rcp_f32_e32 v37, v36
	s_nop 0
	v_mul_f32_e32 v26, v26, v37
	v_pk_mul_f32 v[26:27], v[26:27], v[46:47]
	s_nop 0
	v_cvt_pk_bf16_f32 v26, v26, v27
	v_mul_f32_e32 v27, 0xbfb8aa3b, v28
	v_exp_f32_e32 v36, v27
	v_mul_f32_e32 v27, 0xbfb8aa3b, v29
	v_exp_f32_e32 v37, v27
	s_nop 0
	v_pk_add_f32 v[36:37], v[36:37], 1.0 op_sel_hi:[1,0]
	s_nop 0
	s_nop 0
	v_rcp_f32_e32 v27, v37
	s_nop 0
	v_mul_f32_e32 v29, v29, v27
	s_nop 0
	v_rcp_f32_e32 v27, v36
	s_nop 0
	v_mul_f32_e32 v28, v28, v27
	v_pk_mul_f32 v[28:29], v[28:29], v[48:49]
	s_nop 0
	v_cvt_pk_bf16_f32 v27, v28, v29
	ds_write2st64_b64 v64, v[34:35], v[26:27] offset0:32 offset1:48
	v_mul_f32_e32 v27, 0xbfb8aa3b, v18
	v_exp_f32_e32 v28, v27
	v_mul_f32_e32 v27, 0xbfb8aa3b, v19
	v_exp_f32_e32 v29, v27
	v_bitop3_b32 v26, v63, v230, 2 bitop3:0x36
	v_lshl_add_u32 v26, v26, 4, v62
	v_pk_add_f32 v[28:29], v[28:29], 1.0 op_sel_hi:[1,0]
	s_nop 0
	s_nop 0
	v_rcp_f32_e32 v27, v29
	s_nop 0
	v_mul_f32_e32 v19, v19, v27
	s_nop 0
	v_rcp_f32_e32 v27, v28
	s_nop 0
	v_mul_f32_e32 v18, v18, v27
	v_pk_mul_f32 v[18:19], v[18:19], v[38:39]
	s_nop 0
	v_cvt_pk_bf16_f32 v18, v18, v19
	v_mul_f32_e32 v19, 0xbfb8aa3b, v20
	v_exp_f32_e32 v28, v19
	v_mul_f32_e32 v19, 0xbfb8aa3b, v21
	v_exp_f32_e32 v29, v19
	s_nop 0
	v_pk_add_f32 v[28:29], v[28:29], 1.0 op_sel_hi:[1,0]
	s_nop 0
	s_nop 0
	v_rcp_f32_e32 v19, v29
	s_nop 0
	v_mul_f32_e32 v21, v21, v19
	s_nop 0
	v_rcp_f32_e32 v19, v28
	s_nop 0
	v_mul_f32_e32 v20, v20, v19
	v_pk_mul_f32 v[20:21], v[20:21], v[40:41]
	s_nop 0
	v_cvt_pk_bf16_f32 v19, v20, v21
	v_mul_f32_e32 v20, 0xbfb8aa3b, v10
	v_mul_f32_e32 v21, 0xbfb8aa3b, v11
	v_exp_f32_e32 v20, v20
	v_exp_f32_e32 v21, v21
	s_nop 0
	v_pk_add_f32 v[20:21], v[20:21], 1.0 op_sel_hi:[1,0]
	s_nop 0
	s_nop 0
	v_rcp_f32_e32 v27, v21
	s_nop 0
	v_mul_f32_e32 v11, v11, v27
	s_nop 0
	v_rcp_f32_e32 v21, v20
	s_nop 0
	v_mul_f32_e32 v10, v10, v21
	v_pk_mul_f32 v[10:11], v[10:11], v[30:31]
	s_nop 0
	v_cvt_pk_bf16_f32 v10, v10, v11
	v_mul_f32_e32 v11, 0xbfb8aa3b, v12
	v_exp_f32_e32 v20, v11
	v_mul_f32_e32 v11, 0xbfb8aa3b, v13
	v_exp_f32_e32 v21, v11
	s_nop 0
	v_pk_add_f32 v[20:21], v[20:21], 1.0 op_sel_hi:[1,0]
	s_nop 0
	s_nop 0
	v_rcp_f32_e32 v11, v21
	s_nop 0
	v_mul_f32_e32 v13, v13, v11
	s_nop 0
	v_rcp_f32_e32 v11, v20
	s_nop 0
	v_mul_f32_e32 v12, v12, v11
	v_pk_mul_f32 v[12:13], v[12:13], v[32:33]
	s_nop 0
	v_cvt_pk_bf16_f32 v11, v12, v13
	ds_write2st64_b64 v26, v[18:19], v[10:11] offset1:16
	v_mul_f32_e32 v10, 0xbfb8aa3b, v6
	v_mul_f32_e32 v11, 0xbfb8aa3b, v7
	v_exp_f32_e32 v10, v10
	v_exp_f32_e32 v11, v11
	s_nop 0
	v_pk_add_f32 v[10:11], v[10:11], 1.0 op_sel_hi:[1,0]
	s_nop 0
	s_nop 0
	v_rcp_f32_e32 v12, v11
	s_nop 0
	v_mul_f32_e32 v7, v7, v12
	s_nop 0
	v_rcp_f32_e32 v11, v10
	s_nop 0
	v_mul_f32_e32 v6, v6, v11
	v_pk_mul_f32 v[6:7], v[6:7], v[22:23]
	s_nop 0
	v_cvt_pk_bf16_f32 v6, v6, v7
	v_mul_f32_e32 v7, 0xbfb8aa3b, v8
	v_exp_f32_e32 v10, v7
	v_mul_f32_e32 v7, 0xbfb8aa3b, v9
	v_exp_f32_e32 v11, v7
	s_nop 0
	v_pk_add_f32 v[10:11], v[10:11], 1.0 op_sel_hi:[1,0]
	s_nop 0
	s_nop 0
	v_rcp_f32_e32 v7, v11
	s_nop 0
	v_mul_f32_e32 v9, v9, v7
	s_nop 0
	v_rcp_f32_e32 v7, v10
	s_nop 0
	v_mul_f32_e32 v8, v8, v7
	v_pk_mul_f32 v[8:9], v[8:9], v[24:25]
	s_nop 0
	v_cvt_pk_bf16_f32 v7, v8, v9
	v_mul_f32_e32 v8, 0xbfb8aa3b, v2
	v_mul_f32_e32 v9, 0xbfb8aa3b, v3
	v_exp_f32_e32 v8, v8
	v_exp_f32_e32 v9, v9
	s_nop 0
	v_pk_add_f32 v[8:9], v[8:9], 1.0 op_sel_hi:[1,0]
	s_nop 0
	s_nop 0
	v_rcp_f32_e32 v10, v9
	s_nop 0
	v_mul_f32_e32 v3, v3, v10
	s_nop 0
	v_rcp_f32_e32 v9, v8
	s_nop 0
	v_mul_f32_e32 v2, v2, v9
	v_pk_mul_f32 v[2:3], v[2:3], v[14:15]
	s_nop 0
	v_cvt_pk_bf16_f32 v2, v2, v3
	v_mul_f32_e32 v3, 0xbfb8aa3b, v4
	v_exp_f32_e32 v8, v3
	v_mul_f32_e32 v3, 0xbfb8aa3b, v5
	v_exp_f32_e32 v9, v3
	s_nop 0
	v_pk_add_f32 v[8:9], v[8:9], 1.0 op_sel_hi:[1,0]
	s_nop 0
	s_nop 0
	v_rcp_f32_e32 v3, v9
	s_nop 0
	v_mul_f32_e32 v5, v5, v3
	v_readlane_b32 s16, v254, 5
	v_readlane_b32 s17, v254, 6
	v_rcp_f32_e32 v3, v8
	s_nop 0
	v_mul_f32_e32 v4, v4, v3
	v_pk_mul_f32 v[4:5], v[4:5], v[16:17]
	s_andn2_b64 vcc, exec, s[16:17]
	v_cvt_pk_bf16_f32 v3, v4, v5
	ds_write2st64_b64 v26, v[6:7], v[2:3] offset0:32 offset1:48
	s_waitcnt lgkmcnt(0)
	s_barrier
	s_cbranch_vccnz .LBB0_489
	s_andn2_b64 vcc, exec, s[30:31]
	s_cbranch_vccnz .LBB0_486
	s_getreg_b32 s16, hwreg(HW_REG_XCC_ID, 0, 4)
	s_barrier
	s_mov_b64 s[16:17], exec
	v_readlane_b32 s18, v254, 1
	v_readlane_b32 s19, v254, 2
	s_and_b64 s[18:19], s[16:17], s[18:19]
	s_mov_b64 exec, s[18:19]
	s_cbranch_execz .LBB0_485
	v_readlane_b32 s18, v255, 11
	s_nop 1
	v_mov_b32_e32 v2, s18
	ds_read_b32 v2, v2
	global_load_dword v3, v211, s[88:89] sc1
	s_waitcnt vmcnt(0) lgkmcnt(0)
	v_sub_u32_e32 v3, v2, v3
	v_cmp_gt_i32_e32 vcc, 0, v3
	s_cbranch_vccnz .LBB0_484
	s_mov_b32 s23, 1
	s_branch .LBB0_474

.LBB0_891:
	s_nop 0
	v_readfirstlane_b32 s10, v162
	s_ashr_i32 s10, s10, 6
	s_mul_i32 s66, s66, s10
	s_waitcnt vmcnt(1)
	v_and_or_b32 v131, v162, 15, s64
	s_waitcnt vmcnt(0)
	v_lshrrev_b32_e32 v130, 2, v162
	s_lshl_b32 s48, s66, 4
	v_and_b32_e32 v130, 12, v130
	v_add_u32_e32 v132, s48, v131
	v_cmp_gt_i32_e32 vcc, s65, v132
	v_lshlrev_b32_e32 v162, 1, v130
	s_and_saveexec_b64 s[46:47], vcc
	s_cbranch_execz .LBB0_893
	v_ashrrev_i32_e32 v133, 31, v132
	v_lshl_add_u64 v[134:135], v[132:133], 2, s[26:27]
	global_load_dword v130, v[134:135], off
	v_mul_f32_e32 v134, 0xbfb8aa3b, v94
	v_mul_f32_e32 v135, 0xbfb8aa3b, v95
	v_exp_f32_e32 v134, v134
	v_exp_f32_e32 v135, v135
	v_mul_f32_e32 v136, 0xbfb8aa3b, v96
	v_mul_f32_e32 v137, 0xbfb8aa3b, v97
	v_exp_f32_e32 v136, v136
	v_exp_f32_e32 v137, v137
	v_pk_add_f32 v[134:135], v[134:135], 1.0 op_sel_hi:[1,0]
	v_mul_f32_e32 v138, 0xbfb8aa3b, v90
	v_pk_add_f32 v[136:137], v[136:137], 1.0 op_sel_hi:[1,0]
	v_mul_f32_e32 v139, 0xbfb8aa3b, v91
	v_exp_f32_e32 v138, v138
	v_exp_f32_e32 v139, v139
	v_rcp_f32_e32 v140, v135
	s_nop 0
	v_mul_f32_e32 v95, v95, v140
	v_rcp_f32_e32 v135, v134
	s_nop 0
	v_mul_f32_e32 v94, v94, v135
	v_pk_mul_f32 v[86:87], v[86:87], v[94:95]
	v_pk_add_f32 v[138:139], v[138:139], 1.0 op_sel_hi:[1,0]
	v_rcp_f32_e32 v134, v137
	s_nop 0
	v_mul_f32_e32 v95, v97, v134
	v_rcp_f32_e32 v94, v136
	s_nop 0
	v_mul_f32_e32 v94, v96, v94
	v_add_u32_e32 v132, s63, v132
	v_pk_mul_f32 v[88:89], v[88:89], v[94:95]
	v_ashrrev_i32_e32 v133, 31, v132
	v_lshlrev_b64 v[132:133], 9, v[132:133]
	v_lshl_add_u64 v[132:133], s[20:21], 0, v[132:133]
	s_waitcnt vmcnt(0)
	v_pk_mul_f32 v[86:87], v[86:87], v[130:131] op_sel_hi:[1,0]
	v_pk_mul_f32 v[88:89], v[88:89], v[130:131] op_sel_hi:[1,0]
	v_lshl_add_u64 v[132:133], v[132:133], 0, v[162:163]
	v_cvt_pk_bf16_f32 v86, v86, v87
	v_cvt_pk_bf16_f32 v87, v88, v89
	global_store_dwordx2 v[132:133], v[86:87], off
	v_rcp_f32_e32 v86, v139
	s_nop 0
	v_mul_f32_e32 v87, v91, v86
	v_mul_f32_e32 v88, 0xbfb8aa3b, v92
	v_mul_f32_e32 v89, 0xbfb8aa3b, v93
	v_exp_f32_e32 v88, v88
	v_exp_f32_e32 v89, v89
	v_rcp_f32_e32 v86, v138
	s_nop 0
	v_mul_f32_e32 v86, v90, v86
	v_pk_mul_f32 v[62:63], v[62:63], v[86:87]
	v_pk_add_f32 v[88:89], v[88:89], 1.0 op_sel_hi:[1,0]
	v_pk_mul_f32 v[62:63], v[62:63], v[130:131] op_sel_hi:[1,0]
	v_cvt_pk_bf16_f32 v62, v62, v63
	v_rcp_f32_e32 v63, v89
	s_nop 0
	v_mul_f32_e32 v87, v93, v63
	v_mul_f32_e32 v89, 0xbfb8aa3b, v70
	v_exp_f32_e32 v90, v89
	v_mul_f32_e32 v89, 0xbfb8aa3b, v71
	v_exp_f32_e32 v91, v89
	v_rcp_f32_e32 v63, v88
	s_nop 0
	v_mul_f32_e32 v86, v92, v63
	v_pk_mul_f32 v[64:65], v[64:65], v[86:87]
	v_pk_add_f32 v[86:87], v[90:91], 1.0 op_sel_hi:[1,0]
	v_pk_mul_f32 v[64:65], v[64:65], v[130:131] op_sel_hi:[1,0]
	v_cvt_pk_bf16_f32 v63, v64, v65
	global_store_dwordx2 v[132:133], v[62:63], off offset:32
	v_rcp_f32_e32 v62, v87
	s_nop 0
	v_mul_f32_e32 v63, v71, v62
	v_mul_f32_e32 v64, 0xbfb8aa3b, v72
	v_mul_f32_e32 v65, 0xbfb8aa3b, v73
	v_exp_f32_e32 v64, v64
	v_exp_f32_e32 v65, v65
	v_rcp_f32_e32 v62, v86
	s_nop 0
	v_mul_f32_e32 v62, v70, v62
	v_pk_mul_f32 v[30:31], v[30:31], v[62:63]
	v_pk_add_f32 v[64:65], v[64:65], 1.0 op_sel_hi:[1,0]
	v_pk_mul_f32 v[30:31], v[30:31], v[130:131] op_sel_hi:[1,0]
	v_cvt_pk_bf16_f32 v30, v30, v31
	v_rcp_f32_e32 v31, v65
	s_nop 0
	v_mul_f32_e32 v63, v73, v31
	v_mul_f32_e32 v65, 0xbfb8aa3b, v42
	v_exp_f32_e32 v70, v65
	v_mul_f32_e32 v65, 0xbfb8aa3b, v43
	v_exp_f32_e32 v71, v65
	v_rcp_f32_e32 v31, v64
	s_nop 0
	v_mul_f32_e32 v62, v72, v31
	v_pk_mul_f32 v[32:33], v[32:33], v[62:63]
	v_pk_add_f32 v[62:63], v[70:71], 1.0 op_sel_hi:[1,0]
	v_pk_mul_f32 v[32:33], v[32:33], v[130:131] op_sel_hi:[1,0]
	v_cvt_pk_bf16_f32 v31, v32, v33
	global_store_dwordx2 v[132:133], v[30:31], off offset:64
	v_rcp_f32_e32 v30, v63
	s_nop 0
	v_mul_f32_e32 v31, v43, v30
	v_mul_f32_e32 v32, 0xbfb8aa3b, v44
	v_mul_f32_e32 v33, 0xbfb8aa3b, v45
	v_exp_f32_e32 v32, v32
	v_exp_f32_e32 v33, v33
	v_rcp_f32_e32 v30, v62
	s_nop 0
	v_mul_f32_e32 v30, v42, v30
	v_pk_mul_f32 v[10:11], v[10:11], v[30:31]
	v_pk_add_f32 v[32:33], v[32:33], 1.0 op_sel_hi:[1,0]
	v_pk_mul_f32 v[10:11], v[10:11], v[130:131] op_sel_hi:[1,0]
	v_cvt_pk_bf16_f32 v10, v10, v11
	v_rcp_f32_e32 v11, v33
	s_nop 0
	v_mul_f32_e32 v31, v45, v11
	v_rcp_f32_e32 v11, v32
	s_nop 0
	v_mul_f32_e32 v30, v44, v11
	v_pk_mul_f32 v[12:13], v[12:13], v[30:31]
	s_nop 0
	v_pk_mul_f32 v[12:13], v[12:13], v[130:131] op_sel_hi:[1,0]
	s_nop 0
	v_cvt_pk_bf16_f32 v11, v12, v13
	global_store_dwordx2 v[132:133], v[10:11], off offset:96
.LBB0_893:
	s_or_b64 exec, exec, s[46:47]
	v_or_b32_e32 v10, 16, v131
	v_add_u32_e32 v12, s48, v10
	v_cmp_gt_i32_e32 vcc, s65, v12
	s_and_b64 s[10:11], s[44:45], vcc
	s_and_saveexec_b64 s[44:45], s[10:11]
	s_cbranch_execz .LBB0_895
	v_ashrrev_i32_e32 v13, 31, v12
	v_lshl_add_u64 v[10:11], v[12:13], 2, s[26:27]
	global_load_dword v10, v[10:11], off
	v_mul_f32_e32 v11, 0xbfb8aa3b, v74
	v_mul_f32_e32 v31, 0xbfb8aa3b, v75
	v_exp_f32_e32 v30, v11
	v_exp_f32_e32 v31, v31
	v_mul_f32_e32 v32, 0xbfb8aa3b, v76
	v_mul_f32_e32 v33, 0xbfb8aa3b, v77
	v_exp_f32_e32 v32, v32
	v_exp_f32_e32 v33, v33
	v_pk_add_f32 v[30:31], v[30:31], 1.0 op_sel_hi:[1,0]
	v_mul_f32_e32 v42, 0xbfb8aa3b, v46
	v_pk_add_f32 v[32:33], v[32:33], 1.0 op_sel_hi:[1,0]
	v_mul_f32_e32 v43, 0xbfb8aa3b, v47
	v_exp_f32_e32 v42, v42
	v_exp_f32_e32 v43, v43
	v_rcp_f32_e32 v11, v31
	s_nop 0
	v_mul_f32_e32 v31, v75, v11
	v_rcp_f32_e32 v11, v30
	s_nop 0
	v_mul_f32_e32 v30, v74, v11
	v_pk_add_f32 v[42:43], v[42:43], 1.0 op_sel_hi:[1,0]
	v_pk_mul_f32 v[30:31], v[54:55], v[30:31]
	v_rcp_f32_e32 v11, v33
	s_nop 0
	v_mul_f32_e32 v33, v77, v11
	v_add_u32_e32 v12, s63, v12
	v_rcp_f32_e32 v11, v32
	s_nop 0
	v_mul_f32_e32 v32, v76, v11
	v_ashrrev_i32_e32 v13, 31, v12
	v_lshlrev_b64 v[12:13], 9, v[12:13]
	v_pk_mul_f32 v[32:33], v[56:57], v[32:33]
	v_lshl_add_u64 v[12:13], s[20:21], 0, v[12:13]
	v_lshl_add_u64 v[12:13], v[12:13], 0, v[162:163]
	s_waitcnt vmcnt(0)
	v_pk_mul_f32 v[30:31], v[30:31], v[10:11] op_sel_hi:[1,0]
	v_pk_mul_f32 v[32:33], v[32:33], v[10:11] op_sel_hi:[1,0]
	v_cvt_pk_bf16_f32 v30, v30, v31
	v_cvt_pk_bf16_f32 v31, v32, v33
	global_store_dwordx2 v[12:13], v[30:31], off
	v_rcp_f32_e32 v11, v43
	s_nop 0
	v_mul_f32_e32 v31, v47, v11
	v_mul_f32_e32 v30, 0xbfb8aa3b, v48
	v_exp_f32_e32 v32, v30
	v_mul_f32_e32 v30, 0xbfb8aa3b, v49
	v_exp_f32_e32 v33, v30
	v_rcp_f32_e32 v11, v42
	s_nop 0
	v_mul_f32_e32 v30, v46, v11
	v_pk_mul_f32 v[30:31], v[34:35], v[30:31]
	v_pk_add_f32 v[32:33], v[32:33], 1.0 op_sel_hi:[1,0]
	s_nop 0
	v_pk_mul_f32 v[30:31], v[30:31], v[10:11] op_sel_hi:[1,0]
	s_nop 0
	v_cvt_pk_bf16_f32 v30, v30, v31
	v_rcp_f32_e32 v11, v33
	s_nop 0
	v_mul_f32_e32 v33, v49, v11
	v_mul_f32_e32 v31, 0xbfb8aa3b, v18
	v_exp_f32_e32 v34, v31
	v_mul_f32_e32 v31, 0xbfb8aa3b, v19
	v_exp_f32_e32 v35, v31
	v_rcp_f32_e32 v11, v32
	s_nop 0
	v_mul_f32_e32 v32, v48, v11
	v_pk_mul_f32 v[32:33], v[36:37], v[32:33]
	v_pk_add_f32 v[34:35], v[34:35], 1.0 op_sel_hi:[1,0]
	s_nop 0
	v_pk_mul_f32 v[32:33], v[32:33], v[10:11] op_sel_hi:[1,0]
	s_nop 0
	v_cvt_pk_bf16_f32 v31, v32, v33
	global_store_dwordx2 v[12:13], v[30:31], off offset:32
	v_rcp_f32_e32 v11, v35
	s_nop 0
	v_mul_f32_e32 v19, v19, v11
	v_mul_f32_e32 v30, 0xbfb8aa3b, v20
	v_mul_f32_e32 v31, 0xbfb8aa3b, v21
	v_exp_f32_e32 v30, v30
	v_exp_f32_e32 v31, v31
	v_rcp_f32_e32 v11, v34
	s_nop 0
	v_mul_f32_e32 v18, v18, v11
	v_pk_mul_f32 v[14:15], v[14:15], v[18:19]
	v_pk_add_f32 v[30:31], v[30:31], 1.0 op_sel_hi:[1,0]
	s_nop 0
	v_pk_mul_f32 v[14:15], v[14:15], v[10:11] op_sel_hi:[1,0]
	s_nop 0
	v_cvt_pk_bf16_f32 v14, v14, v15
	v_rcp_f32_e32 v11, v31
	s_nop 0
	v_mul_f32_e32 v19, v21, v11
	v_mul_f32_e32 v15, 0xbfb8aa3b, v6
	v_exp_f32_e32 v32, v15
	v_mul_f32_e32 v15, 0xbfb8aa3b, v7
	v_exp_f32_e32 v33, v15
	v_rcp_f32_e32 v11, v30
	s_nop 0
	v_mul_f32_e32 v18, v20, v11
	v_pk_mul_f32 v[16:17], v[16:17], v[18:19]
	v_pk_add_f32 v[18:19], v[32:33], 1.0 op_sel_hi:[1,0]
	s_nop 0
	v_pk_mul_f32 v[16:17], v[16:17], v[10:11] op_sel_hi:[1,0]
	s_nop 0
	v_cvt_pk_bf16_f32 v15, v16, v17
	global_store_dwordx2 v[12:13], v[14:15], off offset:64
	v_rcp_f32_e32 v11, v19
	s_nop 0
	v_mul_f32_e32 v7, v7, v11
	v_mul_f32_e32 v14, 0xbfb8aa3b, v8
	v_mul_f32_e32 v15, 0xbfb8aa3b, v9
	v_exp_f32_e32 v14, v14
	v_exp_f32_e32 v15, v15
	v_rcp_f32_e32 v11, v18
	s_nop 0
	v_mul_f32_e32 v6, v6, v11
	v_pk_mul_f32 v[2:3], v[2:3], v[6:7]
	v_pk_add_f32 v[14:15], v[14:15], 1.0 op_sel_hi:[1,0]
	s_nop 0
	v_pk_mul_f32 v[2:3], v[2:3], v[10:11] op_sel_hi:[1,0]
	s_nop 0
	v_cvt_pk_bf16_f32 v2, v2, v3
	v_rcp_f32_e32 v3, v15
	s_nop 0
	v_mul_f32_e32 v7, v9, v3
	v_rcp_f32_e32 v3, v14
	s_nop 0
	v_mul_f32_e32 v6, v8, v3
	v_pk_mul_f32 v[4:5], v[4:5], v[6:7]
	s_nop 0
	v_pk_mul_f32 v[4:5], v[4:5], v[10:11] op_sel_hi:[1,0]
	s_nop 0
	v_cvt_pk_bf16_f32 v3, v4, v5
	global_store_dwordx2 v[12:13], v[2:3], off offset:96
.LBB0_895:
	s_or_b64 exec, exec, s[44:45]
	v_or_b32_e32 v2, 32, v131
	v_add_u32_e32 v4, s48, v2
	v_cmp_gt_i32_e32 vcc, s65, v4
	s_and_b64 s[10:11], s[42:43], vcc
	s_and_saveexec_b64 s[42:43], s[10:11]
	s_cbranch_execz .LBB0_897
	v_ashrrev_i32_e32 v5, 31, v4
	v_lshl_add_u64 v[2:3], v[4:5], 2, s[26:27]
	global_load_dword v2, v[2:3], off
	v_mul_f32_e32 v3, 0xbfb8aa3b, v78
	v_mul_f32_e32 v7, 0xbfb8aa3b, v79
	v_exp_f32_e32 v6, v3
	v_exp_f32_e32 v7, v7
	v_mul_f32_e32 v8, 0xbfb8aa3b, v80
	v_mul_f32_e32 v9, 0xbfb8aa3b, v81
	v_exp_f32_e32 v8, v8
	v_exp_f32_e32 v9, v9
	v_pk_add_f32 v[6:7], v[6:7], 1.0 op_sel_hi:[1,0]
	v_mul_f32_e32 v10, 0xbfb8aa3b, v58
	v_pk_add_f32 v[8:9], v[8:9], 1.0 op_sel_hi:[1,0]
	v_mul_f32_e32 v11, 0xbfb8aa3b, v59
	v_exp_f32_e32 v10, v10
	v_exp_f32_e32 v11, v11
	v_rcp_f32_e32 v3, v7
	s_nop 0
	v_mul_f32_e32 v7, v79, v3
	v_rcp_f32_e32 v3, v6
	s_nop 0
	v_mul_f32_e32 v6, v78, v3
	v_pk_add_f32 v[10:11], v[10:11], 1.0 op_sel_hi:[1,0]
	v_pk_mul_f32 v[6:7], v[82:83], v[6:7]
	v_rcp_f32_e32 v3, v9
	s_nop 0
	v_mul_f32_e32 v9, v81, v3
	v_add_u32_e32 v4, s63, v4
	v_rcp_f32_e32 v3, v8
	s_nop 0
	v_mul_f32_e32 v8, v80, v3
	v_ashrrev_i32_e32 v5, 31, v4
	v_lshlrev_b64 v[4:5], 9, v[4:5]
	v_pk_mul_f32 v[8:9], v[84:85], v[8:9]
	v_lshl_add_u64 v[4:5], s[20:21], 0, v[4:5]
	v_lshl_add_u64 v[4:5], v[4:5], 0, v[162:163]
	s_waitcnt vmcnt(0)
	v_pk_mul_f32 v[6:7], v[6:7], v[2:3] op_sel_hi:[1,0]
	v_pk_mul_f32 v[8:9], v[8:9], v[2:3] op_sel_hi:[1,0]
	v_cvt_pk_bf16_f32 v6, v6, v7
	v_cvt_pk_bf16_f32 v7, v8, v9
	global_store_dwordx2 v[4:5], v[6:7], off
	v_rcp_f32_e32 v3, v11
	s_nop 0
	v_mul_f32_e32 v7, v59, v3
	v_mul_f32_e32 v6, 0xbfb8aa3b, v60
	v_exp_f32_e32 v8, v6
	v_mul_f32_e32 v6, 0xbfb8aa3b, v61
	v_exp_f32_e32 v9, v6
	v_rcp_f32_e32 v3, v10
	s_nop 0
	v_mul_f32_e32 v6, v58, v3
	v_pk_mul_f32 v[6:7], v[66:67], v[6:7]
	v_pk_add_f32 v[8:9], v[8:9], 1.0 op_sel_hi:[1,0]
	s_nop 0
	v_pk_mul_f32 v[6:7], v[6:7], v[2:3] op_sel_hi:[1,0]
	s_nop 0
	v_cvt_pk_bf16_f32 v6, v6, v7
	v_rcp_f32_e32 v3, v9
	s_nop 0
	v_mul_f32_e32 v9, v61, v3
	v_mul_f32_e32 v7, 0xbfb8aa3b, v38
	v_exp_f32_e32 v10, v7
	v_mul_f32_e32 v7, 0xbfb8aa3b, v39
	v_exp_f32_e32 v11, v7
	v_rcp_f32_e32 v3, v8
	s_nop 0
	v_mul_f32_e32 v8, v60, v3
	v_pk_mul_f32 v[8:9], v[68:69], v[8:9]
	v_pk_add_f32 v[10:11], v[10:11], 1.0 op_sel_hi:[1,0]
	s_nop 0
	v_pk_mul_f32 v[8:9], v[8:9], v[2:3] op_sel_hi:[1,0]
	s_nop 0
	v_cvt_pk_bf16_f32 v7, v8, v9
	global_store_dwordx2 v[4:5], v[6:7], off offset:32
	v_rcp_f32_e32 v3, v11
	s_nop 0
	v_mul_f32_e32 v7, v39, v3
	v_mul_f32_e32 v6, 0xbfb8aa3b, v40
	v_exp_f32_e32 v8, v6
	v_mul_f32_e32 v6, 0xbfb8aa3b, v41
	v_exp_f32_e32 v9, v6
	v_rcp_f32_e32 v3, v10
	s_nop 0
	v_mul_f32_e32 v6, v38, v3
	v_pk_mul_f32 v[6:7], v[50:51], v[6:7]
	v_pk_add_f32 v[8:9], v[8:9], 1.0 op_sel_hi:[1,0]
	s_nop 0
	v_pk_mul_f32 v[6:7], v[6:7], v[2:3] op_sel_hi:[1,0]
	s_nop 0
	v_cvt_pk_bf16_f32 v6, v6, v7
	v_rcp_f32_e32 v3, v9
	s_nop 0
	v_mul_f32_e32 v9, v41, v3
	v_mul_f32_e32 v7, 0xbfb8aa3b, v22
	v_exp_f32_e32 v10, v7
	v_mul_f32_e32 v7, 0xbfb8aa3b, v23
	v_exp_f32_e32 v11, v7
	v_rcp_f32_e32 v3, v8
	s_nop 0
	v_mul_f32_e32 v8, v40, v3
	v_pk_mul_f32 v[8:9], v[52:53], v[8:9]
	v_pk_add_f32 v[10:11], v[10:11], 1.0 op_sel_hi:[1,0]
	s_nop 0
	v_pk_mul_f32 v[8:9], v[8:9], v[2:3] op_sel_hi:[1,0]
	s_nop 0
	v_cvt_pk_bf16_f32 v7, v8, v9
	global_store_dwordx2 v[4:5], v[6:7], off offset:64
	v_rcp_f32_e32 v3, v11
	s_nop 0
	v_mul_f32_e32 v7, v23, v3
	v_mul_f32_e32 v6, 0xbfb8aa3b, v24
	v_exp_f32_e32 v8, v6
	v_mul_f32_e32 v6, 0xbfb8aa3b, v25
	v_exp_f32_e32 v9, v6
	v_rcp_f32_e32 v3, v10
	s_nop 0
	v_mul_f32_e32 v6, v22, v3
	v_pk_mul_f32 v[6:7], v[26:27], v[6:7]
	v_pk_add_f32 v[8:9], v[8:9], 1.0 op_sel_hi:[1,0]
	s_nop 0
	v_pk_mul_f32 v[6:7], v[6:7], v[2:3] op_sel_hi:[1,0]
	s_nop 0
	v_cvt_pk_bf16_f32 v6, v6, v7
	v_rcp_f32_e32 v3, v9
	s_nop 0
	v_mul_f32_e32 v9, v25, v3
	v_rcp_f32_e32 v3, v8
	s_nop 0
	v_mul_f32_e32 v8, v24, v3
	v_pk_mul_f32 v[8:9], v[28:29], v[8:9]
	s_nop 0
	v_pk_mul_f32 v[2:3], v[8:9], v[2:3] op_sel_hi:[1,0]
	s_nop 0
	v_cvt_pk_bf16_f32 v7, v2, v3
	global_store_dwordx2 v[4:5], v[6:7], off offset:96
.LBB0_897:
	s_or_b64 exec, exec, s[42:43]
	v_or_b32_e32 v2, 48, v131
	v_add_u32_e32 v4, s48, v2
	v_cmp_gt_i32_e32 vcc, s65, v4
	s_and_b64 s[10:11], s[40:41], vcc
	s_and_saveexec_b64 s[40:41], s[10:11]
	s_cbranch_execz .LBB0_868
	v_ashrrev_i32_e32 v5, 31, v4
	v_lshl_add_u64 v[2:3], v[4:5], 2, s[26:27]
	global_load_dword v2, v[2:3], off
	v_mul_f32_e32 v3, 0xbfb8aa3b, v122
	v_mul_f32_e32 v7, 0xbfb8aa3b, v123
	v_exp_f32_e32 v6, v3
	v_exp_f32_e32 v7, v7
	v_mul_f32_e32 v8, 0xbfb8aa3b, v124
	v_mul_f32_e32 v9, 0xbfb8aa3b, v125
	v_exp_f32_e32 v8, v8
	v_exp_f32_e32 v9, v9
	v_pk_add_f32 v[6:7], v[6:7], 1.0 op_sel_hi:[1,0]
	v_mul_f32_e32 v10, 0xbfb8aa3b, v114
	v_pk_add_f32 v[8:9], v[8:9], 1.0 op_sel_hi:[1,0]
	v_mul_f32_e32 v11, 0xbfb8aa3b, v115
	v_exp_f32_e32 v10, v10
	v_exp_f32_e32 v11, v11
	v_rcp_f32_e32 v3, v7
	s_nop 0
	v_mul_f32_e32 v7, v123, v3
	v_rcp_f32_e32 v3, v6
	s_nop 0
	v_mul_f32_e32 v6, v122, v3
	v_pk_add_f32 v[10:11], v[10:11], 1.0 op_sel_hi:[1,0]
	v_pk_mul_f32 v[6:7], v[126:127], v[6:7]
	v_rcp_f32_e32 v3, v9
	s_nop 0
	v_mul_f32_e32 v9, v125, v3
	v_add_u32_e32 v4, s63, v4
	v_rcp_f32_e32 v3, v8
	s_nop 0
	v_mul_f32_e32 v8, v124, v3
	v_ashrrev_i32_e32 v5, 31, v4
	v_lshlrev_b64 v[4:5], 9, v[4:5]
	v_pk_mul_f32 v[8:9], v[128:129], v[8:9]
	v_lshl_add_u64 v[4:5], s[20:21], 0, v[4:5]
	v_lshl_add_u64 v[4:5], v[4:5], 0, v[162:163]
	s_waitcnt vmcnt(0)
	v_pk_mul_f32 v[6:7], v[6:7], v[2:3] op_sel_hi:[1,0]
	v_pk_mul_f32 v[8:9], v[8:9], v[2:3] op_sel_hi:[1,0]
	v_cvt_pk_bf16_f32 v6, v6, v7
	v_cvt_pk_bf16_f32 v7, v8, v9
	global_store_dwordx2 v[4:5], v[6:7], off
	v_rcp_f32_e32 v3, v11
	s_nop 0
	v_mul_f32_e32 v7, v115, v3
	v_mul_f32_e32 v6, 0xbfb8aa3b, v116
	v_exp_f32_e32 v8, v6
	v_mul_f32_e32 v6, 0xbfb8aa3b, v117
	v_exp_f32_e32 v9, v6
	v_rcp_f32_e32 v3, v10
	s_nop 0
	v_mul_f32_e32 v6, v114, v3
	v_pk_mul_f32 v[6:7], v[118:119], v[6:7]
	v_pk_add_f32 v[8:9], v[8:9], 1.0 op_sel_hi:[1,0]
	s_nop 0
	v_pk_mul_f32 v[6:7], v[6:7], v[2:3] op_sel_hi:[1,0]
	s_nop 0
	v_cvt_pk_bf16_f32 v6, v6, v7
	v_rcp_f32_e32 v3, v9
	s_nop 0
	v_mul_f32_e32 v9, v117, v3
	v_mul_f32_e32 v7, 0xbfb8aa3b, v106
	v_exp_f32_e32 v10, v7
	v_mul_f32_e32 v7, 0xbfb8aa3b, v107
	v_exp_f32_e32 v11, v7
	v_rcp_f32_e32 v3, v8
	s_nop 0
	v_mul_f32_e32 v8, v116, v3
	v_pk_mul_f32 v[8:9], v[120:121], v[8:9]
	v_pk_add_f32 v[10:11], v[10:11], 1.0 op_sel_hi:[1,0]
	s_nop 0
	v_pk_mul_f32 v[8:9], v[8:9], v[2:3] op_sel_hi:[1,0]
	s_nop 0
	v_cvt_pk_bf16_f32 v7, v8, v9
	global_store_dwordx2 v[4:5], v[6:7], off offset:32
	v_rcp_f32_e32 v3, v11
	s_nop 0
	v_mul_f32_e32 v7, v107, v3
	v_mul_f32_e32 v6, 0xbfb8aa3b, v108
	v_exp_f32_e32 v8, v6
	v_mul_f32_e32 v6, 0xbfb8aa3b, v109
	v_exp_f32_e32 v9, v6
	v_rcp_f32_e32 v3, v10
	s_nop 0
	v_mul_f32_e32 v6, v106, v3
	v_pk_mul_f32 v[6:7], v[110:111], v[6:7]
	v_pk_add_f32 v[8:9], v[8:9], 1.0 op_sel_hi:[1,0]
	s_nop 0
	v_pk_mul_f32 v[6:7], v[6:7], v[2:3] op_sel_hi:[1,0]
	s_nop 0
	v_cvt_pk_bf16_f32 v6, v6, v7
	v_rcp_f32_e32 v3, v9
	s_nop 0
	v_mul_f32_e32 v9, v109, v3
	v_mul_f32_e32 v7, 0xbfb8aa3b, v102
	v_exp_f32_e32 v10, v7
	v_mul_f32_e32 v7, 0xbfb8aa3b, v103
	v_exp_f32_e32 v11, v7
	v_rcp_f32_e32 v3, v8
	s_nop 0
	v_mul_f32_e32 v8, v108, v3
	v_pk_mul_f32 v[8:9], v[112:113], v[8:9]
	v_pk_add_f32 v[10:11], v[10:11], 1.0 op_sel_hi:[1,0]
	s_nop 0
	v_pk_mul_f32 v[8:9], v[8:9], v[2:3] op_sel_hi:[1,0]
	s_nop 0
	v_cvt_pk_bf16_f32 v7, v8, v9
	global_store_dwordx2 v[4:5], v[6:7], off offset:64
	v_rcp_f32_e32 v3, v11
	s_nop 0
	v_mul_f32_e32 v7, v103, v3
	v_mul_f32_e32 v6, 0xbfb8aa3b, v104
	v_exp_f32_e32 v8, v6
	v_mul_f32_e32 v6, 0xbfb8aa3b, v105
	v_exp_f32_e32 v9, v6
	v_rcp_f32_e32 v3, v10
	s_nop 0
	v_mul_f32_e32 v6, v102, v3
	v_pk_mul_f32 v[6:7], v[98:99], v[6:7]
	v_pk_add_f32 v[8:9], v[8:9], 1.0 op_sel_hi:[1,0]
	s_nop 0
	v_pk_mul_f32 v[6:7], v[6:7], v[2:3] op_sel_hi:[1,0]
	s_nop 0
	v_cvt_pk_bf16_f32 v6, v6, v7
	v_rcp_f32_e32 v3, v9
	s_nop 0
	v_mul_f32_e32 v9, v105, v3
	v_rcp_f32_e32 v3, v8
	s_nop 0
	v_mul_f32_e32 v8, v104, v3
	v_pk_mul_f32 v[8:9], v[100:101], v[8:9]
	s_nop 0
	v_pk_mul_f32 v[2:3], v[8:9], v[2:3] op_sel_hi:[1,0]
	s_nop 0
	v_cvt_pk_bf16_f32 v7, v2, v3
	global_store_dwordx2 v[4:5], v[6:7], off offset:96
	s_branch .LBB0_868

.LBB0_1073:
	s_add_i32 s6, s35, -8
	s_add_i32 s37, s31, -3
	s_and_b32 s39, s6, 0x7c
	s_cmp_lt_u32 s37, 28
	s_cselect_b64 s[6:7], -1, 0
	s_min_u32 s37, s37, 27
	s_add_i32 s37, s37, s33
	s_lshl_b32 s37, s37, 6
	v_cndmask_b32_e64 v116, v212, 0, s[6:7]
	s_and_b32 s37, s37, 0x7c0
	s_waitcnt vmcnt(6) lgkmcnt(3)
	v_mfma_f32_16x16x32_bf16 v[46:49], v[62:65], v[98:101], v[46:49]
	s_waitcnt lgkmcnt(2)
	v_mfma_f32_16x16x32_bf16 v[42:45], v[62:65], v[102:105], v[42:45]
	s_waitcnt lgkmcnt(1)
	v_mfma_f32_16x16x32_bf16 v[34:37], v[62:65], v[110:113], v[34:37]
	s_waitcnt lgkmcnt(0)
	v_mfma_f32_16x16x32_bf16 v[26:29], v[62:65], v[106:109], v[26:29]
	v_sub_u32_e32 v62, s37, v116
	v_ashrrev_i32_e32 v63, 31, v62
	v_lshl_add_u64 v[62:63], v[62:63], 4, v[114:115]
	v_add_co_u32_e32 v64, vcc, s19, v62
	v_mfma_f32_16x16x32_bf16 v[94:97], v[66:69], v[98:101], v[94:97]
	s_nop 0
	v_addc_co_u32_e32 v65, vcc, 0, v63, vcc
	v_bitop3_b32 v98, s39, v217, v219 bitop3:0x36
	v_mfma_f32_16x16x32_bf16 v[58:61], v[66:69], v[102:105], v[58:61]
	v_mfma_f32_16x16x32_bf16 v[54:57], v[66:69], v[110:113], v[54:57]
	v_mfma_f32_16x16x32_bf16 v[50:53], v[66:69], v[106:109], v[50:53]
	global_load_dwordx4 v[66:69], v[62:63], off
	s_nop 0
	global_load_dwordx4 v[62:65], v[64:65], off
	v_lshl_add_u32 v106, v98, 4, v218
	v_add_u32_e32 v107, 0x10000, v106
	v_add_u32_e32 v110, 0x18000, v106
	ds_read_b128 v[98:101], v106
	ds_read_b128 v[102:105], v106 offset:32768
	ds_read_b128 v[106:109], v107
	ds_read_b128 v[110:113], v110
	s_add_i32 s37, s31, -2
	s_min_u32 s37, s37, 27
	s_add_i32 s37, s37, s33
	s_lshl_b32 s37, s37, 6
	s_and_b32 s37, s37, 0x7c0
	s_waitcnt vmcnt(7) lgkmcnt(3)
	v_mfma_f32_16x16x32_bf16 v[94:97], v[70:73], v[98:101], v[94:97]
	s_waitcnt lgkmcnt(2)
	v_mfma_f32_16x16x32_bf16 v[58:61], v[70:73], v[102:105], v[58:61]
	s_waitcnt lgkmcnt(1)
	v_mfma_f32_16x16x32_bf16 v[54:57], v[70:73], v[106:109], v[54:57]
	s_waitcnt lgkmcnt(0)
	v_mfma_f32_16x16x32_bf16 v[50:53], v[70:73], v[110:113], v[50:53]
	v_sub_u32_e32 v70, s37, v116
	v_ashrrev_i32_e32 v71, 31, v70
	v_lshl_add_u64 v[70:71], v[70:71], 4, v[114:115]
	s_waitcnt vmcnt(6)
	v_mfma_f32_16x16x32_bf16 v[46:49], v[74:77], v[98:101], v[46:49]
	s_add_i32 s37, s35, -4
	s_and_b32 s37, s37, 0x7c
	v_bitop3_b32 v98, s37, v217, v219 bitop3:0x36
	v_mfma_f32_16x16x32_bf16 v[42:45], v[74:77], v[102:105], v[42:45]
	v_mfma_f32_16x16x32_bf16 v[34:37], v[74:77], v[106:109], v[34:37]
	v_lshl_add_u32 v106, v98, 4, v218
	v_add_u32_e32 v107, 0x10000, v106
	v_mfma_f32_16x16x32_bf16 v[26:29], v[74:77], v[110:113], v[26:29]
	v_add_co_u32_e32 v74, vcc, s19, v70
	v_add_u32_e32 v110, 0x18000, v106
	s_nop 0
	v_addc_co_u32_e32 v75, vcc, 0, v71, vcc
	global_load_dwordx4 v[70:73], v[70:71], off
	s_nop 0
	global_load_dwordx4 v[74:77], v[74:75], off
	ds_read_b128 v[98:101], v106
	ds_read_b128 v[102:105], v106 offset:32768
	ds_read_b128 v[106:109], v107
	ds_read_b128 v[110:113], v110
	s_add_i32 s37, s31, -1
	s_min_u32 s37, s37, 27
	s_add_i32 s37, s37, s33
	s_lshl_b32 s37, s37, 6
	s_and_b32 s37, s37, 0x7c0
	s_waitcnt vmcnt(7) lgkmcnt(3)
	v_mfma_f32_16x16x32_bf16 v[94:97], v[78:81], v[98:101], v[94:97]
	s_waitcnt lgkmcnt(2)
	v_mfma_f32_16x16x32_bf16 v[58:61], v[78:81], v[102:105], v[58:61]
	s_waitcnt lgkmcnt(1)
	v_mfma_f32_16x16x32_bf16 v[54:57], v[78:81], v[106:109], v[54:57]
	s_waitcnt lgkmcnt(0)
	v_mfma_f32_16x16x32_bf16 v[50:53], v[78:81], v[110:113], v[50:53]
	v_sub_u32_e32 v78, s37, v116
	v_ashrrev_i32_e32 v79, 31, v78
	v_lshl_add_u64 v[78:79], v[78:79], 4, v[114:115]
	s_waitcnt vmcnt(6)
	v_mfma_f32_16x16x32_bf16 v[46:49], v[82:85], v[98:101], v[46:49]
	s_and_b32 s37, s35, 0x7c
	v_bitop3_b32 v98, s37, v217, v219 bitop3:0x36
	v_mfma_f32_16x16x32_bf16 v[42:45], v[82:85], v[102:105], v[42:45]
	v_mfma_f32_16x16x32_bf16 v[34:37], v[82:85], v[106:109], v[34:37]
	v_lshl_add_u32 v106, v98, 4, v218
	v_add_u32_e32 v107, 0x10000, v106
	v_mfma_f32_16x16x32_bf16 v[26:29], v[82:85], v[110:113], v[26:29]
	v_add_co_u32_e32 v82, vcc, s19, v78
	v_add_u32_e32 v110, 0x18000, v106
	s_nop 0
	v_addc_co_u32_e32 v83, vcc, 0, v79, vcc
	global_load_dwordx4 v[78:81], v[78:79], off
	s_nop 0
	global_load_dwordx4 v[82:85], v[82:83], off
	ds_read_b128 v[98:101], v106
	ds_read_b128 v[102:105], v106 offset:32768
	ds_read_b128 v[106:109], v107
	ds_read_b128 v[110:113], v110
	s_min_u32 s37, s31, 27
	s_add_i32 s37, s37, s33
	s_lshl_b32 s37, s37, 6
	s_and_b32 s37, s37, 0x7c0
	s_waitcnt vmcnt(6) lgkmcnt(3)
	v_mfma_f32_16x16x32_bf16 v[46:49], v[86:89], v[98:101], v[46:49]
	s_waitcnt lgkmcnt(2)
	v_mfma_f32_16x16x32_bf16 v[42:45], v[86:89], v[102:105], v[42:45]
	s_waitcnt lgkmcnt(1)
	v_mfma_f32_16x16x32_bf16 v[34:37], v[86:89], v[106:109], v[34:37]
	s_waitcnt lgkmcnt(0)
	v_mfma_f32_16x16x32_bf16 v[26:29], v[86:89], v[110:113], v[26:29]
	v_sub_u32_e32 v86, s37, v116
	v_ashrrev_i32_e32 v87, 31, v86
	v_lshl_add_u64 v[86:87], v[86:87], 4, v[114:115]
	v_add_co_u32_e32 v88, vcc, s19, v86
	v_mfma_f32_16x16x32_bf16 v[94:97], v[90:93], v[98:101], v[94:97]
	s_nop 0
	v_addc_co_u32_e32 v89, vcc, 0, v87, vcc
	s_min_u32 s37, s31, 30
	v_mfma_f32_16x16x32_bf16 v[58:61], v[90:93], v[102:105], v[58:61]
	s_add_i32 s37, s37, s27
	s_lshl_b32 s37, s37, 2
	s_and_b32 s37, s37, 0x7c
	v_mfma_f32_16x16x32_bf16 v[54:57], v[90:93], v[106:109], v[54:57]
	v_bitop3_b32 v98, s37, v217, v219 bitop3:0x36
	v_lshl_add_u32 v106, v98, 4, v218
	v_add_u32_e32 v107, 0x10000, v106
	v_mfma_f32_16x16x32_bf16 v[50:53], v[90:93], v[110:113], v[50:53]
	global_load_dwordx4 v[90:93], v[86:87], off
	s_nop 0
	global_load_dwordx4 v[86:89], v[88:89], off
	ds_read_b128 v[98:101], v106
	ds_read_b128 v[102:105], v106 offset:32768
	v_add_u32_e32 v106, 0x18000, v106
	ds_read_b128 v[110:113], v107
	ds_read_b128 v[106:109], v106
	s_add_i32 s31, s31, 4
	s_add_i32 s35, s35, 16
	s_and_b64 vcc, exec, s[6:7]
	s_cbranch_vccnz .LBB0_1073
	s_waitcnt vmcnt(6)
	v_mul_f32_e32 v62, 0xbfb8aa3b, v38
	v_mul_f32_e32 v63, 0xbfb8aa3b, v39
	v_exp_f32_e32 v62, v62
	v_exp_f32_e32 v63, v63
	v_lshlrev_b32_e32 v65, 3, v219
	v_and_b32_e32 v221, 8, v65
	v_lshlrev_b32_e32 v220, 2, v219
	v_pk_add_f32 v[62:63], v[62:63], 1.0 op_sel_hi:[1,0]
	v_lshl_or_b32 v64, s90, 5, v220
	v_lshl_add_u32 v222, v217, 9, 0
	v_lshrrev_b32_e32 v68, 3, v64
	v_add_u32_e32 v66, v222, v221
	v_xor_b32_e32 v64, v68, v217
	v_lshl_add_u32 v69, v64, 4, v66
	s_waitcnt vmcnt(5)
	v_rcp_f32_e32 v64, v63
	s_nop 0
	v_mul_f32_e32 v39, v39, v64
	v_mul_f32_e32 v64, 0xbfb8aa3b, v40
	v_mul_f32_e32 v65, 0xbfb8aa3b, v41
	v_exp_f32_e32 v64, v64
	v_exp_f32_e32 v65, v65
	v_rcp_f32_e32 v63, v62
	s_nop 0
	v_mul_f32_e32 v38, v38, v63
	v_pk_add_f32 v[64:65], v[64:65], 1.0 op_sel_hi:[1,0]
	v_pk_mul_f32 v[38:39], v[38:39], v[94:95]
	v_cvt_pk_bf16_f32 v38, v38, v39
	s_waitcnt lgkmcnt(0)
	v_rcp_f32_e32 v39, v65
	s_nop 0
	v_mul_f32_e32 v41, v41, v39
	v_mul_f32_e32 v63, 0xbfb8aa3b, v31
	v_mul_f32_e32 v62, 0xbfb8aa3b, v30
	v_exp_f32_e32 v62, v62
	v_exp_f32_e32 v63, v63
	v_rcp_f32_e32 v39, v64
	s_nop 0
	v_mul_f32_e32 v40, v40, v39
	v_pk_add_f32 v[62:63], v[62:63], 1.0 op_sel_hi:[1,0]
	v_pk_mul_f32 v[40:41], v[40:41], v[96:97]
	v_cvt_pk_bf16_f32 v39, v40, v41
	s_barrier
	v_fma_f32 v40, -v65, v67, 1.0
	v_fmac_f32_e32 v67, v40, v67
	v_rcp_f32_e32 v40, v63
	s_nop 0
	v_mul_f32_e32 v31, v31, v40
	v_mul_f32_e32 v40, 0xbfb8aa3b, v32
	v_mul_f32_e32 v41, 0xbfb8aa3b, v33
	v_exp_f32_e32 v40, v40
	v_exp_f32_e32 v41, v41
	v_rcp_f32_e32 v63, v62
	s_nop 0
	v_mul_f32_e32 v30, v30, v63
	v_pk_add_f32 v[40:41], v[40:41], 1.0 op_sel_hi:[1,0]
	v_pk_mul_f32 v[30:31], v[30:31], v[58:59]
	v_cvt_pk_bf16_f32 v30, v30, v31
	v_rcp_f32_e32 v31, v41
	s_nop 0
	v_mul_f32_e32 v33, v33, v31
	v_mul_f32_e32 v58, 0xbfb8aa3b, v22
	v_mul_f32_e32 v59, 0xbfb8aa3b, v23
	v_exp_f32_e32 v58, v58
	v_exp_f32_e32 v59, v59
	v_rcp_f32_e32 v31, v40
	s_nop 0
	v_mul_f32_e32 v32, v32, v31
	v_pk_mul_f32 v[32:33], v[32:33], v[60:61]
	v_pk_add_f32 v[40:41], v[58:59], 1.0 op_sel_hi:[1,0]
	v_cvt_pk_bf16_f32 v31, v32, v33
	ds_write2st64_b64 v69, v[38:39], v[30:31] offset1:16
	v_rcp_f32_e32 v30, v41
	s_nop 0
	v_mul_f32_e32 v23, v23, v30
	v_mul_f32_e32 v30, 0xbfb8aa3b, v24
	v_mul_f32_e32 v31, 0xbfb8aa3b, v25
	v_exp_f32_e32 v30, v30
	v_exp_f32_e32 v31, v31
	v_rcp_f32_e32 v32, v40
	s_nop 0
	v_mul_f32_e32 v22, v22, v32
	v_pk_add_f32 v[30:31], v[30:31], 1.0 op_sel_hi:[1,0]
	v_pk_mul_f32 v[22:23], v[22:23], v[54:55]
	v_cvt_pk_bf16_f32 v22, v22, v23
	v_rcp_f32_e32 v23, v31
	s_nop 0
	v_mul_f32_e32 v25, v25, v23
	v_mul_f32_e32 v32, 0xbfb8aa3b, v18
	v_mul_f32_e32 v33, 0xbfb8aa3b, v19
	v_exp_f32_e32 v32, v32
	v_exp_f32_e32 v33, v33
	v_rcp_f32_e32 v23, v30
	s_nop 0
	v_mul_f32_e32 v24, v24, v23
	v_pk_add_f32 v[32:33], v[32:33], 1.0 op_sel_hi:[1,0]
	v_pk_mul_f32 v[24:25], v[24:25], v[56:57]
	v_cvt_pk_bf16_f32 v23, v24, v25
	v_rcp_f32_e32 v24, v33
	s_nop 0
	v_mul_f32_e32 v19, v19, v24
	v_mul_f32_e32 v24, 0xbfb8aa3b, v20
	v_mul_f32_e32 v25, 0xbfb8aa3b, v21
	v_exp_f32_e32 v24, v24
	v_exp_f32_e32 v25, v25
	v_rcp_f32_e32 v30, v32
	s_nop 0
	v_mul_f32_e32 v18, v18, v30
	v_pk_add_f32 v[24:25], v[24:25], 1.0 op_sel_hi:[1,0]
	v_pk_mul_f32 v[18:19], v[18:19], v[50:51]
	v_cvt_pk_bf16_f32 v18, v18, v19
	v_rcp_f32_e32 v19, v25
	s_nop 0
	v_mul_f32_e32 v21, v21, v19
	v_mul_f32_e32 v25, 0xbfb8aa3b, v14
	v_exp_f32_e32 v30, v25
	v_mul_f32_e32 v25, 0xbfb8aa3b, v15
	v_exp_f32_e32 v31, v25
	v_rcp_f32_e32 v19, v24
	s_nop 0
	v_mul_f32_e32 v20, v20, v19
	v_pk_mul_f32 v[20:21], v[20:21], v[52:53]
	s_nop 0
	v_cvt_pk_bf16_f32 v19, v20, v21
	v_pk_add_f32 v[20:21], v[30:31], 1.0 op_sel_hi:[1,0]
	ds_write2st64_b64 v69, v[22:23], v[18:19] offset0:32 offset1:48
	v_bitop3_b32 v18, v68, v217, 2 bitop3:0x36
	v_lshl_add_u32 v22, v18, 4, v66
	v_rcp_f32_e32 v18, v21
	s_nop 0
	v_mul_f32_e32 v15, v15, v18
	v_mul_f32_e32 v18, 0xbfb8aa3b, v16
	v_mul_f32_e32 v19, 0xbfb8aa3b, v17
	v_exp_f32_e32 v18, v18
	v_exp_f32_e32 v19, v19
	v_rcp_f32_e32 v21, v20
	s_nop 0
	v_mul_f32_e32 v14, v14, v21
	v_pk_add_f32 v[18:19], v[18:19], 1.0 op_sel_hi:[1,0]
	v_pk_mul_f32 v[14:15], v[14:15], v[46:47]
	v_cvt_pk_bf16_f32 v14, v14, v15
	v_rcp_f32_e32 v15, v19
	s_nop 0
	v_mul_f32_e32 v17, v17, v15
	v_mul_f32_e32 v21, 0xbfb8aa3b, v11
	v_mul_f32_e32 v20, 0xbfb8aa3b, v10
	v_exp_f32_e32 v20, v20
	v_exp_f32_e32 v21, v21
	v_rcp_f32_e32 v15, v18
	s_nop 0
	v_mul_f32_e32 v16, v16, v15
	v_pk_add_f32 v[20:21], v[20:21], 1.0 op_sel_hi:[1,0]
	v_pk_mul_f32 v[16:17], v[16:17], v[48:49]
	v_cvt_pk_bf16_f32 v15, v16, v17
	v_rcp_f32_e32 v16, v21
	s_nop 0
	v_mul_f32_e32 v11, v11, v16
	v_mul_f32_e32 v16, 0xbfb8aa3b, v12
	v_mul_f32_e32 v17, 0xbfb8aa3b, v13
	v_exp_f32_e32 v16, v16
	v_exp_f32_e32 v17, v17
	v_rcp_f32_e32 v18, v20
	s_nop 0
	v_mul_f32_e32 v10, v10, v18
	v_pk_add_f32 v[16:17], v[16:17], 1.0 op_sel_hi:[1,0]
	v_pk_mul_f32 v[10:11], v[10:11], v[42:43]
	v_cvt_pk_bf16_f32 v10, v10, v11
	v_rcp_f32_e32 v11, v17
	s_nop 0
	v_mul_f32_e32 v13, v13, v11
	v_mul_f32_e32 v18, 0xbfb8aa3b, v6
	v_mul_f32_e32 v19, 0xbfb8aa3b, v7
	v_exp_f32_e32 v18, v18
	v_exp_f32_e32 v19, v19
	v_rcp_f32_e32 v11, v16
	s_nop 0
	v_mul_f32_e32 v12, v12, v11
	v_pk_mul_f32 v[12:13], v[12:13], v[44:45]
	v_pk_add_f32 v[16:17], v[18:19], 1.0 op_sel_hi:[1,0]
	v_cvt_pk_bf16_f32 v11, v12, v13
	ds_write2st64_b64 v22, v[14:15], v[10:11] offset1:16
	v_rcp_f32_e32 v10, v17
	s_nop 0
	v_mul_f32_e32 v7, v7, v10
	v_mul_f32_e32 v10, 0xbfb8aa3b, v8
	v_mul_f32_e32 v11, 0xbfb8aa3b, v9
	v_exp_f32_e32 v10, v10
	v_exp_f32_e32 v11, v11
	v_rcp_f32_e32 v12, v16
	s_nop 0
	v_mul_f32_e32 v6, v6, v12
	v_pk_add_f32 v[10:11], v[10:11], 1.0 op_sel_hi:[1,0]
	v_pk_mul_f32 v[6:7], v[6:7], v[34:35]
	v_cvt_pk_bf16_f32 v6, v6, v7
	v_rcp_f32_e32 v7, v11
	s_nop 0
	v_mul_f32_e32 v9, v9, v7
	v_mul_f32_e32 v12, 0xbfb8aa3b, v2
	v_mul_f32_e32 v13, 0xbfb8aa3b, v3
	v_exp_f32_e32 v12, v12
	v_exp_f32_e32 v13, v13
	v_rcp_f32_e32 v7, v10
	s_nop 0
	v_mul_f32_e32 v8, v8, v7
	v_pk_add_f32 v[12:13], v[12:13], 1.0 op_sel_hi:[1,0]
	v_pk_mul_f32 v[8:9], v[8:9], v[36:37]
	v_cvt_pk_bf16_f32 v7, v8, v9
	v_rcp_f32_e32 v8, v13
	s_nop 0
	v_mul_f32_e32 v3, v3, v8
	v_mul_f32_e32 v8, 0xbfb8aa3b, v4
	v_mul_f32_e32 v9, 0xbfb8aa3b, v5
	v_exp_f32_e32 v8, v8
	v_exp_f32_e32 v9, v9
	v_rcp_f32_e32 v10, v12
	s_nop 0
	v_mul_f32_e32 v2, v2, v10
	v_pk_add_f32 v[8:9], v[8:9], 1.0 op_sel_hi:[1,0]
	v_pk_mul_f32 v[2:3], v[2:3], v[26:27]
	v_cvt_pk_bf16_f32 v2, v2, v3
	v_rcp_f32_e32 v3, v9
	s_nop 0
	v_mul_f32_e32 v5, v5, v3
	v_readlane_b32 s6, v254, 5
	v_rcp_f32_e32 v3, v8
	s_nop 0
	v_mul_f32_e32 v4, v4, v3
	v_pk_mul_f32 v[4:5], v[4:5], v[28:29]
	v_readlane_b32 s7, v254, 6
	v_cvt_pk_bf16_f32 v3, v4, v5
	s_andn2_b64 vcc, exec, s[6:7]
	ds_write2st64_b64 v22, v[6:7], v[2:3] offset0:32 offset1:48
	s_waitcnt lgkmcnt(0)
	s_barrier
	s_cbranch_vccnz .LBB0_1095
	s_mov_b32 s45, s83
	s_mov_b32 s43, s82
	s_andn2_b64 vcc, exec, s[76:77]
	s_cbranch_vccnz .LBB0_1092
	s_getreg_b32 s6, hwreg(HW_REG_XCC_ID, 0, 4)
	s_barrier
	s_mov_b64 s[6:7], exec
	v_readlane_b32 s76, v254, 1
	v_readlane_b32 s77, v254, 2
	s_and_b64 s[76:77], s[6:7], s[76:77]
	s_mov_b64 exec, s[76:77]
	s_cbranch_execz .LBB0_1091
	v_readlane_b32 s31, v254, 21
	s_nop 1
	v_mov_b32_e32 v2, s31
	ds_read_b32 v2, v2
	global_load_dword v3, v211, s[16:17] sc1
	s_waitcnt vmcnt(0) lgkmcnt(0)
	v_sub_u32_e32 v3, v2, v3
	v_cmp_gt_i32_e32 vcc, 0, v3
	s_cbranch_vccnz .LBB0_1090
	s_mov_b32 s31, 1
	s_branch .LBB0_1080
